# 64-byte alignment (.p2align 6) of the 95 loop headers whose bodies contain MFMAs (GEMM main/unit loops, attention tile loops)
# baseline (speedup 1.0000x reference)
.LBB0_324:
	s_add_i32 m0, s31, 0x18000
	v_lshl_add_u64 v[0:1], v[0:1], 0, s[24:25]
	s_waitcnt vmcnt(2)
	s_barrier
	global_load_lds_dwordx4 v[0:1], off
	v_lshl_add_u64 v[0:1], v[4:5], 0, s[24:25]
	s_add_i32 m0, s31, 0x1a000
	s_add_i32 s78, s31, 0x8000
	global_load_lds_dwordx4 v[0:1], off
	v_lshl_add_u64 v[0:1], v[10:11], 0, s[24:25]
	s_mov_b32 m0, s78
	s_add_i32 s79, s31, 0xa000
	global_load_lds_dwordx4 v[0:1], off
	v_lshl_add_u64 v[0:1], v[12:13], 0, s[24:25]
	s_mov_b32 m0, s79
	v_bfe_u32 v156, v2, 4, 2
	global_load_lds_dwordx4 v[0:1], off
	s_add_i32 m0, s31, 0x1c000
	v_lshl_add_u64 v[0:1], v[6:7], 0, s[24:25]
	global_load_lds_dwordx4 v[0:1], off
	v_lshl_add_u64 v[0:1], v[8:9], 0, s[24:25]
	s_add_i32 m0, s31, 0x1e000
	s_lshr_b32 s1, s1, 26
	global_load_lds_dwordx4 v[0:1], off
	v_and_b32_e32 v155, 15, v2
	s_add_i32 s1, s0, s1
	v_lshlrev_b32_e32 v0, 4, v156
	v_lshlrev_b32_e32 v1, 2, v2
	s_and_b32 s8, s7, 3
	s_ashr_i32 s85, s1, 6
	v_lshl_or_b32 v0, v155, 6, v0
	s_lshl_b32 s1, s12, 13
	v_and_b32_e32 v1, 32, v1
	v_bitop3_b32 v4, v0, s1, v1 bitop3:0xde
	s_lshl_b32 s1, s8, 12
	v_bitop3_b32 v157, v0, s1, v1 bitop3:0xde
	v_and_b32_e32 v159, 3, v2
	v_and_b32_e32 v0, 60, v2
	v_lshl_or_b32 v160, v159, 6, v0
	v_lshlrev_b32_e32 v0, 4, v155
	v_bfe_u32 v158, v2, 2, 4
	v_lshl_or_b32 v2, v156, 8, v0
	v_lshlrev_b32_e32 v0, 14, v14
	v_and_b32_e32 v0, 0xffff8000, v0
	v_lshl_add_u32 v0, v15, 11, v0
	v_and_b32_e32 v1, 1, v14
	s_lshl_b32 s92, s12, 6
	s_lshl_b32 s93, s8, 5
	v_lshl_or_b32 v0, v1, 6, v0
	s_cmp_gt_i32 s0, 63
	v_lshl_add_u32 v150, v16, 1, v0
	v_lshlrev_b32_e32 v0, 14, v17
	s_cselect_b64 s[66:67], -1, 0
	s_add_i32 s94, s85, -2
	v_and_b32_e32 v0, 0xffff8000, v0
	s_waitcnt vmcnt(6)
	s_cmpk_lt_u32 s6, 0x100
	v_lshl_add_u32 v0, v18, 11, v0
	v_and_b32_e32 v1, 1, v17
	s_cselect_b64 s[68:69], -1, 0
	s_or_b32 s59, s93, 0x80
	v_writelane_b32 v255, s52, 1
	v_lshl_or_b32 v0, v1, 6, v0
	s_or_b32 s95, s8, 0xffffff78
	s_mulk_i32 s12, 0x180
	s_bfe_u32 s58, s7, 0x10001
	s_lshr_b32 s44, s59, 6
	v_writelane_b32 v255, s53, 2
	v_lshl_add_u64 v[148:149], s[52:53], 0, v[2:3]
	v_mov_b32_e32 v151, v3
	v_lshl_add_u32 v152, v19, 1, v0
	v_mov_b32_e32 v153, v3
	s_mov_b32 s45, 0
	v_add_u32_e32 v161, 0, v4
	s_barrier
	s_branch .LBB0_327
	.p2align	6
.LBB0_325:
	s_mov_b64 s[0:1], 0
	.p2align	6

.LBB0_332:
	s_ashr_i32 s87, s86, 31
	s_lshl_b64 s[6:7], s[86:87], 19
	s_add_u32 s52, s15, s6
	s_addc_u32 s53, s20, s7
	s_andn2_b64 vcc, exec, s[66:67]
	s_cbranch_vccnz .LBB0_373
	s_and_b64 s[0:1], s[0:1], exec
	s_cselect_b32 s6, s53, s5
	s_cselect_b32 s7, s52, s4
	s_add_u32 s0, s4, 0x40080
	s_addc_u32 s1, s5, 0
	s_add_u32 s4, s2, 0x100
	v_mov_b32_e32 v4, 0
	s_addc_u32 s5, s3, 0
	s_mov_b32 s2, 0
	v_mov_b32_e32 v5, v4
	v_mov_b32_e32 v6, v4
	v_mov_b32_e32 v7, v4
	v_mov_b32_e32 v8, v4
	v_mov_b32_e32 v9, v4
	v_mov_b32_e32 v10, v4
	v_mov_b32_e32 v11, v4
	v_mov_b32_e32 v20, v4
	v_mov_b32_e32 v21, v4
	v_mov_b32_e32 v22, v4
	v_mov_b32_e32 v23, v4
	v_mov_b32_e32 v24, v4
	v_mov_b32_e32 v25, v4
	v_mov_b32_e32 v26, v4
	v_mov_b32_e32 v27, v4
	v_mov_b32_e32 v36, v4
	v_mov_b32_e32 v37, v4
	v_mov_b32_e32 v38, v4
	v_mov_b32_e32 v39, v4
	v_mov_b32_e32 v40, v4
	v_mov_b32_e32 v41, v4
	v_mov_b32_e32 v42, v4
	v_mov_b32_e32 v43, v4
	v_mov_b32_e32 v52, v4
	v_mov_b32_e32 v53, v4
	v_mov_b32_e32 v54, v4
	v_mov_b32_e32 v55, v4
	v_mov_b32_e32 v56, v4
	v_mov_b32_e32 v57, v4
	v_mov_b32_e32 v58, v4
	v_mov_b32_e32 v59, v4
	v_mov_b32_e32 v12, v4
	v_mov_b32_e32 v13, v4
	v_mov_b32_e32 v14, v4
	v_mov_b32_e32 v15, v4
	v_mov_b32_e32 v16, v4
	v_mov_b32_e32 v17, v4
	v_mov_b32_e32 v18, v4
	v_mov_b32_e32 v19, v4
	v_mov_b32_e32 v28, v4
	v_mov_b32_e32 v29, v4
	v_mov_b32_e32 v30, v4
	v_mov_b32_e32 v31, v4
	v_mov_b32_e32 v32, v4
	v_mov_b32_e32 v33, v4
	v_mov_b32_e32 v34, v4
	v_mov_b32_e32 v35, v4
	v_mov_b32_e32 v44, v4
	v_mov_b32_e32 v45, v4
	v_mov_b32_e32 v46, v4
	v_mov_b32_e32 v47, v4
	v_mov_b32_e32 v48, v4
	v_mov_b32_e32 v49, v4
	v_mov_b32_e32 v50, v4
	v_mov_b32_e32 v51, v4
	v_mov_b32_e32 v60, v4
	v_mov_b32_e32 v61, v4
	v_mov_b32_e32 v62, v4
	v_mov_b32_e32 v63, v4
	v_mov_b32_e32 v64, v4
	v_mov_b32_e32 v65, v4
	v_mov_b32_e32 v66, v4
	v_mov_b32_e32 v67, v4
	v_mov_b32_e32 v68, v4
	v_mov_b32_e32 v69, v4
	v_mov_b32_e32 v70, v4
	v_mov_b32_e32 v71, v4
	v_mov_b32_e32 v72, v4
	v_mov_b32_e32 v73, v4
	v_mov_b32_e32 v74, v4
	v_mov_b32_e32 v75, v4
	v_mov_b32_e32 v84, v4
	v_mov_b32_e32 v85, v4
	v_mov_b32_e32 v86, v4
	v_mov_b32_e32 v87, v4
	v_mov_b32_e32 v88, v4
	v_mov_b32_e32 v89, v4
	v_mov_b32_e32 v90, v4
	v_mov_b32_e32 v91, v4
	v_mov_b32_e32 v100, v4
	v_mov_b32_e32 v101, v4
	v_mov_b32_e32 v102, v4
	v_mov_b32_e32 v103, v4
	v_mov_b32_e32 v104, v4
	v_mov_b32_e32 v105, v4
	v_mov_b32_e32 v106, v4
	v_mov_b32_e32 v107, v4
	v_mov_b32_e32 v116, v4
	v_mov_b32_e32 v117, v4
	v_mov_b32_e32 v118, v4
	v_mov_b32_e32 v119, v4
	v_mov_b32_e32 v120, v4
	v_mov_b32_e32 v121, v4
	v_mov_b32_e32 v122, v4
	v_mov_b32_e32 v123, v4
	v_mov_b32_e32 v76, v4
	v_mov_b32_e32 v77, v4
	v_mov_b32_e32 v78, v4
	v_mov_b32_e32 v79, v4
	v_mov_b32_e32 v80, v4
	v_mov_b32_e32 v81, v4
	v_mov_b32_e32 v82, v4
	v_mov_b32_e32 v83, v4
	v_mov_b32_e32 v92, v4
	v_mov_b32_e32 v93, v4
	v_mov_b32_e32 v94, v4
	v_mov_b32_e32 v95, v4
	v_mov_b32_e32 v96, v4
	v_mov_b32_e32 v97, v4
	v_mov_b32_e32 v98, v4
	v_mov_b32_e32 v99, v4
	v_mov_b32_e32 v108, v4
	v_mov_b32_e32 v109, v4
	v_mov_b32_e32 v110, v4
	v_mov_b32_e32 v111, v4
	v_mov_b32_e32 v112, v4
	v_mov_b32_e32 v113, v4
	v_mov_b32_e32 v114, v4
	v_mov_b32_e32 v115, v4
	v_mov_b32_e32 v124, v4
	v_mov_b32_e32 v125, v4
	v_mov_b32_e32 v126, v4
	v_mov_b32_e32 v127, v4
	v_mov_b32_e32 v128, v4
	v_mov_b32_e32 v129, v4
	v_mov_b32_e32 v130, v4
	v_mov_b32_e32 v131, v4
	.p2align	6

.LBB0_824:
	s_add_i32 m0, s9, 0x18000
	v_lshl_add_u64 v[0:1], v[0:1], 0, s[24:25]
	s_waitcnt vmcnt(2)
	s_barrier
	global_load_lds_dwordx4 v[0:1], off
	v_lshl_add_u64 v[0:1], v[4:5], 0, s[24:25]
	s_add_i32 m0, s9, 0x1a000
	s_add_i32 s70, s9, 0x8000
	global_load_lds_dwordx4 v[0:1], off
	v_lshl_add_u64 v[0:1], v[10:11], 0, s[24:25]
	s_mov_b32 m0, s70
	s_add_i32 s71, s9, 0xa000
	global_load_lds_dwordx4 v[0:1], off
	v_lshl_add_u64 v[0:1], v[12:13], 0, s[24:25]
	s_mov_b32 m0, s71
	v_bfe_u32 v155, v2, 4, 2
	global_load_lds_dwordx4 v[0:1], off
	s_add_i32 m0, s9, 0x1c000
	v_lshl_add_u64 v[0:1], v[6:7], 0, s[24:25]
	global_load_lds_dwordx4 v[0:1], off
	v_lshl_add_u64 v[0:1], v[8:9], 0, s[24:25]
	s_add_i32 m0, s9, 0x1e000
	s_lshr_b32 s1, s1, 26
	global_load_lds_dwordx4 v[0:1], off
	v_and_b32_e32 v154, 15, v2
	s_add_i32 s1, s0, s1
	v_lshlrev_b32_e32 v0, 4, v155
	v_lshlrev_b32_e32 v1, 2, v2
	s_and_b32 s12, s7, 3
	s_ashr_i32 s78, s1, 6
	v_lshl_or_b32 v0, v154, 6, v0
	s_lshl_b32 s1, s85, 13
	v_and_b32_e32 v1, 32, v1
	v_bitop3_b32 v4, v0, s1, v1 bitop3:0xde
	s_lshl_b32 s1, s12, 12
	v_bitop3_b32 v156, v0, s1, v1 bitop3:0xde
	v_and_b32_e32 v158, 3, v2
	v_and_b32_e32 v0, 60, v2
	v_lshl_or_b32 v159, v158, 6, v0
	v_lshlrev_b32_e32 v0, 4, v154
	v_bfe_u32 v157, v2, 2, 4
	v_lshl_or_b32 v2, v155, 8, v0
	v_lshlrev_b32_e32 v0, 14, v14
	v_and_b32_e32 v0, 0xffff8000, v0
	v_lshl_add_u32 v0, v15, 11, v0
	v_and_b32_e32 v1, 1, v14
	s_lshl_b32 s79, s85, 6
	s_lshl_b32 s82, s12, 5
	v_lshl_or_b32 v0, v1, 6, v0
	s_cmp_gt_i32 s0, 63
	v_lshl_add_u32 v150, v16, 1, v0
	v_lshlrev_b32_e32 v0, 14, v17
	s_cselect_b64 s[66:67], -1, 0
	s_add_i32 s83, s78, -2
	v_and_b32_e32 v0, 0xffff8000, v0
	s_waitcnt vmcnt(6)
	s_cmpk_lt_u32 s6, 0x100
	v_lshl_add_u32 v0, v18, 11, v0
	v_and_b32_e32 v1, 1, v17
	s_cselect_b64 s[68:69], -1, 0
	s_or_b32 s44, s82, 0x80
	v_lshl_or_b32 v0, v1, 6, v0
	s_or_b32 s12, s12, 0xffffff78
	s_mulk_i32 s85, 0x180
	s_bfe_u32 s92, s7, 0x10001
	s_lshr_b32 s45, s44, 6
	v_lshl_add_u64 v[148:149], s[52:53], 0, v[2:3]
	v_mov_b32_e32 v151, v3
	v_lshl_add_u32 v152, v19, 1, v0
	v_mov_b32_e32 v153, v3
	s_mov_b32 s93, 0
	v_add_u32_e32 v160, 0, v4
	s_barrier
	s_branch .LBB0_827
	.p2align	6

.LBB0_832:
	s_ashr_i32 s59, s58, 31
	s_lshl_b64 s[6:7], s[58:59], 19
	s_add_u32 s72, s15, s6
	s_addc_u32 s73, s20, s7
	s_andn2_b64 vcc, exec, s[66:67]
	s_cbranch_vccnz .LBB0_873
	s_and_b64 s[0:1], s[0:1], exec
	s_cselect_b32 s6, s73, s5
	s_cselect_b32 s7, s72, s4
	s_add_u32 s0, s4, 0x40080
	s_addc_u32 s1, s5, 0
	s_add_u32 s4, s2, 0x100
	v_mov_b32_e32 v4, 0
	s_addc_u32 s5, s3, 0
	s_mov_b32 s2, 0
	v_mov_b32_e32 v5, v4
	v_mov_b32_e32 v6, v4
	v_mov_b32_e32 v7, v4
	v_mov_b32_e32 v8, v4
	v_mov_b32_e32 v9, v4
	v_mov_b32_e32 v10, v4
	v_mov_b32_e32 v11, v4
	v_mov_b32_e32 v20, v4
	v_mov_b32_e32 v21, v4
	v_mov_b32_e32 v22, v4
	v_mov_b32_e32 v23, v4
	v_mov_b32_e32 v24, v4
	v_mov_b32_e32 v25, v4
	v_mov_b32_e32 v26, v4
	v_mov_b32_e32 v27, v4
	v_mov_b32_e32 v36, v4
	v_mov_b32_e32 v37, v4
	v_mov_b32_e32 v38, v4
	v_mov_b32_e32 v39, v4
	v_mov_b32_e32 v40, v4
	v_mov_b32_e32 v41, v4
	v_mov_b32_e32 v42, v4
	v_mov_b32_e32 v43, v4
	v_mov_b32_e32 v52, v4
	v_mov_b32_e32 v53, v4
	v_mov_b32_e32 v54, v4
	v_mov_b32_e32 v55, v4
	v_mov_b32_e32 v56, v4
	v_mov_b32_e32 v57, v4
	v_mov_b32_e32 v58, v4
	v_mov_b32_e32 v59, v4
	v_mov_b32_e32 v12, v4
	v_mov_b32_e32 v13, v4
	v_mov_b32_e32 v14, v4
	v_mov_b32_e32 v15, v4
	v_mov_b32_e32 v16, v4
	v_mov_b32_e32 v17, v4
	v_mov_b32_e32 v18, v4
	v_mov_b32_e32 v19, v4
	v_mov_b32_e32 v28, v4
	v_mov_b32_e32 v29, v4
	v_mov_b32_e32 v30, v4
	v_mov_b32_e32 v31, v4
	v_mov_b32_e32 v32, v4
	v_mov_b32_e32 v33, v4
	v_mov_b32_e32 v34, v4
	v_mov_b32_e32 v35, v4
	v_mov_b32_e32 v44, v4
	v_mov_b32_e32 v45, v4
	v_mov_b32_e32 v46, v4
	v_mov_b32_e32 v47, v4
	v_mov_b32_e32 v48, v4
	v_mov_b32_e32 v49, v4
	v_mov_b32_e32 v50, v4
	v_mov_b32_e32 v51, v4
	v_mov_b32_e32 v60, v4
	v_mov_b32_e32 v61, v4
	v_mov_b32_e32 v62, v4
	v_mov_b32_e32 v63, v4
	v_mov_b32_e32 v64, v4
	v_mov_b32_e32 v65, v4
	v_mov_b32_e32 v66, v4
	v_mov_b32_e32 v67, v4
	v_mov_b32_e32 v68, v4
	v_mov_b32_e32 v69, v4
	v_mov_b32_e32 v70, v4
	v_mov_b32_e32 v71, v4
	v_mov_b32_e32 v72, v4
	v_mov_b32_e32 v73, v4
	v_mov_b32_e32 v74, v4
	v_mov_b32_e32 v75, v4
	v_mov_b32_e32 v84, v4
	v_mov_b32_e32 v85, v4
	v_mov_b32_e32 v86, v4
	v_mov_b32_e32 v87, v4
	v_mov_b32_e32 v88, v4
	v_mov_b32_e32 v89, v4
	v_mov_b32_e32 v90, v4
	v_mov_b32_e32 v91, v4
	v_mov_b32_e32 v100, v4
	v_mov_b32_e32 v101, v4
	v_mov_b32_e32 v102, v4
	v_mov_b32_e32 v103, v4
	v_mov_b32_e32 v104, v4
	v_mov_b32_e32 v105, v4
	v_mov_b32_e32 v106, v4
	v_mov_b32_e32 v107, v4
	v_mov_b32_e32 v116, v4
	v_mov_b32_e32 v117, v4
	v_mov_b32_e32 v118, v4
	v_mov_b32_e32 v119, v4
	v_mov_b32_e32 v120, v4
	v_mov_b32_e32 v121, v4
	v_mov_b32_e32 v122, v4
	v_mov_b32_e32 v123, v4
	v_mov_b32_e32 v76, v4
	v_mov_b32_e32 v77, v4
	v_mov_b32_e32 v78, v4
	v_mov_b32_e32 v79, v4
	v_mov_b32_e32 v80, v4
	v_mov_b32_e32 v81, v4
	v_mov_b32_e32 v82, v4
	v_mov_b32_e32 v83, v4
	v_mov_b32_e32 v92, v4
	v_mov_b32_e32 v93, v4
	v_mov_b32_e32 v94, v4
	v_mov_b32_e32 v95, v4
	v_mov_b32_e32 v96, v4
	v_mov_b32_e32 v97, v4
	v_mov_b32_e32 v98, v4
	v_mov_b32_e32 v99, v4
	v_mov_b32_e32 v108, v4
	v_mov_b32_e32 v109, v4
	v_mov_b32_e32 v110, v4
	v_mov_b32_e32 v111, v4
	v_mov_b32_e32 v112, v4
	v_mov_b32_e32 v113, v4
	v_mov_b32_e32 v114, v4
	v_mov_b32_e32 v115, v4
	v_mov_b32_e32 v124, v4
	v_mov_b32_e32 v125, v4
	v_mov_b32_e32 v126, v4
	v_mov_b32_e32 v127, v4
	v_mov_b32_e32 v128, v4
	v_mov_b32_e32 v129, v4
	v_mov_b32_e32 v130, v4
	v_mov_b32_e32 v131, v4
	.p2align	6

.LBB0_1174:
	s_add_i32 m0, s41, 0x18000
	v_lshl_add_u64 v[4:5], v[4:5], 0, s[24:25]
	s_waitcnt vmcnt(2)
	s_barrier
	global_load_lds_dwordx4 v[4:5], off
	v_lshl_add_u64 v[4:5], v[6:7], 0, s[24:25]
	s_add_i32 m0, s41, 0x1a000
	s_add_i32 s6, s41, 0x8000
	global_load_lds_dwordx4 v[4:5], off
	v_lshl_add_u64 v[4:5], v[12:13], 0, s[24:25]
	s_mov_b32 m0, s6
	s_add_i32 s7, s41, 0xa000
	global_load_lds_dwordx4 v[4:5], off
	v_lshl_add_u64 v[4:5], v[14:15], 0, s[24:25]
	s_mov_b32 m0, s7
	s_lshl_b32 s14, s57, 13
	global_load_lds_dwordx4 v[4:5], off
	s_add_i32 m0, s41, 0x1c000
	v_lshl_add_u64 v[4:5], v[8:9], 0, s[24:25]
	global_load_lds_dwordx4 v[4:5], off
	v_lshl_add_u64 v[4:5], v[10:11], 0, s[24:25]
	s_add_i32 m0, s41, 0x1e000
	s_mov_b64 s[60:61], 0x19c40000
	global_load_lds_dwordx4 v[4:5], off
	v_lshrrev_b32_e32 v5, 1, v16
	v_and_b32_e32 v5, 24, v5
	v_and_b32_e32 v4, 15, v16
	v_lshlrev_b32_e32 v6, 1, v5
	v_lshl_or_b32 v157, s57, 6, v4
	v_lshl_or_b32 v4, v4, 6, v6
	v_lshlrev_b32_e32 v6, 2, v16
	v_and_b32_e32 v6, 32, v6
	v_bitop3_b32 v7, v4, s14, v6 bitop3:0xde
	s_lshl_b32 s14, s56, 5
	s_and_b32 s14, s14, 0x60
	s_lshl_b32 s56, s14, 7
	v_bitop3_b32 v158, v4, s56, v6 bitop3:0xde
	v_or_b32_e32 v6, s14, v5
	v_lshlrev_b32_e32 v4, 2, v6
	v_mov_b32_e32 v5, v3
	v_lshl_add_u64 v[4:5], s[50:51], 0, v[4:5]
	v_lshl_add_u64 v[144:145], v[4:5], 0, s[60:61]
	v_lshlrev_b32_e32 v4, 1, v6
	v_mov_b32_e32 v5, v3
	v_lshl_add_u64 v[146:147], s[48:49], 0, v[4:5]
	v_lshlrev_b32_e32 v4, 14, v21
	v_and_b32_e32 v4, 0xffff8000, v4
	s_lshr_b32 s5, s5, 26
	v_lshl_add_u32 v4, v20, 11, v4
	v_and_b32_e32 v5, 1, v21
	s_add_i32 s5, s4, s5
	v_lshl_or_b32 v4, v5, 6, v4
	s_ashr_i32 s5, s5, 6
	v_lshl_add_u32 v148, v22, 1, v4
	v_lshlrev_b32_e32 v4, 14, v17
	s_cmp_gt_i32 s4, 63
	v_and_b32_e32 v4, 0xffff8000, v4
	s_waitcnt vmcnt(6)
	s_cselect_b64 s[56:57], -1, 0
	s_add_i32 s4, s5, -2
	v_lshl_add_u32 v4, v18, 11, v4
	v_and_b32_e32 v5, 1, v17
	s_cmpk_lt_u32 s30, 0x100
	v_lshl_or_b32 v4, v5, 6, v4
	s_cselect_b64 s[58:59], -1, 0
	v_mov_b32_e32 v149, v3
	v_lshl_add_u32 v150, v19, 1, v4
	v_mov_b32_e32 v151, v3
	s_mov_b32 s69, 0
	v_add_u32_e32 v159, 0, v7
	s_mov_b32 s30, s46
	s_mov_b64 s[60:61], s[2:3]
	s_barrier
	s_branch .LBB0_1177
	.p2align	6

.LBB0_1179:
	s_and_b64 s[62:63], s[64:65], exec
	s_cselect_b32 s62, s72, s14
	s_ashr_i32 s63, s62, 31
	s_lshl_b64 s[62:63], s[62:63], 19
	s_add_u32 s62, s9, s62
	v_mov_b32_e32 v139, 0
	s_addc_u32 s63, s12, s63
	s_andn2_b64 vcc, exec, s[56:57]
	v_mov_b32_e32 v138, v139
	v_mov_b32_e32 v137, v139
	v_mov_b32_e32 v136, v139
	v_mov_b32_e32 v135, v139
	v_mov_b32_e32 v134, v139
	v_mov_b32_e32 v133, v139
	v_mov_b32_e32 v132, v139
	v_mov_b32_e32 v131, v139
	v_mov_b32_e32 v130, v139
	v_mov_b32_e32 v129, v139
	v_mov_b32_e32 v128, v139
	v_mov_b32_e32 v127, v139
	v_mov_b32_e32 v126, v139
	v_mov_b32_e32 v125, v139
	v_mov_b32_e32 v124, v139
	v_mov_b32_e32 v123, v139
	v_mov_b32_e32 v122, v139
	v_mov_b32_e32 v121, v139
	v_mov_b32_e32 v120, v139
	v_mov_b32_e32 v119, v139
	v_mov_b32_e32 v118, v139
	v_mov_b32_e32 v117, v139
	v_mov_b32_e32 v116, v139
	v_mov_b32_e32 v115, v139
	v_mov_b32_e32 v114, v139
	v_mov_b32_e32 v113, v139
	v_mov_b32_e32 v112, v139
	v_mov_b32_e32 v111, v139
	v_mov_b32_e32 v110, v139
	v_mov_b32_e32 v109, v139
	v_mov_b32_e32 v108, v139
	v_mov_b32_e32 v67, v139
	v_mov_b32_e32 v66, v139
	v_mov_b32_e32 v65, v139
	v_mov_b32_e32 v64, v139
	v_mov_b32_e32 v63, v139
	v_mov_b32_e32 v62, v139
	v_mov_b32_e32 v61, v139
	v_mov_b32_e32 v60, v139
	v_mov_b32_e32 v59, v139
	v_mov_b32_e32 v58, v139
	v_mov_b32_e32 v57, v139
	v_mov_b32_e32 v56, v139
	v_mov_b32_e32 v55, v139
	v_mov_b32_e32 v54, v139
	v_mov_b32_e32 v53, v139
	v_mov_b32_e32 v52, v139
	v_mov_b32_e32 v51, v139
	v_mov_b32_e32 v50, v139
	v_mov_b32_e32 v49, v139
	v_mov_b32_e32 v48, v139
	v_mov_b32_e32 v47, v139
	v_mov_b32_e32 v46, v139
	v_mov_b32_e32 v45, v139
	v_mov_b32_e32 v44, v139
	v_mov_b32_e32 v43, v139
	v_mov_b32_e32 v42, v139
	v_mov_b32_e32 v41, v139
	v_mov_b32_e32 v40, v139
	v_mov_b32_e32 v39, v139
	v_mov_b32_e32 v38, v139
	v_mov_b32_e32 v37, v139
	v_mov_b32_e32 v36, v139
	v_mov_b32_e32 v107, v139
	v_mov_b32_e32 v106, v139
	v_mov_b32_e32 v105, v139
	v_mov_b32_e32 v104, v139
	v_mov_b32_e32 v103, v139
	v_mov_b32_e32 v102, v139
	v_mov_b32_e32 v101, v139
	v_mov_b32_e32 v100, v139
	v_mov_b32_e32 v99, v139
	v_mov_b32_e32 v98, v139
	v_mov_b32_e32 v97, v139
	v_mov_b32_e32 v96, v139
	v_mov_b32_e32 v95, v139
	v_mov_b32_e32 v94, v139
	v_mov_b32_e32 v93, v139
	v_mov_b32_e32 v92, v139
	v_mov_b32_e32 v83, v139
	v_mov_b32_e32 v82, v139
	v_mov_b32_e32 v81, v139
	v_mov_b32_e32 v80, v139
	v_mov_b32_e32 v79, v139
	v_mov_b32_e32 v78, v139
	v_mov_b32_e32 v77, v139
	v_mov_b32_e32 v76, v139
	v_mov_b32_e32 v75, v139
	v_mov_b32_e32 v74, v139
	v_mov_b32_e32 v73, v139
	v_mov_b32_e32 v72, v139
	v_mov_b32_e32 v71, v139
	v_mov_b32_e32 v70, v139
	v_mov_b32_e32 v69, v139
	v_mov_b32_e32 v68, v139
	v_mov_b32_e32 v35, v139
	v_mov_b32_e32 v34, v139
	v_mov_b32_e32 v33, v139
	v_mov_b32_e32 v32, v139
	v_mov_b32_e32 v31, v139
	v_mov_b32_e32 v30, v139
	v_mov_b32_e32 v29, v139
	v_mov_b32_e32 v28, v139
	v_mov_b32_e32 v27, v139
	v_mov_b32_e32 v26, v139
	v_mov_b32_e32 v25, v139
	v_mov_b32_e32 v24, v139
	v_mov_b32_e32 v23, v139
	v_mov_b32_e32 v22, v139
	v_mov_b32_e32 v21, v139
	v_mov_b32_e32 v20, v139
	v_mov_b32_e32 v19, v139
	v_mov_b32_e32 v18, v139
	v_mov_b32_e32 v17, v139
	v_mov_b32_e32 v16, v139
	v_mov_b32_e32 v15, v139
	v_mov_b32_e32 v14, v139
	v_mov_b32_e32 v13, v139
	v_mov_b32_e32 v12, v139
	v_mov_b32_e32 v11, v139
	v_mov_b32_e32 v10, v139
	v_mov_b32_e32 v9, v139
	v_mov_b32_e32 v8, v139
	v_mov_b32_e32 v7, v139
	v_mov_b32_e32 v6, v139
	v_mov_b32_e32 v5, v139
	v_mov_b32_e32 v4, v139
	s_cbranch_vccnz .LBB0_1183
	s_and_b64 s[74:75], s[64:65], exec
	s_cselect_b32 s73, s63, s1
	s_cselect_b32 s74, s62, s0
	s_add_u32 s0, s0, 0x40080
	s_addc_u32 s1, s1, 0
	s_add_u32 s75, s2, 0x100
	v_mov_b32_e32 v4, 0
	s_addc_u32 s77, s3, 0
	s_mov_b32 s2, 0
	v_mov_b32_e32 v5, v4
	v_mov_b32_e32 v6, v4
	v_mov_b32_e32 v7, v4
	v_mov_b32_e32 v8, v4
	v_mov_b32_e32 v9, v4
	v_mov_b32_e32 v10, v4
	v_mov_b32_e32 v11, v4
	v_mov_b32_e32 v12, v4
	v_mov_b32_e32 v13, v4
	v_mov_b32_e32 v14, v4
	v_mov_b32_e32 v15, v4
	v_mov_b32_e32 v16, v4
	v_mov_b32_e32 v17, v4
	v_mov_b32_e32 v18, v4
	v_mov_b32_e32 v19, v4
	v_mov_b32_e32 v20, v4
	v_mov_b32_e32 v21, v4
	v_mov_b32_e32 v22, v4
	v_mov_b32_e32 v23, v4
	v_mov_b32_e32 v24, v4
	v_mov_b32_e32 v25, v4
	v_mov_b32_e32 v26, v4
	v_mov_b32_e32 v27, v4
	v_mov_b32_e32 v28, v4
	v_mov_b32_e32 v29, v4
	v_mov_b32_e32 v30, v4
	v_mov_b32_e32 v31, v4
	v_mov_b32_e32 v32, v4
	v_mov_b32_e32 v33, v4
	v_mov_b32_e32 v34, v4
	v_mov_b32_e32 v35, v4
	v_mov_b32_e32 v68, v4
	v_mov_b32_e32 v69, v4
	v_mov_b32_e32 v70, v4
	v_mov_b32_e32 v71, v4
	v_mov_b32_e32 v72, v4
	v_mov_b32_e32 v73, v4
	v_mov_b32_e32 v74, v4
	v_mov_b32_e32 v75, v4
	v_mov_b32_e32 v76, v4
	v_mov_b32_e32 v77, v4
	v_mov_b32_e32 v78, v4
	v_mov_b32_e32 v79, v4
	v_mov_b32_e32 v80, v4
	v_mov_b32_e32 v81, v4
	v_mov_b32_e32 v82, v4
	v_mov_b32_e32 v83, v4
	v_mov_b32_e32 v92, v4
	v_mov_b32_e32 v93, v4
	v_mov_b32_e32 v94, v4
	v_mov_b32_e32 v95, v4
	v_mov_b32_e32 v96, v4
	v_mov_b32_e32 v97, v4
	v_mov_b32_e32 v98, v4
	v_mov_b32_e32 v99, v4
	v_mov_b32_e32 v100, v4
	v_mov_b32_e32 v101, v4
	v_mov_b32_e32 v102, v4
	v_mov_b32_e32 v103, v4
	v_mov_b32_e32 v104, v4
	v_mov_b32_e32 v105, v4
	v_mov_b32_e32 v106, v4
	v_mov_b32_e32 v107, v4
	v_mov_b32_e32 v36, v4
	v_mov_b32_e32 v37, v4
	v_mov_b32_e32 v38, v4
	v_mov_b32_e32 v39, v4
	v_mov_b32_e32 v40, v4
	v_mov_b32_e32 v41, v4
	v_mov_b32_e32 v42, v4
	v_mov_b32_e32 v43, v4
	v_mov_b32_e32 v44, v4
	v_mov_b32_e32 v45, v4
	v_mov_b32_e32 v46, v4
	v_mov_b32_e32 v47, v4
	v_mov_b32_e32 v48, v4
	v_mov_b32_e32 v49, v4
	v_mov_b32_e32 v50, v4
	v_mov_b32_e32 v51, v4
	v_mov_b32_e32 v52, v4
	v_mov_b32_e32 v53, v4
	v_mov_b32_e32 v54, v4
	v_mov_b32_e32 v55, v4
	v_mov_b32_e32 v56, v4
	v_mov_b32_e32 v57, v4
	v_mov_b32_e32 v58, v4
	v_mov_b32_e32 v59, v4
	v_mov_b32_e32 v60, v4
	v_mov_b32_e32 v61, v4
	v_mov_b32_e32 v62, v4
	v_mov_b32_e32 v63, v4
	v_mov_b32_e32 v64, v4
	v_mov_b32_e32 v65, v4
	v_mov_b32_e32 v66, v4
	v_mov_b32_e32 v67, v4
	v_mov_b32_e32 v108, v4
	v_mov_b32_e32 v109, v4
	v_mov_b32_e32 v110, v4
	v_mov_b32_e32 v111, v4
	v_mov_b32_e32 v112, v4
	v_mov_b32_e32 v113, v4
	v_mov_b32_e32 v114, v4
	v_mov_b32_e32 v115, v4
	v_mov_b32_e32 v116, v4
	v_mov_b32_e32 v117, v4
	v_mov_b32_e32 v118, v4
	v_mov_b32_e32 v119, v4
	v_mov_b32_e32 v120, v4
	v_mov_b32_e32 v121, v4
	v_mov_b32_e32 v122, v4
	v_mov_b32_e32 v123, v4
	v_mov_b32_e32 v124, v4
	v_mov_b32_e32 v125, v4
	v_mov_b32_e32 v126, v4
	v_mov_b32_e32 v127, v4
	v_mov_b32_e32 v128, v4
	v_mov_b32_e32 v129, v4
	v_mov_b32_e32 v130, v4
	v_mov_b32_e32 v131, v4
	v_mov_b32_e32 v132, v4
	v_mov_b32_e32 v133, v4
	v_mov_b32_e32 v134, v4
	v_mov_b32_e32 v135, v4
	v_mov_b32_e32 v136, v4
	v_mov_b32_e32 v137, v4
	v_mov_b32_e32 v138, v4
	v_mov_b32_e32 v139, v4
	.p2align	6

.LBB0_1197:
	s_add_i32 m0, s41, 0x18000
	v_lshl_add_u64 v[4:5], v[4:5], 0, s[24:25]
	s_waitcnt vmcnt(2)
	s_barrier
	global_load_lds_dwordx4 v[4:5], off
	v_lshl_add_u64 v[4:5], v[6:7], 0, s[24:25]
	s_add_i32 m0, s41, 0x1a000
	s_add_i32 s79, s41, 0x8000
	global_load_lds_dwordx4 v[4:5], off
	v_lshl_add_u64 v[4:5], v[12:13], 0, s[24:25]
	s_mov_b32 m0, s79
	s_add_i32 s82, s41, 0xa000
	global_load_lds_dwordx4 v[4:5], off
	v_lshl_add_u64 v[4:5], v[14:15], 0, s[24:25]
	s_mov_b32 m0, s82
	s_sext_i32_i8 s65, s6
	global_load_lds_dwordx4 v[4:5], off
	s_add_i32 m0, s41, 0x1c000
	v_lshl_add_u64 v[4:5], v[8:9], 0, s[24:25]
	global_load_lds_dwordx4 v[4:5], off
	v_lshl_add_u64 v[4:5], v[10:11], 0, s[24:25]
	s_add_i32 m0, s41, 0x1e000
	s_lshr_b32 s5, s5, 26
	global_load_lds_dwordx4 v[4:5], off
	v_and_b32_e32 v4, 48, v2
	v_lshlrev_b32_e32 v5, 6, v2
	s_movk_i32 s6, 0x3c0
	s_add_i32 s5, s4, s5
	v_and_or_b32 v4, v5, s6, v4
	v_lshlrev_b32_e32 v5, 2, v2
	s_ashr_i32 s83, s5, 6
	s_lshl_b32 s5, s35, 13
	v_and_b32_e32 v5, 32, v5
	v_bitop3_b32 v6, v4, s5, v5 bitop3:0xde
	s_lshl_b32 s5, s34, 5
	s_and_b32 s5, s5, 0x60
	s_lshl_b32 s6, s5, 7
	v_bitop3_b32 v144, s6, v4, v5 bitop3:0xf6
	v_bfe_u32 v4, v2, 2, 4
	v_lshl_or_b32 v146, s35, 6, v4
	v_lshlrev_b32_e32 v4, 14, v16
	v_and_b32_e32 v5, 3, v2
	v_and_b32_e32 v2, 60, v2
	v_and_b32_e32 v4, 0xffff8000, v4
	v_lshl_or_b32 v145, v5, 6, v2
	v_lshlrev_b32_e32 v2, 3, v5
	v_lshl_add_u32 v4, v17, 11, v4
	v_and_b32_e32 v5, 1, v16
	v_lshl_or_b32 v4, v5, 6, v4
	s_ashr_i32 s85, s71, 31
	v_lshl_add_u32 v138, v18, 1, v4
	v_lshlrev_b32_e32 v4, 14, v19
	s_cmp_gt_i32 s4, 63
	v_and_b32_e32 v4, 0xffff8000, v4
	s_waitcnt vmcnt(6)
	s_cselect_b64 s[60:61], -1, 0
	s_add_i32 s86, s83, -2
	v_lshl_add_u32 v4, v20, 11, v4
	v_and_b32_e32 v5, 1, v19
	s_cmpk_lt_u32 s7, 0x100
	v_lshl_or_b32 v4, v5, 6, v4
	s_cselect_b64 s[62:63], -1, 0
	v_mov_b32_e32 v139, v3
	v_lshl_add_u32 v140, v21, 1, v4
	v_mov_b32_e32 v141, v3
	s_mov_b32 s87, 0
	v_add_u32_e32 v147, 0, v6
	s_lshl_b32 s64, s5, 1
	v_lshlrev_b32_e32 v2, 1, v2
	s_barrier
	s_branch .LBB0_1200
	.p2align	6

.LBB0_1209:
	s_ashr_i32 s67, s66, 31
	s_lshl_b64 s[6:7], s[66:67], 19
	s_add_u32 s74, s12, s6
	v_mov_b32_e32 v127, 0
	s_addc_u32 s75, s13, s7
	s_andn2_b64 vcc, exec, s[60:61]
	v_mov_b32_e32 v126, v127
	v_mov_b32_e32 v125, v127
	v_mov_b32_e32 v124, v127
	v_mov_b32_e32 v131, v127
	v_mov_b32_e32 v130, v127
	v_mov_b32_e32 v129, v127
	v_mov_b32_e32 v128, v127
	v_mov_b32_e32 v115, v127
	v_mov_b32_e32 v114, v127
	v_mov_b32_e32 v113, v127
	v_mov_b32_e32 v112, v127
	v_mov_b32_e32 v111, v127
	v_mov_b32_e32 v110, v127
	v_mov_b32_e32 v109, v127
	v_mov_b32_e32 v108, v127
	v_mov_b32_e32 v99, v127
	v_mov_b32_e32 v98, v127
	v_mov_b32_e32 v97, v127
	v_mov_b32_e32 v96, v127
	v_mov_b32_e32 v95, v127
	v_mov_b32_e32 v94, v127
	v_mov_b32_e32 v93, v127
	v_mov_b32_e32 v92, v127
	v_mov_b32_e32 v83, v127
	v_mov_b32_e32 v82, v127
	v_mov_b32_e32 v81, v127
	v_mov_b32_e32 v80, v127
	v_mov_b32_e32 v79, v127
	v_mov_b32_e32 v78, v127
	v_mov_b32_e32 v77, v127
	v_mov_b32_e32 v76, v127
	v_mov_b32_e32 v123, v127
	v_mov_b32_e32 v122, v127
	v_mov_b32_e32 v121, v127
	v_mov_b32_e32 v120, v127
	v_mov_b32_e32 v119, v127
	v_mov_b32_e32 v118, v127
	v_mov_b32_e32 v117, v127
	v_mov_b32_e32 v116, v127
	v_mov_b32_e32 v107, v127
	v_mov_b32_e32 v106, v127
	v_mov_b32_e32 v105, v127
	v_mov_b32_e32 v104, v127
	v_mov_b32_e32 v103, v127
	v_mov_b32_e32 v102, v127
	v_mov_b32_e32 v101, v127
	v_mov_b32_e32 v100, v127
	v_mov_b32_e32 v91, v127
	v_mov_b32_e32 v90, v127
	v_mov_b32_e32 v89, v127
	v_mov_b32_e32 v88, v127
	v_mov_b32_e32 v87, v127
	v_mov_b32_e32 v86, v127
	v_mov_b32_e32 v85, v127
	v_mov_b32_e32 v84, v127
	v_mov_b32_e32 v75, v127
	v_mov_b32_e32 v74, v127
	v_mov_b32_e32 v73, v127
	v_mov_b32_e32 v72, v127
	v_mov_b32_e32 v71, v127
	v_mov_b32_e32 v70, v127
	v_mov_b32_e32 v69, v127
	v_mov_b32_e32 v68, v127
	v_mov_b32_e32 v67, v127
	v_mov_b32_e32 v66, v127
	v_mov_b32_e32 v65, v127
	v_mov_b32_e32 v64, v127
	v_mov_b32_e32 v63, v127
	v_mov_b32_e32 v62, v127
	v_mov_b32_e32 v61, v127
	v_mov_b32_e32 v60, v127
	v_mov_b32_e32 v51, v127
	v_mov_b32_e32 v50, v127
	v_mov_b32_e32 v49, v127
	v_mov_b32_e32 v48, v127
	v_mov_b32_e32 v47, v127
	v_mov_b32_e32 v46, v127
	v_mov_b32_e32 v45, v127
	v_mov_b32_e32 v44, v127
	v_mov_b32_e32 v35, v127
	v_mov_b32_e32 v34, v127
	v_mov_b32_e32 v33, v127
	v_mov_b32_e32 v32, v127
	v_mov_b32_e32 v31, v127
	v_mov_b32_e32 v30, v127
	v_mov_b32_e32 v29, v127
	v_mov_b32_e32 v28, v127
	v_mov_b32_e32 v19, v127
	v_mov_b32_e32 v18, v127
	v_mov_b32_e32 v17, v127
	v_mov_b32_e32 v16, v127
	v_mov_b32_e32 v15, v127
	v_mov_b32_e32 v14, v127
	v_mov_b32_e32 v13, v127
	v_mov_b32_e32 v12, v127
	v_mov_b32_e32 v59, v127
	v_mov_b32_e32 v58, v127
	v_mov_b32_e32 v57, v127
	v_mov_b32_e32 v56, v127
	v_mov_b32_e32 v55, v127
	v_mov_b32_e32 v54, v127
	v_mov_b32_e32 v53, v127
	v_mov_b32_e32 v52, v127
	v_mov_b32_e32 v43, v127
	v_mov_b32_e32 v42, v127
	v_mov_b32_e32 v41, v127
	v_mov_b32_e32 v40, v127
	v_mov_b32_e32 v39, v127
	v_mov_b32_e32 v38, v127
	v_mov_b32_e32 v37, v127
	v_mov_b32_e32 v36, v127
	v_mov_b32_e32 v27, v127
	v_mov_b32_e32 v26, v127
	v_mov_b32_e32 v25, v127
	v_mov_b32_e32 v24, v127
	v_mov_b32_e32 v23, v127
	v_mov_b32_e32 v22, v127
	v_mov_b32_e32 v21, v127
	v_mov_b32_e32 v20, v127
	v_mov_b32_e32 v11, v127
	v_mov_b32_e32 v10, v127
	v_mov_b32_e32 v9, v127
	v_mov_b32_e32 v8, v127
	v_mov_b32_e32 v7, v127
	v_mov_b32_e32 v6, v127
	v_mov_b32_e32 v5, v127
	v_mov_b32_e32 v4, v127
	s_cbranch_vccnz .LBB0_1213
	s_and_b64 s[4:5], s[4:5], exec
	s_cselect_b32 s4, s75, s1
	s_cselect_b32 s5, s74, s0
	s_add_u32 s0, s0, 0x40080
	s_addc_u32 s1, s1, 0
	s_add_u32 s6, s2, 0x100
	v_mov_b32_e32 v4, 0
	s_addc_u32 s7, s3, 0
	s_mov_b32 s2, 0
	v_mov_b32_e32 v5, v4
	v_mov_b32_e32 v6, v4
	v_mov_b32_e32 v7, v4
	v_mov_b32_e32 v8, v4
	v_mov_b32_e32 v9, v4
	v_mov_b32_e32 v10, v4
	v_mov_b32_e32 v11, v4
	v_mov_b32_e32 v20, v4
	v_mov_b32_e32 v21, v4
	v_mov_b32_e32 v22, v4
	v_mov_b32_e32 v23, v4
	v_mov_b32_e32 v24, v4
	v_mov_b32_e32 v25, v4
	v_mov_b32_e32 v26, v4
	v_mov_b32_e32 v27, v4
	v_mov_b32_e32 v36, v4
	v_mov_b32_e32 v37, v4
	v_mov_b32_e32 v38, v4
	v_mov_b32_e32 v39, v4
	v_mov_b32_e32 v40, v4
	v_mov_b32_e32 v41, v4
	v_mov_b32_e32 v42, v4
	v_mov_b32_e32 v43, v4
	v_mov_b32_e32 v52, v4
	v_mov_b32_e32 v53, v4
	v_mov_b32_e32 v54, v4
	v_mov_b32_e32 v55, v4
	v_mov_b32_e32 v56, v4
	v_mov_b32_e32 v57, v4
	v_mov_b32_e32 v58, v4
	v_mov_b32_e32 v59, v4
	v_mov_b32_e32 v12, v4
	v_mov_b32_e32 v13, v4
	v_mov_b32_e32 v14, v4
	v_mov_b32_e32 v15, v4
	v_mov_b32_e32 v16, v4
	v_mov_b32_e32 v17, v4
	v_mov_b32_e32 v18, v4
	v_mov_b32_e32 v19, v4
	v_mov_b32_e32 v28, v4
	v_mov_b32_e32 v29, v4
	v_mov_b32_e32 v30, v4
	v_mov_b32_e32 v31, v4
	v_mov_b32_e32 v32, v4
	v_mov_b32_e32 v33, v4
	v_mov_b32_e32 v34, v4
	v_mov_b32_e32 v35, v4
	v_mov_b32_e32 v44, v4
	v_mov_b32_e32 v45, v4
	v_mov_b32_e32 v46, v4
	v_mov_b32_e32 v47, v4
	v_mov_b32_e32 v48, v4
	v_mov_b32_e32 v49, v4
	v_mov_b32_e32 v50, v4
	v_mov_b32_e32 v51, v4
	v_mov_b32_e32 v60, v4
	v_mov_b32_e32 v61, v4
	v_mov_b32_e32 v62, v4
	v_mov_b32_e32 v63, v4
	v_mov_b32_e32 v64, v4
	v_mov_b32_e32 v65, v4
	v_mov_b32_e32 v66, v4
	v_mov_b32_e32 v67, v4
	v_mov_b32_e32 v68, v4
	v_mov_b32_e32 v69, v4
	v_mov_b32_e32 v70, v4
	v_mov_b32_e32 v71, v4
	v_mov_b32_e32 v72, v4
	v_mov_b32_e32 v73, v4
	v_mov_b32_e32 v74, v4
	v_mov_b32_e32 v75, v4
	v_mov_b32_e32 v84, v4
	v_mov_b32_e32 v85, v4
	v_mov_b32_e32 v86, v4
	v_mov_b32_e32 v87, v4
	v_mov_b32_e32 v88, v4
	v_mov_b32_e32 v89, v4
	v_mov_b32_e32 v90, v4
	v_mov_b32_e32 v91, v4
	v_mov_b32_e32 v100, v4
	v_mov_b32_e32 v101, v4
	v_mov_b32_e32 v102, v4
	v_mov_b32_e32 v103, v4
	v_mov_b32_e32 v104, v4
	v_mov_b32_e32 v105, v4
	v_mov_b32_e32 v106, v4
	v_mov_b32_e32 v107, v4
	v_mov_b32_e32 v116, v4
	v_mov_b32_e32 v117, v4
	v_mov_b32_e32 v118, v4
	v_mov_b32_e32 v119, v4
	v_mov_b32_e32 v120, v4
	v_mov_b32_e32 v121, v4
	v_mov_b32_e32 v122, v4
	v_mov_b32_e32 v123, v4
	v_mov_b32_e32 v76, v4
	v_mov_b32_e32 v77, v4
	v_mov_b32_e32 v78, v4
	v_mov_b32_e32 v79, v4
	v_mov_b32_e32 v80, v4
	v_mov_b32_e32 v81, v4
	v_mov_b32_e32 v82, v4
	v_mov_b32_e32 v83, v4
	v_mov_b32_e32 v92, v4
	v_mov_b32_e32 v93, v4
	v_mov_b32_e32 v94, v4
	v_mov_b32_e32 v95, v4
	v_mov_b32_e32 v96, v4
	v_mov_b32_e32 v97, v4
	v_mov_b32_e32 v98, v4
	v_mov_b32_e32 v99, v4
	v_mov_b32_e32 v108, v4
	v_mov_b32_e32 v109, v4
	v_mov_b32_e32 v110, v4
	v_mov_b32_e32 v111, v4
	v_mov_b32_e32 v112, v4
	v_mov_b32_e32 v113, v4
	v_mov_b32_e32 v114, v4
	v_mov_b32_e32 v115, v4
	v_mov_b32_e32 v128, v4
	v_mov_b32_e32 v129, v4
	v_mov_b32_e32 v130, v4
	v_mov_b32_e32 v131, v4
	v_mov_b32_e32 v124, v4
	v_mov_b32_e32 v125, v4
	v_mov_b32_e32 v126, v4
	v_mov_b32_e32 v127, v4
	.p2align	6

.LBB0_1224:
	v_lshl_add_u64 v[4:5], s[4:5], 0, v[2:3]
	v_mov_b32_e32 v1, v3
	v_lshl_add_u64 v[6:7], s[4:5], 0, v[0:1]
	v_mov_b32_e32 v135, v3
	s_add_i32 m0, s35, 0x18000
	v_lshl_add_u64 v[4:5], v[4:5], 0, s[24:25]
	s_waitcnt vmcnt(0)
	v_lshl_add_u64 v[8:9], s[20:21], 0, v[2:3]
	v_lshl_add_u64 v[10:11], s[20:21], 0, v[0:1]
	v_lshl_add_u64 v[12:13], s[2:3], 0, v[134:135]
	v_mov_b32_e32 v133, v3
	s_waitcnt vmcnt(2)
	s_barrier
	global_load_lds_dwordx4 v[4:5], off
	v_lshl_add_u64 v[4:5], v[6:7], 0, s[24:25]
	s_add_i32 m0, s35, 0x1a000
	s_add_i32 s20, s35, 0x8000
	v_lshl_add_u64 v[14:15], s[2:3], 0, v[132:133]
	global_load_lds_dwordx4 v[4:5], off
	v_lshl_add_u64 v[4:5], v[12:13], 0, s[24:25]
	s_mov_b32 m0, s20
	s_add_i32 s21, s35, 0xa000
	global_load_lds_dwordx4 v[4:5], off
	v_lshl_add_u64 v[4:5], v[14:15], 0, s[24:25]
	s_mov_b32 m0, s21
	s_lshl_b32 s12, s56, 5
	global_load_lds_dwordx4 v[4:5], off
	s_add_i32 m0, s35, 0x1c000
	v_lshl_add_u64 v[4:5], v[8:9], 0, s[24:25]
	global_load_lds_dwordx4 v[4:5], off
	v_lshl_add_u64 v[4:5], v[10:11], 0, s[24:25]
	s_add_i32 m0, s35, 0x1e000
	s_lshl_b32 s13, s58, 6
	global_load_lds_dwordx4 v[4:5], off
	s_waitcnt vmcnt(6)
	s_and_b32 s12, s12, 0x60
	v_mov_b32_e32 v131, 0
	s_cmp_lt_i32 s8, 64
	v_mov_b32_e32 v130, v131
	v_mov_b32_e32 v129, v131
	v_mov_b32_e32 v128, v131
	v_mov_b32_e32 v127, v131
	v_mov_b32_e32 v126, v131
	v_mov_b32_e32 v125, v131
	v_mov_b32_e32 v124, v131
	v_mov_b32_e32 v115, v131
	v_mov_b32_e32 v114, v131
	v_mov_b32_e32 v113, v131
	v_mov_b32_e32 v112, v131
	v_mov_b32_e32 v111, v131
	v_mov_b32_e32 v110, v131
	v_mov_b32_e32 v109, v131
	v_mov_b32_e32 v108, v131
	v_mov_b32_e32 v99, v131
	v_mov_b32_e32 v98, v131
	v_mov_b32_e32 v97, v131
	v_mov_b32_e32 v96, v131
	v_mov_b32_e32 v95, v131
	v_mov_b32_e32 v94, v131
	v_mov_b32_e32 v93, v131
	v_mov_b32_e32 v92, v131
	v_mov_b32_e32 v83, v131
	v_mov_b32_e32 v82, v131
	v_mov_b32_e32 v81, v131
	v_mov_b32_e32 v80, v131
	v_mov_b32_e32 v79, v131
	v_mov_b32_e32 v78, v131
	v_mov_b32_e32 v77, v131
	v_mov_b32_e32 v76, v131
	v_mov_b32_e32 v123, v131
	v_mov_b32_e32 v122, v131
	v_mov_b32_e32 v121, v131
	v_mov_b32_e32 v120, v131
	v_mov_b32_e32 v119, v131
	v_mov_b32_e32 v118, v131
	v_mov_b32_e32 v117, v131
	v_mov_b32_e32 v116, v131
	v_mov_b32_e32 v107, v131
	v_mov_b32_e32 v106, v131
	v_mov_b32_e32 v105, v131
	v_mov_b32_e32 v104, v131
	v_mov_b32_e32 v103, v131
	v_mov_b32_e32 v102, v131
	v_mov_b32_e32 v101, v131
	v_mov_b32_e32 v100, v131
	v_mov_b32_e32 v91, v131
	v_mov_b32_e32 v90, v131
	v_mov_b32_e32 v89, v131
	v_mov_b32_e32 v88, v131
	v_mov_b32_e32 v87, v131
	v_mov_b32_e32 v86, v131
	v_mov_b32_e32 v85, v131
	v_mov_b32_e32 v84, v131
	v_mov_b32_e32 v75, v131
	v_mov_b32_e32 v74, v131
	v_mov_b32_e32 v73, v131
	v_mov_b32_e32 v72, v131
	v_mov_b32_e32 v71, v131
	v_mov_b32_e32 v70, v131
	v_mov_b32_e32 v69, v131
	v_mov_b32_e32 v68, v131
	v_mov_b32_e32 v67, v131
	v_mov_b32_e32 v66, v131
	v_mov_b32_e32 v65, v131
	v_mov_b32_e32 v64, v131
	v_mov_b32_e32 v63, v131
	v_mov_b32_e32 v62, v131
	v_mov_b32_e32 v61, v131
	v_mov_b32_e32 v60, v131
	v_mov_b32_e32 v51, v131
	v_mov_b32_e32 v50, v131
	v_mov_b32_e32 v49, v131
	v_mov_b32_e32 v48, v131
	v_mov_b32_e32 v47, v131
	v_mov_b32_e32 v46, v131
	v_mov_b32_e32 v45, v131
	v_mov_b32_e32 v44, v131
	v_mov_b32_e32 v35, v131
	v_mov_b32_e32 v34, v131
	v_mov_b32_e32 v33, v131
	v_mov_b32_e32 v32, v131
	v_mov_b32_e32 v31, v131
	v_mov_b32_e32 v30, v131
	v_mov_b32_e32 v29, v131
	v_mov_b32_e32 v28, v131
	v_mov_b32_e32 v19, v131
	v_mov_b32_e32 v18, v131
	v_mov_b32_e32 v17, v131
	v_mov_b32_e32 v16, v131
	v_mov_b32_e32 v15, v131
	v_mov_b32_e32 v14, v131
	v_mov_b32_e32 v13, v131
	v_mov_b32_e32 v12, v131
	v_mov_b32_e32 v59, v131
	v_mov_b32_e32 v58, v131
	v_mov_b32_e32 v57, v131
	v_mov_b32_e32 v56, v131
	v_mov_b32_e32 v55, v131
	v_mov_b32_e32 v54, v131
	v_mov_b32_e32 v53, v131
	v_mov_b32_e32 v52, v131
	v_mov_b32_e32 v43, v131
	v_mov_b32_e32 v42, v131
	v_mov_b32_e32 v41, v131
	v_mov_b32_e32 v40, v131
	v_mov_b32_e32 v39, v131
	v_mov_b32_e32 v38, v131
	v_mov_b32_e32 v37, v131
	v_mov_b32_e32 v36, v131
	v_mov_b32_e32 v27, v131
	v_mov_b32_e32 v26, v131
	v_mov_b32_e32 v25, v131
	v_mov_b32_e32 v24, v131
	v_mov_b32_e32 v23, v131
	v_mov_b32_e32 v22, v131
	v_mov_b32_e32 v21, v131
	v_mov_b32_e32 v20, v131
	v_mov_b32_e32 v11, v131
	v_mov_b32_e32 v10, v131
	v_mov_b32_e32 v9, v131
	v_mov_b32_e32 v8, v131
	v_mov_b32_e32 v7, v131
	v_mov_b32_e32 v6, v131
	v_mov_b32_e32 v5, v131
	v_mov_b32_e32 v4, v131
	s_barrier
	s_cbranch_scc1 .LBB0_1228
	s_lshr_b32 s9, s9, 26
	v_and_b32_e32 v4, 15, v140
	s_add_i32 s8, s8, s9
	v_or_b32_e32 v6, s13, v4
	s_ashr_i32 s56, s8, 6
	v_and_b32_e32 v5, 48, v140
	v_lshlrev_b32_e32 v7, 6, v6
	s_movk_i32 s8, 0x3c0
	v_lshlrev_b32_e32 v6, 2, v6
	v_and_or_b32 v7, v7, s8, v5
	s_lshl_b32 s8, s58, 13
	v_and_b32_e32 v6, 32, v6
	v_lshl_or_b32 v4, v4, 6, v5
	v_lshlrev_b32_e32 v5, 2, v140
	v_bitop3_b32 v6, v7, s8, v6 bitop3:0xde
	s_lshl_b32 s8, s12, 7
	v_and_b32_e32 v5, 32, v5
	v_bitop3_b32 v141, s8, v4, v5 bitop3:0xf6
	v_lshlrev_b32_e32 v4, 14, v137
	v_and_b32_e32 v4, 0xffff8000, v4
	s_add_i32 s57, s56, -2
	v_lshl_add_u32 v4, v136, 11, v4
	v_and_b32_e32 v5, 1, v137
	v_lshl_or_b32 v4, v5, 6, v4
	s_add_u32 s6, s36, s6
	v_lshl_add_u32 v4, v143, 1, v4
	v_mov_b32_e32 v5, v3
	s_addc_u32 s7, s37, s7
	v_lshl_add_u64 v[136:137], s[6:7], 0, v[4:5]
	v_lshlrev_b32_e32 v4, 14, v138
	v_and_b32_e32 v4, 0xffff8000, v4
	v_lshl_add_u32 v4, v139, 11, v4
	v_and_b32_e32 v5, 1, v138
	v_lshl_or_b32 v4, v5, 6, v4
	v_lshl_add_u32 v4, v142, 1, v4
	v_mov_b32_e32 v5, v3
	v_lshl_add_u64 v[138:139], s[6:7], 0, v[4:5]
	v_mov_b32_e32 v4, 0
	s_mov_b32 s8, 0
	s_mov_b64 s[6:7], 0x75208080
	v_add_u32_e32 v142, 0, v6
	v_mov_b32_e32 v5, v4
	v_mov_b32_e32 v6, v4
	v_mov_b32_e32 v7, v4
	v_mov_b32_e32 v8, v4
	v_mov_b32_e32 v9, v4
	v_mov_b32_e32 v10, v4
	v_mov_b32_e32 v11, v4
	v_mov_b32_e32 v20, v4
	v_mov_b32_e32 v21, v4
	v_mov_b32_e32 v22, v4
	v_mov_b32_e32 v23, v4
	v_mov_b32_e32 v24, v4
	v_mov_b32_e32 v25, v4
	v_mov_b32_e32 v26, v4
	v_mov_b32_e32 v27, v4
	v_mov_b32_e32 v36, v4
	v_mov_b32_e32 v37, v4
	v_mov_b32_e32 v38, v4
	v_mov_b32_e32 v39, v4
	v_mov_b32_e32 v40, v4
	v_mov_b32_e32 v41, v4
	v_mov_b32_e32 v42, v4
	v_mov_b32_e32 v43, v4
	v_mov_b32_e32 v52, v4
	v_mov_b32_e32 v53, v4
	v_mov_b32_e32 v54, v4
	v_mov_b32_e32 v55, v4
	v_mov_b32_e32 v56, v4
	v_mov_b32_e32 v57, v4
	v_mov_b32_e32 v58, v4
	v_mov_b32_e32 v59, v4
	v_mov_b32_e32 v12, v4
	v_mov_b32_e32 v13, v4
	v_mov_b32_e32 v14, v4
	v_mov_b32_e32 v15, v4
	v_mov_b32_e32 v16, v4
	v_mov_b32_e32 v17, v4
	v_mov_b32_e32 v18, v4
	v_mov_b32_e32 v19, v4
	v_mov_b32_e32 v28, v4
	v_mov_b32_e32 v29, v4
	v_mov_b32_e32 v30, v4
	v_mov_b32_e32 v31, v4
	v_mov_b32_e32 v32, v4
	v_mov_b32_e32 v33, v4
	v_mov_b32_e32 v34, v4
	v_mov_b32_e32 v35, v4
	v_mov_b32_e32 v44, v4
	v_mov_b32_e32 v45, v4
	v_mov_b32_e32 v46, v4
	v_mov_b32_e32 v47, v4
	v_mov_b32_e32 v48, v4
	v_mov_b32_e32 v49, v4
	v_mov_b32_e32 v50, v4
	v_mov_b32_e32 v51, v4
	v_mov_b32_e32 v60, v4
	v_mov_b32_e32 v61, v4
	v_mov_b32_e32 v62, v4
	v_mov_b32_e32 v63, v4
	v_mov_b32_e32 v64, v4
	v_mov_b32_e32 v65, v4
	v_mov_b32_e32 v66, v4
	v_mov_b32_e32 v67, v4
	v_mov_b32_e32 v68, v4
	v_mov_b32_e32 v69, v4
	v_mov_b32_e32 v70, v4
	v_mov_b32_e32 v71, v4
	v_mov_b32_e32 v72, v4
	v_mov_b32_e32 v73, v4
	v_mov_b32_e32 v74, v4
	v_mov_b32_e32 v75, v4
	v_mov_b32_e32 v84, v4
	v_mov_b32_e32 v85, v4
	v_mov_b32_e32 v86, v4
	v_mov_b32_e32 v87, v4
	v_mov_b32_e32 v88, v4
	v_mov_b32_e32 v89, v4
	v_mov_b32_e32 v90, v4
	v_mov_b32_e32 v91, v4
	v_mov_b32_e32 v100, v4
	v_mov_b32_e32 v101, v4
	v_mov_b32_e32 v102, v4
	v_mov_b32_e32 v103, v4
	v_mov_b32_e32 v104, v4
	v_mov_b32_e32 v105, v4
	v_mov_b32_e32 v106, v4
	v_mov_b32_e32 v107, v4
	v_mov_b32_e32 v116, v4
	v_mov_b32_e32 v117, v4
	v_mov_b32_e32 v118, v4
	v_mov_b32_e32 v119, v4
	v_mov_b32_e32 v120, v4
	v_mov_b32_e32 v121, v4
	v_mov_b32_e32 v122, v4
	v_mov_b32_e32 v123, v4
	v_mov_b32_e32 v76, v4
	v_mov_b32_e32 v77, v4
	v_mov_b32_e32 v78, v4
	v_mov_b32_e32 v79, v4
	v_mov_b32_e32 v80, v4
	v_mov_b32_e32 v81, v4
	v_mov_b32_e32 v82, v4
	v_mov_b32_e32 v83, v4
	v_mov_b32_e32 v92, v4
	v_mov_b32_e32 v93, v4
	v_mov_b32_e32 v94, v4
	v_mov_b32_e32 v95, v4
	v_mov_b32_e32 v96, v4
	v_mov_b32_e32 v97, v4
	v_mov_b32_e32 v98, v4
	v_mov_b32_e32 v99, v4
	v_mov_b32_e32 v108, v4
	v_mov_b32_e32 v109, v4
	v_mov_b32_e32 v110, v4
	v_mov_b32_e32 v111, v4
	v_mov_b32_e32 v112, v4
	v_mov_b32_e32 v113, v4
	v_mov_b32_e32 v114, v4
	v_mov_b32_e32 v115, v4
	v_mov_b32_e32 v124, v4
	v_mov_b32_e32 v125, v4
	v_mov_b32_e32 v126, v4
	v_mov_b32_e32 v127, v4
	v_mov_b32_e32 v128, v4
	v_mov_b32_e32 v129, v4
	v_mov_b32_e32 v130, v4
	v_mov_b32_e32 v131, v4
	.p2align	6

.LBB0_1234:
	s_add_i32 m0, s47, 0x18000
	v_lshl_add_u64 v[4:5], v[4:5], 0, s[24:25]
	s_waitcnt vmcnt(2)
	s_barrier
	global_load_lds_dwordx4 v[4:5], off
	v_lshl_add_u64 v[4:5], v[6:7], 0, s[24:25]
	s_add_i32 m0, s47, 0x1a000
	s_add_i32 s60, s47, 0x8000
	global_load_lds_dwordx4 v[4:5], off
	v_lshl_add_u64 v[4:5], v[12:13], 0, s[24:25]
	s_mov_b32 m0, s60
	s_add_i32 s61, s47, 0xa000
	global_load_lds_dwordx4 v[4:5], off
	v_lshl_add_u64 v[4:5], v[14:15], 0, s[24:25]
	s_mov_b32 m0, s61
	s_add_i32 s62, s47, 0x1c000
	global_load_lds_dwordx4 v[4:5], off
	v_lshl_add_u64 v[4:5], v[8:9], 0, s[24:25]
	s_mov_b32 m0, s62
	s_add_i32 s63, s47, 0x1e000
	global_load_lds_dwordx4 v[4:5], off
	v_lshl_add_u64 v[4:5], v[10:11], 0, s[24:25]
	s_mov_b32 m0, s63
	s_lshr_b32 s7, s7, 26
	global_load_lds_dwordx4 v[4:5], off
	v_lshrrev_b32_e32 v5, 1, v2
	v_and_b32_e32 v5, 24, v5
	v_and_b32_e32 v4, 15, v2
	s_add_i32 s7, s6, s7
	v_lshlrev_b32_e32 v6, 1, v5
	v_lshlrev_b32_e32 v2, 2, v2
	s_and_b32 s14, s12, 3
	s_ashr_i32 s64, s7, 6
	v_lshl_or_b32 v6, v4, 6, v6
	s_lshl_b32 s7, s9, 13
	v_and_b32_e32 v2, 32, v2
	s_lshl_b32 s20, s9, 6
	v_bitop3_b32 v7, v6, s7, v2 bitop3:0xde
	s_lshl_b32 s7, s14, 12
	s_cmp_gt_i32 s6, 63
	v_bitop3_b32 v80, v6, s7, v2 bitop3:0xde
	s_cselect_b64 s[6:7], -1, 0
	s_add_i32 s65, s64, -2
	s_cmpk_lt_u32 s8, 0x100
	s_cselect_b64 s[8:9], -1, 0
	s_cmp_lt_u32 s14, 2
	s_cselect_b64 s[12:13], -1, 0
	v_lshl_or_b32 v2, s14, 5, v5
	s_ashr_i32 s14, s20, 31
	v_or_b32_e32 v4, s20, v4
	v_mov_b32_e32 v5, s14
	v_lshlrev_b64 v[4:5], 7, v[4:5]
	v_lshl_add_u64 v[4:5], s[36:37], 0, v[4:5]
	s_mov_b64 s[20:21], 0x5d088000
	v_lshl_add_u64 v[74:75], v[4:5], 0, s[20:21]
	v_lshlrev_b32_e32 v4, 12, v20
	v_and_b32_e32 v4, 0xffffe000, v4
	v_lshl_add_u32 v4, v19, 9, v4
	v_and_b32_e32 v5, 1, v20
	v_lshl_or_b32 v4, v5, 6, v4
	v_lshl_add_u32 v76, v21, 1, v4
	v_lshlrev_b32_e32 v4, 12, v16
	v_and_b32_e32 v4, 0xffffe000, v4
	s_waitcnt vmcnt(6)
	v_lshl_add_u32 v4, v17, 9, v4
	v_and_b32_e32 v5, 1, v16
	v_lshl_or_b32 v4, v5, 6, v4
	v_mov_b32_e32 v77, v3
	v_lshl_add_u32 v78, v18, 1, v4
	v_mov_b32_e32 v79, v3
	s_mov_b32 s66, 0
	v_add_u32_e32 v81, 0, v7
	v_lshlrev_b32_e32 v2, 1, v2
	s_mov_b32 s34, s46
	s_mov_b64 s[20:21], s[52:53]
	s_barrier
	s_branch .LBB0_1237
	.p2align	6
.LBB0_1235:
	s_mov_b64 s[28:29], 0
	.p2align	6

.LBB0_1239:
	s_and_b64 s[22:23], s[28:29], exec
	s_cselect_b32 s22, s67, s14
	s_ashr_i32 s23, s22, 31
	s_lshl_b64 s[22:23], s[22:23], 17
	s_add_u32 s22, s48, s22
	v_mov_b32_e32 v67, 0
	s_addc_u32 s23, s49, s23
	s_andn2_b64 vcc, exec, s[6:7]
	v_mov_b32_e32 v66, v67
	v_mov_b32_e32 v65, v67
	v_mov_b32_e32 v64, v67
	v_mov_b32_e32 v63, v67
	v_mov_b32_e32 v62, v67
	v_mov_b32_e32 v61, v67
	v_mov_b32_e32 v60, v67
	v_mov_b32_e32 v59, v67
	v_mov_b32_e32 v58, v67
	v_mov_b32_e32 v57, v67
	v_mov_b32_e32 v56, v67
	v_mov_b32_e32 v55, v67
	v_mov_b32_e32 v54, v67
	v_mov_b32_e32 v53, v67
	v_mov_b32_e32 v52, v67
	v_mov_b32_e32 v51, v67
	v_mov_b32_e32 v50, v67
	v_mov_b32_e32 v49, v67
	v_mov_b32_e32 v48, v67
	v_mov_b32_e32 v47, v67
	v_mov_b32_e32 v46, v67
	v_mov_b32_e32 v45, v67
	v_mov_b32_e32 v44, v67
	v_mov_b32_e32 v43, v67
	v_mov_b32_e32 v42, v67
	v_mov_b32_e32 v41, v67
	v_mov_b32_e32 v40, v67
	v_mov_b32_e32 v39, v67
	v_mov_b32_e32 v38, v67
	v_mov_b32_e32 v37, v67
	v_mov_b32_e32 v36, v67
	v_mov_b32_e32 v35, v67
	v_mov_b32_e32 v34, v67
	v_mov_b32_e32 v33, v67
	v_mov_b32_e32 v32, v67
	v_mov_b32_e32 v31, v67
	v_mov_b32_e32 v30, v67
	v_mov_b32_e32 v29, v67
	v_mov_b32_e32 v28, v67
	v_mov_b32_e32 v27, v67
	v_mov_b32_e32 v26, v67
	v_mov_b32_e32 v25, v67
	v_mov_b32_e32 v24, v67
	v_mov_b32_e32 v23, v67
	v_mov_b32_e32 v22, v67
	v_mov_b32_e32 v21, v67
	v_mov_b32_e32 v20, v67
	v_mov_b32_e32 v19, v67
	v_mov_b32_e32 v18, v67
	v_mov_b32_e32 v17, v67
	v_mov_b32_e32 v16, v67
	v_mov_b32_e32 v15, v67
	v_mov_b32_e32 v14, v67
	v_mov_b32_e32 v13, v67
	v_mov_b32_e32 v12, v67
	v_mov_b32_e32 v11, v67
	v_mov_b32_e32 v10, v67
	v_mov_b32_e32 v9, v67
	v_mov_b32_e32 v8, v67
	v_mov_b32_e32 v7, v67
	v_mov_b32_e32 v6, v67
	v_mov_b32_e32 v5, v67
	v_mov_b32_e32 v4, v67
	s_cbranch_vccz .LBB0_1243
	s_and_b64 vcc, exec, s[8:9]
	s_cbranch_vccnz .LBB0_1246
	.p2align	6
.LBB0_1241:
	s_andn2_b64 vcc, exec, s[12:13]
	s_cbranch_vccz .LBB0_1247
	.p2align	6

.LBB0_1243:
	s_and_b64 s[68:69], s[28:29], exec
	s_cselect_b32 s35, s23, s51
	s_cselect_b32 s68, s22, s50
	s_add_u32 s50, s50, 0x10080
	s_addc_u32 s51, s51, 0
	s_add_u32 s69, s52, 0x100
	v_mov_b32_e32 v4, 0
	s_addc_u32 s72, s53, 0
	s_mov_b32 s52, 0
	v_mov_b32_e32 v5, v4
	v_mov_b32_e32 v6, v4
	v_mov_b32_e32 v7, v4
	v_mov_b32_e32 v8, v4
	v_mov_b32_e32 v9, v4
	v_mov_b32_e32 v10, v4
	v_mov_b32_e32 v11, v4
	v_mov_b32_e32 v12, v4
	v_mov_b32_e32 v13, v4
	v_mov_b32_e32 v14, v4
	v_mov_b32_e32 v15, v4
	v_mov_b32_e32 v16, v4
	v_mov_b32_e32 v17, v4
	v_mov_b32_e32 v18, v4
	v_mov_b32_e32 v19, v4
	v_mov_b32_e32 v20, v4
	v_mov_b32_e32 v21, v4
	v_mov_b32_e32 v22, v4
	v_mov_b32_e32 v23, v4
	v_mov_b32_e32 v24, v4
	v_mov_b32_e32 v25, v4
	v_mov_b32_e32 v26, v4
	v_mov_b32_e32 v27, v4
	v_mov_b32_e32 v28, v4
	v_mov_b32_e32 v29, v4
	v_mov_b32_e32 v30, v4
	v_mov_b32_e32 v31, v4
	v_mov_b32_e32 v32, v4
	v_mov_b32_e32 v33, v4
	v_mov_b32_e32 v34, v4
	v_mov_b32_e32 v35, v4
	v_mov_b32_e32 v36, v4
	v_mov_b32_e32 v37, v4
	v_mov_b32_e32 v38, v4
	v_mov_b32_e32 v39, v4
	v_mov_b32_e32 v40, v4
	v_mov_b32_e32 v41, v4
	v_mov_b32_e32 v42, v4
	v_mov_b32_e32 v43, v4
	v_mov_b32_e32 v44, v4
	v_mov_b32_e32 v45, v4
	v_mov_b32_e32 v46, v4
	v_mov_b32_e32 v47, v4
	v_mov_b32_e32 v48, v4
	v_mov_b32_e32 v49, v4
	v_mov_b32_e32 v50, v4
	v_mov_b32_e32 v51, v4
	v_mov_b32_e32 v52, v4
	v_mov_b32_e32 v53, v4
	v_mov_b32_e32 v54, v4
	v_mov_b32_e32 v55, v4
	v_mov_b32_e32 v56, v4
	v_mov_b32_e32 v57, v4
	v_mov_b32_e32 v58, v4
	v_mov_b32_e32 v59, v4
	v_mov_b32_e32 v60, v4
	v_mov_b32_e32 v61, v4
	v_mov_b32_e32 v62, v4
	v_mov_b32_e32 v63, v4
	v_mov_b32_e32 v64, v4
	v_mov_b32_e32 v65, v4
	v_mov_b32_e32 v66, v4
	v_mov_b32_e32 v67, v4
	.p2align	6

.LBB0_1340:
	s_waitcnt vmcnt(1)
	v_mov_b32_e32 v14, v3
	v_mov_b32_e32 v15, v3
	v_mov_b32_e32 v48, v3
	v_mov_b32_e32 v49, v3
	s_waitcnt lgkmcnt(0)
	v_mov_b32_e32 v0, v3
	v_mov_b32_e32 v1, v3
	v_mov_b32_e32 v2, v3
	v_mov_b32_e32 v4, v3
	v_mov_b32_e32 v5, v3
	v_mov_b32_e32 v6, v3
	v_mov_b32_e32 v7, v3
	v_mov_b32_e32 v8, v3
	v_mov_b32_e32 v9, v3
	v_mov_b32_e32 v10, v3
	v_mov_b32_e32 v11, v3
	v_mov_b32_e32 v12, v3
	v_mov_b32_e32 v13, v3
	v_mov_b32_e32 v50, v3
	v_mov_b32_e32 v51, v3
	v_mov_b32_e32 v52, v3
	v_mov_b32_e32 v53, v3
	v_mov_b32_e32 v54, v3
	v_mov_b32_e32 v55, v3
	v_mov_b32_e32 v56, v3
	v_mov_b32_e32 v57, v3
	v_mov_b32_e32 v58, v3
	v_mov_b32_e32 v59, v3
	v_mov_b32_e32 v60, v3
	v_mov_b32_e32 v61, v3
	v_mov_b32_e32 v62, v3
	v_mov_b32_e32 v63, v3
	v_mov_b64_e32 v[16:17], v[48:49]
	v_mov_b64_e32 v[46:47], v[14:15]
	v_mov_b64_e32 v[18:19], v[50:51]
	v_mov_b64_e32 v[20:21], v[52:53]
	v_mov_b64_e32 v[22:23], v[54:55]
	v_mov_b64_e32 v[24:25], v[56:57]
	v_mov_b64_e32 v[26:27], v[58:59]
	v_mov_b64_e32 v[28:29], v[60:61]
	v_mov_b64_e32 v[30:31], v[62:63]
	v_mov_b64_e32 v[44:45], v[12:13]
	v_mov_b64_e32 v[42:43], v[10:11]
	v_mov_b64_e32 v[40:41], v[8:9]
	v_mov_b64_e32 v[38:39], v[6:7]
	v_mov_b64_e32 v[36:37], v[4:5]
	v_mov_b64_e32 v[34:35], v[2:3]
	v_mov_b64_e32 v[32:33], v[0:1]
	.p2align	6

.LBB0_1408:
	s_cmp_gt_u32 s21, 3
	s_mov_b32 s23, 0
	s_cselect_b64 s[4:5], -1, 0
	s_cmp_lt_u32 s21, 4
	s_mov_b32 s29, 0
	s_cbranch_scc0 .LBB0_1451
	s_cmp_lt_u32 s21, 5
	s_cbranch_scc0 .LBB0_1452
	.p2align	6
.LBB0_1410:
	s_cmp_lt_u32 s21, 6
	s_mov_b32 s48, 0
	s_cbranch_scc1 .LBB0_1412
	.p2align	6
.LBB0_1411:
	v_readlane_b32 s0, v254, 22
	s_nop 1
	v_mov_b32_e32 v2, s0
	ds_read_b32 v2, v2
	s_waitcnt lgkmcnt(0)
	v_readfirstlane_b32 s48, v2
	.p2align	6

.LBB0_1417:
	v_or_b32_e32 v17, v0, v1
	s_movk_i32 s5, 0x1001
	v_mul_u32_u24_sdwa v18, v17, s5 dst_sel:DWORD dst_unused:UNUSED_PAD src0_sel:BYTE_1 src1_sel:DWORD
	s_mov_b32 s5, 0x40040
	v_mul_u32_u24_sdwa v17, v17, s5 dst_sel:DWORD dst_unused:UNUSED_PAD src0_sel:BYTE_1 src1_sel:DWORD
	s_mov_b32 s6, 0x3030303
	s_movk_i32 s5, 0xff
	v_bitop3_b32 v17, v17, s6, v18 bitop3:0xc8
	v_bitop3_b32 v0, v0, s5, v1 bitop3:0xc8
	v_lshl_add_u32 v17, v17, 3, v17
	v_mul_u32_u24_e32 v1, 0x1001, v0
	v_mul_u32_u24_e32 v0, 0x40040, v0
	s_add_i32 s5, s30, 1
	v_and_b32_e32 v17, 0x11111111, v17
	v_bitop3_b32 v0, v0, s6, v1 bitop3:0xc8
	v_cvt_f32_ubyte0_e32 v1, s5
	v_mul_lo_u32 v107, v17, 15
	v_exp_f32_e64 v1, -v1
	v_or_b32_e32 v17, 32, v110
	v_cvt_f32_u32_e32 v17, v17
	v_lshl_add_u32 v0, v0, 3, v0
	v_and_b32_e32 v0, 0x11111111, v0
	v_mul_lo_u32 v106, v0, 15
	v_mul_f32_e32 v0, 0x3fb8aa3b, v1
	s_add_i32 s4, s21, 1
	v_and_b32_e32 v18, 31, v110
	v_and_b32_e32 v113, 0x7fff0000, v17
	v_and_b32_e32 v17, 0xffff0000, v0
	s_mov_b32 s5, 0x3fb8aa3b
	s_lshr_b32 s4, s4, 1
	v_cvt_f32_ubyte0_e32 v19, v18
	v_fma_f32 v1, v1, s5, -v17
	v_and_b32_e32 v112, 0x7fff0000, v19
	v_and_b32_e32 v19, 0xffff0000, v1
	s_add_u32 s46, s0, s10
	v_sub_f32_e32 v20, v1, v19
	v_or_b32_sdwa v0, v19, v0 dst_sel:DWORD dst_unused:UNUSED_PAD src0_sel:DWORD src1_sel:WORD_1
	v_cmp_gt_u32_e64 s[36:37], 32, v110
	s_addc_u32 s47, s1, 0
	v_readlane_b32 s0, v254, 36
	v_and_b32_e32 v21, 0xffff0000, v20
	v_cndmask_b32_e64 v100, 0, v0, s[36:37]
	v_or_b32_sdwa v0, v20, v17 dst_sel:DWORD dst_unused:UNUSED_PAD src0_sel:WORD_1 src1_sel:DWORD
	v_readlane_b32 s1, v254, 37
	s_add_u32 s0, s2, s0
	v_cndmask_b32_e64 v101, 0, v0, s[36:37]
	v_or_b32_sdwa v0, v21, v1 dst_sel:DWORD dst_unused:UNUSED_PAD src0_sel:DWORD src1_sel:WORD_1
	v_mov_b32_e32 v1, 0xffff
	s_addc_u32 s1, s3, 0
	v_cndmask_b32_e64 v102, 0, v0, s[36:37]
	v_ashrrev_i32_e32 v0, 5, v110
	v_cndmask_b32_e64 v114, 0, v1, s[36:37]
	v_cndmask_b32_e64 v1, 0, v112, s[36:37]
	v_cndmask_b32_e64 v17, 0, v113, s[36:37]
	v_lshl_add_u64 v[108:109], s[0:1], 0, v[2:3]
	s_movk_i32 s0, 0x410
	v_or_b32_sdwa v2, v1, v1 dst_sel:DWORD dst_unused:UNUSED_PAD src0_sel:WORD_1 src1_sel:DWORD
	v_or_b32_sdwa v116, v17, v17 dst_sel:DWORD dst_unused:UNUSED_PAD src0_sel:WORD_1 src1_sel:DWORD
	v_mul_lo_u32 v1, v0, s0
	v_lshlrev_b32_e32 v17, 4, v18
	v_add3_u32 v117, 0, v1, v17
	v_lshlrev_b32_e32 v1, 1, v110
	v_and_b32_e32 v1, 32, v1
	v_add3_u32 v1, s94, v1, v16
	v_lshlrev_b32_e32 v16, 4, v110
	v_lshlrev_b32_e32 v118, 2, v0
	v_lshlrev_b32_e32 v151, 4, v0
	v_lshlrev_b32_e32 v0, 8, v0
	v_and_b32_e32 v16, 0xc0, v16
	v_mov_b32_e32 v30, v3
	v_mov_b32_e32 v31, v3
	v_lshl_add_u32 v150, v18, 2, s33
	v_add3_u32 v152, v1, v0, v16
	v_mov_b32_e32 v16, v3
	v_mov_b32_e32 v17, v3
	v_mov_b32_e32 v18, v3
	v_mov_b32_e32 v19, v3
	v_mov_b32_e32 v20, v3
	v_mov_b32_e32 v21, v3
	v_mov_b32_e32 v22, v3
	v_mov_b32_e32 v23, v3
	v_mov_b32_e32 v24, v3
	v_mov_b32_e32 v25, v3
	v_mov_b32_e32 v26, v3
	v_mov_b32_e32 v27, v3
	v_mov_b32_e32 v28, v3
	v_mov_b32_e32 v29, v3
	v_mov_b64_e32 v[62:63], v[30:31]
	s_mov_b32 s5, 0
	v_mov_b32_e32 v103, v3
	v_add_u32_e32 v115, 0xc0000001, v104
	v_add_u32_e32 v119, 32, v118
	v_or_b32_e32 v120, 1, v118
	v_add_u32_e32 v121, 33, v118
	v_or_b32_e32 v122, 2, v118
	v_add_u32_e32 v123, 34, v118
	v_or_b32_e32 v124, 3, v118
	v_add_u32_e32 v125, 35, v118
	v_add_u32_e32 v126, 8, v118
	v_add_u32_e32 v127, 40, v118
	v_add_u32_e32 v128, 9, v118
	v_add_u32_e32 v129, 41, v118
	v_add_u32_e32 v130, 10, v118
	v_add_u32_e32 v131, 42, v118
	v_add_u32_e32 v132, 11, v118
	v_add_u32_e32 v133, 43, v118
	v_add_u32_e32 v134, 16, v118
	v_add_u32_e32 v135, 48, v118
	v_add_u32_e32 v136, 17, v118
	v_add_u32_e32 v137, 49, v118
	v_add_u32_e32 v138, 18, v118
	v_add_u32_e32 v139, 50, v118
	v_add_u32_e32 v140, 19, v118
	v_add_u32_e32 v141, 51, v118
	v_add_u32_e32 v142, 24, v118
	v_add_u32_e32 v143, 56, v118
	v_add_u32_e32 v144, 25, v118
	v_add_u32_e32 v145, 57, v118
	v_add_u32_e32 v146, 26, v118
	v_add_u32_e32 v147, 58, v118
	v_add_u32_e32 v148, 27, v118
	v_add_u32_e32 v149, 59, v118
	s_add_i32 s6, s4, -1
	v_mov_b32_e32 v32, v3
	v_mov_b32_e32 v33, v3
	v_mov_b32_e32 v34, v3
	v_mov_b32_e32 v35, v3
	v_mov_b32_e32 v36, v3
	v_mov_b32_e32 v37, v3
	v_mov_b32_e32 v38, v3
	v_mov_b32_e32 v39, v3
	v_mov_b32_e32 v40, v3
	v_mov_b32_e32 v41, v3
	v_mov_b32_e32 v42, v3
	v_mov_b32_e32 v43, v3
	v_mov_b32_e32 v44, v3
	v_mov_b32_e32 v45, v3
	v_mov_b32_e32 v46, v3
	v_mov_b32_e32 v47, v3
	v_mov_b32_e32 v153, 0
	s_mov_b64 s[38:39], -1
	s_mov_b32 s7, 7
	v_readlane_b32 s8, v254, 26
	v_mov_b64_e32 v[60:61], v[28:29]
	v_mov_b64_e32 v[58:59], v[26:27]
	v_mov_b64_e32 v[56:57], v[24:25]
	v_mov_b64_e32 v[54:55], v[22:23]
	v_mov_b64_e32 v[52:53], v[20:21]
	v_mov_b64_e32 v[50:51], v[18:19]
	v_mov_b64_e32 v[48:49], v[16:17]
	s_waitcnt vmcnt(0) lgkmcnt(0)
	s_barrier
	.p2align	6

.LBB0_1529:
	s_cmp_gt_u32 s7, 3
	s_mov_b32 s9, 0
	s_cselect_b64 s[0:1], -1, 0
	s_cmp_lt_u32 s7, 4
	s_mov_b32 s12, 0
	s_cbranch_scc0 .LBB0_1572
	s_cmp_lt_u32 s7, 5
	s_cbranch_scc0 .LBB0_1573
	.p2align	6
.LBB0_1531:
	s_cmp_lt_u32 s7, 6
	s_mov_b32 s13, 0
	s_cbranch_scc1 .LBB0_1533
	.p2align	6
.LBB0_1532:
	s_add_i32 s13, 0, 0x21c14
	v_mov_b32_e32 v2, s13
	ds_read_b32 v2, v2
	s_waitcnt lgkmcnt(0)
	v_readfirstlane_b32 s13, v2
	.p2align	6

.LBB0_1538:
	s_add_i32 s0, s7, 1
	s_lshr_b32 s4, s0, 1
	v_or_b32_e32 v17, v0, v1
	s_movk_i32 s0, 0x1001
	v_mul_u32_u24_sdwa v18, v17, s0 dst_sel:DWORD dst_unused:UNUSED_PAD src0_sel:BYTE_1 src1_sel:DWORD
	s_mov_b32 s0, 0x40040
	v_mul_u32_u24_sdwa v17, v17, s0 dst_sel:DWORD dst_unused:UNUSED_PAD src0_sel:BYTE_1 src1_sel:DWORD
	s_movk_i32 s0, 0xff
	v_bitop3_b32 v0, v0, s0, v1 bitop3:0xc8
	s_mov_b32 s1, 0x3030303
	v_mul_u32_u24_e32 v1, 0x1001, v0
	v_mul_u32_u24_e32 v0, 0x40040, v0
	v_bitop3_b32 v0, v0, s1, v1 bitop3:0xc8
	v_lshl_add_u32 v0, v0, 3, v0
	v_and_b32_e32 v0, 0x11111111, v0
	v_mul_lo_u32 v106, v0, 15
	v_or_b32_e32 v0, 32, v113
	v_cvt_f32_u32_e32 v0, v0
	v_bitop3_b32 v17, v17, s1, v18 bitop3:0xc8
	v_lshl_add_u32 v17, v17, 3, v17
	v_cmp_gt_u32_e64 s[36:37], 32, v113
	v_and_b32_e32 v116, 0x7fff0000, v0
	v_and_b32_e32 v17, 0x11111111, v17
	v_and_b32_e32 v1, 31, v113
	v_cndmask_b32_e64 v18, 0, v116, s[36:37]
	v_mul_lo_u32 v107, v17, 15
	v_cvt_f32_ubyte0_e32 v17, v1
	v_or_b32_sdwa v119, v18, v18 dst_sel:DWORD dst_unused:UNUSED_PAD src0_sel:WORD_1 src1_sel:DWORD
	v_lshlrev_b32_e32 v18, 4, v1
	v_lshl_add_u32 v153, v1, 2, s33
	v_lshlrev_b32_e32 v1, 1, v113
	v_and_b32_e32 v115, 0x7fff0000, v17
	v_mov_b32_e32 v17, 0xffff
	v_and_b32_e32 v1, 32, v1
	v_ashrrev_i32_e32 v0, 5, v113
	v_cndmask_b32_e64 v117, 0, v17, s[36:37]
	v_cndmask_b32_e64 v17, 0, v115, s[36:37]
	s_movk_i32 s0, 0x410
	v_add3_u32 v1, s94, v1, v16
	v_lshlrev_b32_e32 v16, 4, v113
	v_lshl_add_u64 v[108:109], s[82:83], 0, v[2:3]
	v_or_b32_sdwa v2, v17, v17 dst_sel:DWORD dst_unused:UNUSED_PAD src0_sel:WORD_1 src1_sel:DWORD
	v_mul_lo_u32 v17, v0, s0
	v_lshlrev_b32_e32 v121, 2, v0
	v_lshlrev_b32_e32 v154, 4, v0
	v_lshlrev_b32_e32 v0, 8, v0
	v_and_b32_e32 v16, 0xc0, v16
	v_mov_b32_e32 v30, v3
	v_mov_b32_e32 v31, v3
	v_add3_u32 v120, 0, v17, v18
	v_add3_u32 v155, v1, v0, v16
	v_mov_b32_e32 v16, v3
	v_mov_b32_e32 v17, v3
	v_mov_b32_e32 v18, v3
	v_mov_b32_e32 v19, v3
	v_mov_b32_e32 v20, v3
	v_mov_b32_e32 v21, v3
	v_mov_b32_e32 v22, v3
	v_mov_b32_e32 v23, v3
	v_mov_b32_e32 v24, v3
	v_mov_b32_e32 v25, v3
	v_mov_b32_e32 v26, v3
	v_mov_b32_e32 v27, v3
	v_mov_b32_e32 v28, v3
	v_mov_b32_e32 v29, v3
	v_mov_b64_e32 v[62:63], v[30:31]
	s_mov_b32 s5, 0
	v_cndmask_b32_e64 v100, 0, v110, s[36:37]
	v_cndmask_b32_e64 v101, 0, v111, s[36:37]
	v_cndmask_b32_e64 v102, 0, v112, s[36:37]
	v_mov_b32_e32 v103, v3
	v_add_u32_e32 v118, 0xc0000001, v104
	v_add_u32_e32 v122, 32, v121
	v_or_b32_e32 v123, 1, v121
	v_add_u32_e32 v124, 33, v121
	v_or_b32_e32 v125, 2, v121
	v_add_u32_e32 v126, 34, v121
	v_or_b32_e32 v127, 3, v121
	v_add_u32_e32 v128, 35, v121
	v_add_u32_e32 v129, 8, v121
	v_add_u32_e32 v130, 40, v121
	v_add_u32_e32 v131, 9, v121
	v_add_u32_e32 v132, 41, v121
	v_add_u32_e32 v133, 10, v121
	v_add_u32_e32 v134, 42, v121
	v_add_u32_e32 v135, 11, v121
	v_add_u32_e32 v136, 43, v121
	v_add_u32_e32 v137, 16, v121
	v_add_u32_e32 v138, 48, v121
	v_add_u32_e32 v139, 17, v121
	v_add_u32_e32 v140, 49, v121
	v_add_u32_e32 v141, 18, v121
	v_add_u32_e32 v142, 50, v121
	v_add_u32_e32 v143, 19, v121
	v_add_u32_e32 v144, 51, v121
	v_add_u32_e32 v145, 24, v121
	v_add_u32_e32 v146, 56, v121
	v_add_u32_e32 v147, 25, v121
	v_add_u32_e32 v148, 57, v121
	v_add_u32_e32 v149, 26, v121
	v_add_u32_e32 v150, 58, v121
	v_add_u32_e32 v151, 27, v121
	v_add_u32_e32 v152, 59, v121
	s_add_i32 s20, 0, 0x21c1c
	s_add_i32 s21, s4, -1
	v_mov_b32_e32 v32, v3
	v_mov_b32_e32 v33, v3
	v_mov_b32_e32 v34, v3
	v_mov_b32_e32 v35, v3
	v_mov_b32_e32 v36, v3
	v_mov_b32_e32 v37, v3
	v_mov_b32_e32 v38, v3
	v_mov_b32_e32 v39, v3
	v_mov_b32_e32 v40, v3
	v_mov_b32_e32 v41, v3
	v_mov_b32_e32 v42, v3
	v_mov_b32_e32 v43, v3
	v_mov_b32_e32 v44, v3
	v_mov_b32_e32 v45, v3
	v_mov_b32_e32 v46, v3
	v_mov_b32_e32 v47, v3
	v_mov_b32_e32 v156, 0
	s_mov_b64 s[38:39], -1
	s_mov_b32 s22, 7
	v_mov_b64_e32 v[60:61], v[28:29]
	v_mov_b64_e32 v[58:59], v[26:27]
	v_mov_b64_e32 v[56:57], v[24:25]
	v_mov_b64_e32 v[54:55], v[22:23]
	v_mov_b64_e32 v[52:53], v[20:21]
	v_mov_b64_e32 v[50:51], v[18:19]
	v_mov_b64_e32 v[48:49], v[16:17]
	s_waitcnt vmcnt(0) lgkmcnt(0)
	s_barrier
	.p2align	6

.LBB0_1587:
	ds_read_b128 v[4:7], v38
	ds_read_b128 v[20:23], v38 offset:512
	ds_read_b128 v[42:45], v38 offset:2080
	ds_read_b128 v[46:49], v38 offset:2592
	v_mov_b32_e32 v41, v124
	s_waitcnt lgkmcnt(3)
	v_mfma_f32_32x32x16_bf16 v[4:19], v[4:7], v[84:87], 0
	s_waitcnt lgkmcnt(2)
	v_mfma_f32_32x32x16_bf16 v[20:35], v[20:23], v[84:87], 0
	s_waitcnt lgkmcnt(1)
	v_mfma_f32_32x32x16_bf16 v[4:19], v[42:45], v[88:91], v[4:19]
	ds_read_b128 v[42:45], v38 offset:4160
	ds_read_b128 v[50:53], v38 offset:4672
	s_waitcnt lgkmcnt(2)
	v_mfma_f32_32x32x16_bf16 v[20:35], v[46:49], v[88:91], v[20:35]
	s_waitcnt lgkmcnt(1)
	v_mfma_f32_32x32x16_bf16 v[4:19], v[42:45], v[92:95], v[4:19]
	ds_read_b128 v[42:45], v38 offset:6240
	ds_read_b128 v[46:49], v38 offset:6752
	s_waitcnt lgkmcnt(2)
	v_mfma_f32_32x32x16_bf16 v[20:35], v[50:53], v[92:95], v[20:35]
	s_waitcnt lgkmcnt(1)
	v_mfma_f32_32x32x16_bf16 v[4:19], v[42:45], v[96:99], v[4:19]
	s_waitcnt lgkmcnt(0)
	v_mfma_f32_32x32x16_bf16 v[20:35], v[46:49], v[96:99], v[20:35]
	v_cmp_le_i32_e32 vcc, v71, v40
	s_add_i32 s0, s0, -1
	v_add_u32_e32 v38, 0x2080, v38
	s_nop 6
	v_cndmask_b32_e32 v2, v207, v4, vcc
	v_cmp_le_i32_e32 vcc, v72, v40
	s_cmp_eq_u32 s0, 0
	s_nop 0
	v_cndmask_b32_e32 v4, v207, v20, vcc
	v_cmp_lt_i32_e32 vcc, v71, v40
	s_nop 1
	v_cndmask_b32_e32 v20, v207, v5, vcc
	v_cmp_le_i32_e32 vcc, v73, v40
	v_max_f32_e32 v5, v20, v20
	s_nop 0
	v_cndmask_b32_e32 v21, v207, v21, vcc
	v_cmp_le_i32_e32 vcc, v74, v40
	s_nop 1
	v_cndmask_b32_e32 v6, v207, v6, vcc
	v_cmp_le_i32_e32 vcc, v75, v40
	s_nop 1
	v_cndmask_b32_e32 v22, v207, v22, vcc
	v_cmp_le_i32_e32 vcc, v76, v40
	s_nop 1
	v_cndmask_b32_e32 v42, v207, v7, vcc
	v_cmp_le_i32_e32 vcc, v77, v40
	v_max_f32_e32 v7, v2, v2
	v_max_f32_e32 v5, v7, v5
	v_cndmask_b32_e32 v23, v207, v23, vcc
	v_cmp_le_i32_e32 vcc, v78, v40
	v_max3_f32 v7, v6, v42, v21
	v_max3_f32 v5, v5, v4, v22
	v_cndmask_b32_e32 v8, v207, v8, vcc
	v_cmp_le_i32_e32 vcc, v79, v40
	v_max3_f32 v5, v5, v23, v8
	s_nop 0
	v_cndmask_b32_e32 v24, v207, v24, vcc
	v_cmp_le_i32_e32 vcc, v80, v40
	s_nop 1
	v_cndmask_b32_e32 v9, v207, v9, vcc
	v_cmp_le_i32_e32 vcc, v81, v40
	v_max3_f32 v5, v5, v9, v24
	s_nop 0
	v_cndmask_b32_e32 v25, v207, v25, vcc
	v_cmp_le_i32_e32 vcc, v82, v40
	s_nop 1
	v_cndmask_b32_e32 v10, v207, v10, vcc
	v_cmp_le_i32_e32 vcc, v83, v40
	s_nop 1
	v_cndmask_b32_e32 v26, v207, v26, vcc
	v_cmp_le_i32_e32 vcc, v100, v40
	s_nop 1
	v_cndmask_b32_e32 v11, v207, v11, vcc
	v_cmp_le_i32_e32 vcc, v101, v40
	v_max3_f32 v7, v7, v10, v11
	s_nop 0
	v_cndmask_b32_e32 v27, v207, v27, vcc
	v_cmp_le_i32_e32 vcc, v102, v40
	v_max3_f32 v7, v7, v26, v27
	s_nop 0
	v_cndmask_b32_e32 v12, v207, v12, vcc
	v_cmp_le_i32_e32 vcc, v103, v40
	v_max3_f32 v5, v5, v25, v12
	s_nop 0
	v_cndmask_b32_e32 v28, v207, v28, vcc
	v_cmp_le_i32_e32 vcc, v108, v40
	s_nop 1
	v_cndmask_b32_e32 v13, v207, v13, vcc
	v_cmp_le_i32_e32 vcc, v109, v40
	v_max3_f32 v5, v5, v13, v28
	s_nop 0
	v_cndmask_b32_e32 v29, v207, v29, vcc
	v_cmp_le_i32_e32 vcc, v110, v40
	s_nop 1
	v_cndmask_b32_e32 v14, v207, v14, vcc
	v_cmp_le_i32_e32 vcc, v111, v40
	s_nop 1
	v_cndmask_b32_e32 v30, v207, v30, vcc
	v_cmp_le_i32_e32 vcc, v114, v40
	s_nop 1
	v_cndmask_b32_e32 v15, v207, v15, vcc
	v_cmp_le_i32_e32 vcc, v115, v40
	v_max3_f32 v7, v7, v14, v15
	s_nop 0
	v_cndmask_b32_e32 v31, v207, v31, vcc
	v_cmp_le_i32_e32 vcc, v116, v40
	v_max3_f32 v7, v7, v30, v31
	s_nop 0
	v_cndmask_b32_e32 v16, v207, v16, vcc
	v_cmp_le_i32_e32 vcc, v117, v40
	v_max3_f32 v5, v5, v29, v16
	s_nop 0
	v_cndmask_b32_e32 v32, v207, v32, vcc
	v_cmp_le_i32_e32 vcc, v118, v40
	s_nop 1
	v_cndmask_b32_e32 v17, v207, v17, vcc
	v_cmp_le_i32_e32 vcc, v119, v40
	v_max3_f32 v5, v5, v17, v32
	s_nop 0
	v_cndmask_b32_e32 v33, v207, v33, vcc
	v_cmp_le_i32_e32 vcc, v120, v40
	s_nop 1
	v_cndmask_b32_e32 v18, v207, v18, vcc
	v_cmp_le_i32_e32 vcc, v121, v40
	s_nop 1
	v_cndmask_b32_e32 v34, v207, v34, vcc
	v_cmp_le_i32_e32 vcc, v122, v40
	s_nop 1
	v_cndmask_b32_e32 v19, v207, v19, vcc
	v_cmp_le_i32_e32 vcc, v123, v40
	v_max3_f32 v7, v7, v18, v19
	v_subrev_u32_e32 v40, 64, v40
	v_cndmask_b32_e32 v35, v207, v35, vcc
	v_max3_f32 v7, v7, v34, v35
	v_max3_f32 v5, v5, v33, v7
	v_mov_b32_e32 v7, v5
	s_nop 1
	v_permlane32_swap_b32_e32 v5, v7
	v_max3_f32 v124, v41, v5, v7
	v_sub_f32_e32 v2, v2, v124
	v_sub_f32_e32 v4, v4, v124
	v_exp_f32_e32 v2, v2
	v_exp_f32_e32 v4, v4
	s_nop 0
	v_add_f32_e32 v5, v2, v4
	v_sub_f32_e32 v2, v20, v124
	v_exp_f32_e32 v4, v2
	v_sub_f32_e32 v2, v21, v124
	v_exp_f32_e32 v2, v2
	s_nop 0
	v_pk_add_f32 v[4:5], v[4:5], v[2:3]
	s_nop 0
	v_pk_add_f32 v[4:5], v[4:5], v[4:5] op_sel_hi:[0,1]
	v_sub_f32_e32 v2, v6, v124
	v_sub_f32_e32 v4, v22, v124
	v_exp_f32_e32 v2, v2
	v_exp_f32_e32 v4, v4
	s_nop 0
	v_add_f32_e32 v7, v2, v4
	v_sub_f32_e32 v2, v42, v124
	v_exp_f32_e32 v6, v2
	v_sub_f32_e32 v2, v23, v124
	v_exp_f32_e32 v4, v2
	v_sub_f32_e32 v2, v8, v124
	v_exp_f32_e32 v2, v2
	v_pk_add_f32 v[4:5], v[6:7], v[4:5]
	s_nop 0
	v_pk_add_f32 v[4:5], v[4:5], v[4:5] op_sel_hi:[0,1]
	v_sub_f32_e32 v4, v24, v124
	v_exp_f32_e32 v4, v4
	s_nop 0
	v_add_f32_e32 v7, v2, v4
	v_sub_f32_e32 v2, v9, v124
	v_exp_f32_e32 v6, v2
	v_sub_f32_e32 v2, v25, v124
	v_exp_f32_e32 v4, v2
	v_sub_f32_e32 v2, v10, v124
	v_exp_f32_e32 v2, v2
	v_pk_add_f32 v[4:5], v[6:7], v[4:5]
	s_nop 0
	v_pk_add_f32 v[4:5], v[4:5], v[4:5] op_sel_hi:[0,1]
	v_sub_f32_e32 v4, v26, v124
	v_exp_f32_e32 v4, v4
	s_nop 0
	v_add_f32_e32 v7, v2, v4
	v_sub_f32_e32 v2, v11, v124
	v_exp_f32_e32 v6, v2
	v_sub_f32_e32 v2, v27, v124
	v_exp_f32_e32 v4, v2
	v_sub_f32_e32 v2, v12, v124
	v_exp_f32_e32 v2, v2
	v_pk_add_f32 v[4:5], v[6:7], v[4:5]
	s_nop 0
	v_pk_add_f32 v[4:5], v[4:5], v[4:5] op_sel_hi:[0,1]
	v_sub_f32_e32 v4, v28, v124
	v_exp_f32_e32 v4, v4
	s_nop 0
	v_add_f32_e32 v7, v2, v4
	v_sub_f32_e32 v2, v13, v124
	v_exp_f32_e32 v6, v2
	v_sub_f32_e32 v2, v29, v124
	v_exp_f32_e32 v4, v2
	v_sub_f32_e32 v2, v14, v124
	v_exp_f32_e32 v2, v2
	v_pk_add_f32 v[4:5], v[6:7], v[4:5]
	s_nop 0
	v_pk_add_f32 v[4:5], v[4:5], v[4:5] op_sel_hi:[0,1]
	v_sub_f32_e32 v4, v30, v124
	v_exp_f32_e32 v4, v4
	s_nop 0
	v_add_f32_e32 v7, v2, v4
	v_sub_f32_e32 v2, v15, v124
	v_exp_f32_e32 v6, v2
	v_sub_f32_e32 v2, v31, v124
	v_exp_f32_e32 v4, v2
	v_sub_f32_e32 v2, v16, v124
	v_exp_f32_e32 v2, v2
	v_pk_add_f32 v[4:5], v[6:7], v[4:5]
	s_nop 0
	v_pk_add_f32 v[4:5], v[4:5], v[4:5] op_sel_hi:[0,1]
	v_sub_f32_e32 v4, v32, v124
	v_exp_f32_e32 v4, v4
	s_nop 0
	v_add_f32_e32 v7, v2, v4
	v_sub_f32_e32 v2, v17, v124
	v_exp_f32_e32 v6, v2
	v_sub_f32_e32 v2, v33, v124
	v_exp_f32_e32 v4, v2
	v_sub_f32_e32 v2, v18, v124
	v_exp_f32_e32 v2, v2
	v_pk_add_f32 v[4:5], v[6:7], v[4:5]
	s_nop 0
	v_pk_add_f32 v[4:5], v[4:5], v[4:5] op_sel_hi:[0,1]
	v_sub_f32_e32 v4, v34, v124
	v_exp_f32_e32 v4, v4
	s_nop 0
	v_add_f32_e32 v7, v2, v4
	v_sub_f32_e32 v2, v19, v124
	v_exp_f32_e32 v6, v2
	v_sub_f32_e32 v2, v35, v124
	v_exp_f32_e32 v4, v2
	s_nop 0
	v_pk_add_f32 v[4:5], v[6:7], v[4:5]
	s_nop 0
	v_add_f32_e32 v2, v4, v5
	v_sub_f32_e32 v4, v41, v124
	v_exp_f32_e32 v4, v4
	v_mov_b32_e32 v5, v39
	v_mov_b32_e32 v39, v2
	v_fmac_f32_e32 v39, v5, v4
	s_cbranch_scc0 .LBB0_1587
	v_mov_b32_e32 v2, v39
	s_nop 1
	v_permlane32_swap_b32_e32 v39, v2
	v_add_f32_e32 v2, v39, v2
	v_div_scale_f32 v5, s[0:1], v2, v2, 1.0
	v_rcp_f32_e32 v6, v5
	v_lshlrev_b32_e32 v4, 3, v112
	v_and_b32_e32 v7, 24, v4
	v_mov_b32_e32 v4, 0
	v_fma_f32 v8, -v5, v6, 1.0
	v_fmac_f32_e32 v6, v8, v6
	v_div_scale_f32 v8, vcc, 1.0, v2, 1.0
	v_mul_f32_e32 v9, v8, v6
	v_fma_f32 v10, -v5, v9, v8
	v_fmac_f32_e32 v9, v10, v6
	v_fma_f32 v5, -v5, v9, v8
	v_div_fmas_f32 v5, v5, v6, v9
	v_div_fixup_f32 v5, v5, v2, 1.0
	v_cmp_lt_f32_e32 vcc, 0, v2
	v_lshlrev_b32_e32 v6, 4, v112
	v_and_b32_e32 v6, 0xc0, v6
	v_cndmask_b32_e32 v2, 0, v5, vcc
	v_lshlrev_b32_e32 v5, 1, v112
	v_and_b32_e32 v5, 32, v5
	v_lshl_or_b32 v6, v70, 8, v6
	s_movk_i32 s0, 0x104
	v_or3_b32 v125, v6, v5, v7
	v_subrev_u32_e32 v126, 49, v70
	v_mad_u32_u24 v127, v68, s0, v71
	v_add_u32_e32 v128, v36, v37
	v_mov_b32_e32 v5, v4
	v_mov_b32_e32 v6, v4
	v_mov_b32_e32 v7, v4
	v_mov_b32_e32 v8, v4
	v_mov_b32_e32 v9, v4
	v_mov_b32_e32 v10, v4
	v_mov_b32_e32 v11, v4
	v_mov_b32_e32 v12, v4
	v_mov_b32_e32 v13, v4
	v_mov_b32_e32 v14, v4
	v_mov_b32_e32 v15, v4
	v_mov_b32_e32 v16, v4
	v_mov_b32_e32 v17, v4
	v_mov_b32_e32 v18, v4
	v_mov_b32_e32 v19, v4
	v_mov_b32_e32 v20, v4
	v_mov_b32_e32 v21, v4
	v_mov_b32_e32 v22, v4
	v_mov_b32_e32 v23, v4
	v_mov_b32_e32 v24, v4
	v_mov_b32_e32 v25, v4
	v_mov_b32_e32 v26, v4
	v_mov_b32_e32 v27, v4
	v_mov_b32_e32 v28, v4
	v_mov_b32_e32 v29, v4
	v_mov_b32_e32 v30, v4
	v_mov_b32_e32 v31, v4
	v_mov_b32_e32 v32, v4
	v_mov_b32_e32 v33, v4
	v_mov_b32_e32 v34, v4
	v_mov_b32_e32 v35, v4
	s_branch .LBB0_1590
	.p2align	6

.LBB0_1669:
	v_mov_b32_e32 v1, s7
	s_waitcnt vmcnt(0) lgkmcnt(0)
	s_barrier
	ds_read_b32 v1, v1
	s_mov_b32 s7, 0
	s_andn2_b64 vcc, exec, s[4:5]
	s_mov_b32 s12, 0
	s_waitcnt lgkmcnt(0)
	v_readfirstlane_b32 s15, v1
	s_cbranch_vccz .LBB0_1758
	s_cmp_lt_u32 s6, 3
	s_cbranch_scc0 .LBB0_1759
	.p2align	6
.LBB0_1671:
	s_cmp_lt_u32 s6, 4
	s_mov_b32 s4, 0
	s_cbranch_scc1 .LBB0_1673
	.p2align	6
.LBB0_1672:
	v_readlane_b32 s4, v254, 20
	s_nop 1
	v_mov_b32_e32 v1, s4
	ds_read_b32 v1, v1
	s_waitcnt lgkmcnt(0)
	v_readfirstlane_b32 s4, v1
	.p2align	6
.LBB0_1673:
	v_or_b32_e32 v1, 32, v122
	v_cvt_f32_u32_e32 v1, v1
	s_add_i32 s5, s6, 1
	s_lshr_b32 s5, s5, 1
	v_cmp_gt_u32_e64 s[36:37], 32, v122
	v_and_b32_e32 v125, 0x7fff0000, v1
	s_add_u32 s50, s0, s10
	v_and_b32_e32 v4, 31, v122
	v_cndmask_b32_e64 v6, 0, v125, s[36:37]
	s_addc_u32 s51, s1, 0
	v_readlane_b32 s0, v254, 36
	v_cvt_f32_ubyte0_e32 v5, v4
	v_readlane_b32 s1, v254, 37
	s_add_u32 s0, s2, s0
	v_or_b32_sdwa v128, v6, v6 dst_sel:DWORD dst_unused:UNUSED_PAD src0_sel:WORD_1 src1_sel:DWORD
	v_lshlrev_b32_e32 v6, 4, v4
	v_lshl_add_u32 v162, v4, 2, s96
	v_lshlrev_b32_e32 v4, 1, v122
	v_and_b32_e32 v124, 0x7fff0000, v5
	v_mov_b32_e32 v5, 0xffff
	s_addc_u32 s1, s3, 0
	v_and_b32_e32 v4, 32, v4
	v_ashrrev_i32_e32 v1, 5, v122
	v_cndmask_b32_e64 v126, 0, v5, s[36:37]
	v_cndmask_b32_e64 v5, 0, v124, s[36:37]
	v_lshl_add_u64 v[110:111], s[0:1], 0, v[2:3]
	s_movk_i32 s0, 0x410
	v_add3_u32 v0, 0, v4, v0
	v_lshlrev_b32_e32 v4, 4, v122
	v_or_b32_sdwa v2, v5, v5 dst_sel:DWORD dst_unused:UNUSED_PAD src0_sel:WORD_1 src1_sel:DWORD
	v_mul_lo_u32 v5, v1, s0
	v_lshlrev_b32_e32 v130, 2, v1
	v_lshlrev_b32_e32 v163, 4, v1
	v_lshlrev_b32_e32 v1, 8, v1
	v_and_b32_e32 v4, 0xc0, v4
	v_mov_b32_e32 v18, v3
	v_mov_b32_e32 v19, v3
	v_add3_u32 v129, 0, v5, v6
	v_add3_u32 v164, v0, v1, v4
	v_mov_b32_e32 v4, v3
	v_mov_b32_e32 v5, v3
	v_mov_b32_e32 v6, v3
	v_mov_b32_e32 v7, v3
	v_mov_b32_e32 v8, v3
	v_mov_b32_e32 v9, v3
	v_mov_b32_e32 v10, v3
	v_mov_b32_e32 v11, v3
	v_mov_b32_e32 v12, v3
	v_mov_b32_e32 v13, v3
	v_mov_b32_e32 v14, v3
	v_mov_b32_e32 v15, v3
	v_mov_b32_e32 v16, v3
	v_mov_b32_e32 v17, v3
	v_mov_b64_e32 v[34:35], v[18:19]
	v_mov_b64_e32 v[50:51], v[18:19]
	v_cndmask_b32_e64 v100, 0, v120, s[36:37]
	v_cndmask_b32_e64 v101, 0, v104, s[36:37]
	v_cndmask_b32_e64 v102, 0, v121, s[36:37]
	v_mov_b32_e32 v103, v3
	s_mov_b32 s8, 5
	v_add_u32_e32 v127, 0xc0000001, v107
	v_add_u32_e32 v131, 32, v130
	v_or_b32_e32 v132, 1, v130
	v_add_u32_e32 v133, 33, v130
	v_or_b32_e32 v134, 2, v130
	v_add_u32_e32 v135, 34, v130
	v_or_b32_e32 v136, 3, v130
	v_add_u32_e32 v137, 35, v130
	v_add_u32_e32 v138, 8, v130
	v_add_u32_e32 v139, 40, v130
	v_add_u32_e32 v140, 9, v130
	v_add_u32_e32 v141, 41, v130
	v_add_u32_e32 v142, 10, v130
	v_add_u32_e32 v143, 42, v130
	v_add_u32_e32 v144, 11, v130
	v_add_u32_e32 v145, 43, v130
	v_add_u32_e32 v146, 16, v130
	v_add_u32_e32 v147, 48, v130
	v_add_u32_e32 v148, 17, v130
	v_add_u32_e32 v149, 49, v130
	v_add_u32_e32 v150, 18, v130
	v_add_u32_e32 v151, 50, v130
	v_add_u32_e32 v152, 19, v130
	v_add_u32_e32 v153, 51, v130
	v_add_u32_e32 v154, 24, v130
	v_add_u32_e32 v155, 56, v130
	v_add_u32_e32 v156, 25, v130
	v_add_u32_e32 v157, 57, v130
	v_add_u32_e32 v158, 26, v130
	v_add_u32_e32 v159, 58, v130
	v_add_u32_e32 v160, 27, v130
	v_add_u32_e32 v161, 59, v130
	s_add_i32 s9, 0, 0x21c14
	s_mov_b64 s[38:39], -1
	v_mov_b32_e32 v165, 0
	v_mov_b64_e32 v[32:33], v[16:17]
	v_mov_b64_e32 v[30:31], v[14:15]
	v_mov_b64_e32 v[28:29], v[12:13]
	v_mov_b64_e32 v[26:27], v[10:11]
	v_mov_b64_e32 v[24:25], v[8:9]
	v_mov_b64_e32 v[22:23], v[6:7]
	v_mov_b64_e32 v[20:21], v[4:5]
	v_mov_b64_e32 v[48:49], v[16:17]
	v_mov_b64_e32 v[46:47], v[14:15]
	v_mov_b64_e32 v[44:45], v[12:13]
	v_mov_b64_e32 v[42:43], v[10:11]
	v_mov_b64_e32 v[40:41], v[8:9]
	v_mov_b64_e32 v[38:39], v[6:7]
	v_mov_b64_e32 v[36:37], v[4:5]
	.p2align	6
.LBB0_1674:
	s_add_i32 s0, s8, -1
	s_and_b32 s13, s0, 2
	s_add_i32 s1, s8, -3
	s_cmp_ge_i32 s1, s6
	s_cbranch_scc0 .LBB0_1702
	s_add_i32 s1, s8, -2
	s_cmp_ge_i32 s1, s6
	s_cbranch_scc0 .LBB0_1703
	.p2align	6
.LBB0_1676:
	s_cmp_ge_i32 s0, s6
	v_mov_b32_e32 v166, 0
	v_mov_b32_e32 v167, 0
	s_cbranch_scc0 .LBB0_1704
	.p2align	6
.LBB0_1677:
	s_cmp_ge_i32 s8, s6
	s_cbranch_scc1 .LBB0_1679
	.p2align	6
.LBB0_1678:
	v_mov_b32_e32 v0, s9
	ds_read_b32 v166, v0
	.p2align	6

.LBB0_1723:
	v_or_b32_e32 v1, 32, v112
	v_cvt_f32_u32_e32 v1, v1
	s_add_i32 s5, s6, 1
	s_lshr_b32 s5, s5, 1
	v_cmp_gt_u32_e64 s[36:37], 32, v112
	v_and_b32_e32 v110, 0x7fff0000, v1
	s_add_u32 s50, s0, s10
	v_and_b32_e32 v4, 31, v112
	v_cndmask_b32_e64 v6, 0, v110, s[36:37]
	s_addc_u32 s51, s1, 0
	v_readlane_b32 s0, v254, 36
	v_cvt_f32_ubyte0_e32 v5, v4
	v_cndmask_b32_e64 v100, 0, v120, s[36:37]
	v_readlane_b32 s1, v254, 37
	s_add_u32 s0, s2, s0
	v_or_b32_sdwa v120, v6, v6 dst_sel:DWORD dst_unused:UNUSED_PAD src0_sel:WORD_1 src1_sel:DWORD
	v_lshlrev_b32_e32 v6, 4, v4
	v_lshl_add_u32 v154, v4, 2, s96
	v_lshlrev_b32_e32 v4, 1, v112
	v_and_b32_e32 v109, 0x7fff0000, v5
	v_mov_b32_e32 v5, 0xffff
	s_addc_u32 s1, s3, 0
	v_and_b32_e32 v4, 32, v4
	v_cndmask_b32_e64 v101, 0, v104, s[36:37]
	v_ashrrev_i32_e32 v1, 5, v112
	v_cndmask_b32_e64 v111, 0, v5, s[36:37]
	v_cndmask_b32_e64 v5, 0, v109, s[36:37]
	v_lshl_add_u64 v[104:105], s[0:1], 0, v[2:3]
	s_movk_i32 s0, 0x410
	v_add3_u32 v0, 0, v4, v0
	v_lshlrev_b32_e32 v4, 4, v112
	v_or_b32_sdwa v2, v5, v5 dst_sel:DWORD dst_unused:UNUSED_PAD src0_sel:WORD_1 src1_sel:DWORD
	v_mul_lo_u32 v5, v1, s0
	v_lshlrev_b32_e32 v122, 2, v1
	v_lshlrev_b32_e32 v155, 4, v1
	v_lshlrev_b32_e32 v1, 8, v1
	v_and_b32_e32 v4, 0xc0, v4
	v_mov_b32_e32 v18, v3
	v_mov_b32_e32 v19, v3
	v_cndmask_b32_e64 v102, 0, v121, s[36:37]
	v_add3_u32 v121, 0, v5, v6
	v_add3_u32 v156, v0, v1, v4
	v_mov_b32_e32 v4, v3
	v_mov_b32_e32 v5, v3
	v_mov_b32_e32 v6, v3
	v_mov_b32_e32 v7, v3
	v_mov_b32_e32 v8, v3
	v_mov_b32_e32 v9, v3
	v_mov_b32_e32 v10, v3
	v_mov_b32_e32 v11, v3
	v_mov_b32_e32 v12, v3
	v_mov_b32_e32 v13, v3
	v_mov_b32_e32 v14, v3
	v_mov_b32_e32 v15, v3
	v_mov_b32_e32 v16, v3
	v_mov_b32_e32 v17, v3
	v_mov_b64_e32 v[34:35], v[18:19]
	v_mov_b64_e32 v[50:51], v[18:19]
	v_mov_b32_e32 v103, v3
	s_mov_b32 s8, 5
	v_add_u32_e32 v113, 0xfffffe01, v107
	v_add_u32_e32 v123, 32, v122
	v_or_b32_e32 v124, 1, v122
	v_add_u32_e32 v125, 33, v122
	v_or_b32_e32 v126, 2, v122
	v_add_u32_e32 v127, 34, v122
	v_or_b32_e32 v128, 3, v122
	v_add_u32_e32 v129, 35, v122
	v_add_u32_e32 v130, 8, v122
	v_add_u32_e32 v131, 40, v122
	v_add_u32_e32 v132, 9, v122
	v_add_u32_e32 v133, 41, v122
	v_add_u32_e32 v134, 10, v122
	v_add_u32_e32 v135, 42, v122
	v_add_u32_e32 v136, 11, v122
	v_add_u32_e32 v137, 43, v122
	v_add_u32_e32 v138, 16, v122
	v_add_u32_e32 v139, 48, v122
	v_add_u32_e32 v140, 17, v122
	v_add_u32_e32 v141, 49, v122
	v_add_u32_e32 v142, 18, v122
	v_add_u32_e32 v143, 50, v122
	v_add_u32_e32 v144, 19, v122
	v_add_u32_e32 v145, 51, v122
	v_add_u32_e32 v146, 24, v122
	v_add_u32_e32 v147, 56, v122
	v_add_u32_e32 v148, 25, v122
	v_add_u32_e32 v149, 57, v122
	v_add_u32_e32 v150, 26, v122
	v_add_u32_e32 v151, 58, v122
	v_add_u32_e32 v152, 27, v122
	v_add_u32_e32 v153, 59, v122
	s_add_i32 s9, 0, 0x21c14
	s_mov_b64 s[38:39], -1
	v_mov_b32_e32 v157, 0
	v_mov_b64_e32 v[32:33], v[16:17]
	v_mov_b64_e32 v[30:31], v[14:15]
	v_mov_b64_e32 v[28:29], v[12:13]
	v_mov_b64_e32 v[26:27], v[10:11]
	v_mov_b64_e32 v[24:25], v[8:9]
	v_mov_b64_e32 v[22:23], v[6:7]
	v_mov_b64_e32 v[20:21], v[4:5]
	v_mov_b64_e32 v[48:49], v[16:17]
	v_mov_b64_e32 v[46:47], v[14:15]
	v_mov_b64_e32 v[44:45], v[12:13]
	v_mov_b64_e32 v[42:43], v[10:11]
	v_mov_b64_e32 v[40:41], v[8:9]
	v_mov_b64_e32 v[38:39], v[6:7]
	v_mov_b64_e32 v[36:37], v[4:5]
	.p2align	6

.LBB0_1726:
	s_cmp_ge_i32 s0, s6
	v_mov_b32_e32 v158, 0
	v_mov_b32_e32 v159, 0
	s_cbranch_scc0 .LBB0_1754
	.p2align	6

.LBB0_1728:
	v_mov_b32_e32 v0, s9
	ds_read_b32 v158, v0
	.p2align	6

.LBB0_1779:
	ds_read_b128 v[4:7], v38
	ds_read_b128 v[20:23], v38 offset:512
	ds_read_b128 v[42:45], v38 offset:2080
	ds_read_b128 v[46:49], v38 offset:2592
	v_mov_b32_e32 v41, v127
	s_waitcnt lgkmcnt(3)
	v_mfma_f32_32x32x16_bf16 v[4:19], v[4:7], v[84:87], 0
	s_waitcnt lgkmcnt(2)
	v_mfma_f32_32x32x16_bf16 v[20:35], v[20:23], v[84:87], 0
	s_waitcnt lgkmcnt(1)
	v_mfma_f32_32x32x16_bf16 v[4:19], v[42:45], v[88:91], v[4:19]
	ds_read_b128 v[42:45], v38 offset:4160
	ds_read_b128 v[50:53], v38 offset:4672
	s_waitcnt lgkmcnt(2)
	v_mfma_f32_32x32x16_bf16 v[20:35], v[46:49], v[88:91], v[20:35]
	s_waitcnt lgkmcnt(1)
	v_mfma_f32_32x32x16_bf16 v[4:19], v[42:45], v[92:95], v[4:19]
	ds_read_b128 v[42:45], v38 offset:6240
	ds_read_b128 v[46:49], v38 offset:6752
	s_waitcnt lgkmcnt(2)
	v_mfma_f32_32x32x16_bf16 v[20:35], v[50:53], v[92:95], v[20:35]
	s_waitcnt lgkmcnt(1)
	v_mfma_f32_32x32x16_bf16 v[4:19], v[42:45], v[96:99], v[4:19]
	s_waitcnt lgkmcnt(0)
	v_mfma_f32_32x32x16_bf16 v[20:35], v[46:49], v[96:99], v[20:35]
	v_cmp_le_i32_e32 vcc, v71, v40
	s_add_i32 s0, s0, -1
	v_add_u32_e32 v38, 0x2080, v38
	s_nop 6
	v_cndmask_b32_e32 v2, v207, v4, vcc
	v_cmp_le_i32_e32 vcc, v72, v40
	s_cmp_eq_u32 s0, 0
	s_nop 0
	v_cndmask_b32_e32 v4, v207, v20, vcc
	v_cmp_lt_i32_e32 vcc, v71, v40
	s_nop 1
	v_cndmask_b32_e32 v20, v207, v5, vcc
	v_cmp_le_i32_e32 vcc, v73, v40
	v_max_f32_e32 v5, v20, v20
	s_nop 0
	v_cndmask_b32_e32 v21, v207, v21, vcc
	v_cmp_le_i32_e32 vcc, v74, v40
	s_nop 1
	v_cndmask_b32_e32 v6, v207, v6, vcc
	v_cmp_le_i32_e32 vcc, v75, v40
	s_nop 1
	v_cndmask_b32_e32 v22, v207, v22, vcc
	v_cmp_le_i32_e32 vcc, v76, v40
	s_nop 1
	v_cndmask_b32_e32 v42, v207, v7, vcc
	v_cmp_le_i32_e32 vcc, v77, v40
	v_max_f32_e32 v7, v2, v2
	v_max_f32_e32 v5, v7, v5
	v_cndmask_b32_e32 v23, v207, v23, vcc
	v_cmp_le_i32_e32 vcc, v78, v40
	v_max3_f32 v7, v6, v42, v21
	v_max3_f32 v5, v5, v4, v22
	v_cndmask_b32_e32 v8, v207, v8, vcc
	v_cmp_le_i32_e32 vcc, v79, v40
	v_max3_f32 v5, v5, v23, v8
	s_nop 0
	v_cndmask_b32_e32 v24, v207, v24, vcc
	v_cmp_le_i32_e32 vcc, v80, v40
	s_nop 1
	v_cndmask_b32_e32 v9, v207, v9, vcc
	v_cmp_le_i32_e32 vcc, v81, v40
	v_max3_f32 v5, v5, v9, v24
	s_nop 0
	v_cndmask_b32_e32 v25, v207, v25, vcc
	v_cmp_le_i32_e32 vcc, v82, v40
	s_nop 1
	v_cndmask_b32_e32 v10, v207, v10, vcc
	v_cmp_le_i32_e32 vcc, v83, v40
	s_nop 1
	v_cndmask_b32_e32 v26, v207, v26, vcc
	v_cmp_le_i32_e32 vcc, v100, v40
	s_nop 1
	v_cndmask_b32_e32 v11, v207, v11, vcc
	v_cmp_le_i32_e32 vcc, v101, v40
	v_max3_f32 v7, v7, v10, v11
	s_nop 0
	v_cndmask_b32_e32 v27, v207, v27, vcc
	v_cmp_le_i32_e32 vcc, v102, v40
	v_max3_f32 v7, v7, v26, v27
	s_nop 0
	v_cndmask_b32_e32 v12, v207, v12, vcc
	v_cmp_le_i32_e32 vcc, v103, v40
	v_max3_f32 v5, v5, v25, v12
	s_nop 0
	v_cndmask_b32_e32 v28, v207, v28, vcc
	v_cmp_le_i32_e32 vcc, v110, v40
	s_nop 1
	v_cndmask_b32_e32 v13, v207, v13, vcc
	v_cmp_le_i32_e32 vcc, v111, v40
	v_max3_f32 v5, v5, v13, v28
	s_nop 0
	v_cndmask_b32_e32 v29, v207, v29, vcc
	v_cmp_le_i32_e32 vcc, v112, v40
	s_nop 1
	v_cndmask_b32_e32 v14, v207, v14, vcc
	v_cmp_le_i32_e32 vcc, v113, v40
	s_nop 1
	v_cndmask_b32_e32 v30, v207, v30, vcc
	v_cmp_le_i32_e32 vcc, v117, v40
	s_nop 1
	v_cndmask_b32_e32 v15, v207, v15, vcc
	v_cmp_le_i32_e32 vcc, v118, v40
	v_max3_f32 v7, v7, v14, v15
	s_nop 0
	v_cndmask_b32_e32 v31, v207, v31, vcc
	v_cmp_le_i32_e32 vcc, v119, v40
	v_max3_f32 v7, v7, v30, v31
	s_nop 0
	v_cndmask_b32_e32 v16, v207, v16, vcc
	v_cmp_le_i32_e32 vcc, v120, v40
	v_max3_f32 v5, v5, v29, v16
	s_nop 0
	v_cndmask_b32_e32 v32, v207, v32, vcc
	v_cmp_le_i32_e32 vcc, v121, v40
	s_nop 1
	v_cndmask_b32_e32 v17, v207, v17, vcc
	v_cmp_le_i32_e32 vcc, v122, v40
	v_max3_f32 v5, v5, v17, v32
	s_nop 0
	v_cndmask_b32_e32 v33, v207, v33, vcc
	v_cmp_le_i32_e32 vcc, v123, v40
	s_nop 1
	v_cndmask_b32_e32 v18, v207, v18, vcc
	v_cmp_le_i32_e32 vcc, v124, v40
	s_nop 1
	v_cndmask_b32_e32 v34, v207, v34, vcc
	v_cmp_le_i32_e32 vcc, v125, v40
	s_nop 1
	v_cndmask_b32_e32 v19, v207, v19, vcc
	v_cmp_le_i32_e32 vcc, v126, v40
	v_max3_f32 v7, v7, v18, v19
	v_subrev_u32_e32 v40, 64, v40
	v_cndmask_b32_e32 v35, v207, v35, vcc
	v_max3_f32 v7, v7, v34, v35
	v_max3_f32 v5, v5, v33, v7
	v_mov_b32_e32 v7, v5
	s_nop 1
	v_permlane32_swap_b32_e32 v5, v7
	v_max3_f32 v127, v41, v5, v7
	v_sub_f32_e32 v2, v2, v127
	v_sub_f32_e32 v4, v4, v127
	v_exp_f32_e32 v2, v2
	v_exp_f32_e32 v4, v4
	s_nop 0
	v_add_f32_e32 v5, v2, v4
	v_sub_f32_e32 v2, v20, v127
	v_exp_f32_e32 v4, v2
	v_sub_f32_e32 v2, v21, v127
	v_exp_f32_e32 v2, v2
	s_nop 0
	v_pk_add_f32 v[4:5], v[4:5], v[2:3]
	s_nop 0
	v_pk_add_f32 v[4:5], v[4:5], v[4:5] op_sel_hi:[0,1]
	v_sub_f32_e32 v2, v6, v127
	v_sub_f32_e32 v4, v22, v127
	v_exp_f32_e32 v2, v2
	v_exp_f32_e32 v4, v4
	s_nop 0
	v_add_f32_e32 v7, v2, v4
	v_sub_f32_e32 v2, v42, v127
	v_exp_f32_e32 v6, v2
	v_sub_f32_e32 v2, v23, v127
	v_exp_f32_e32 v4, v2
	v_sub_f32_e32 v2, v8, v127
	v_exp_f32_e32 v2, v2
	v_pk_add_f32 v[4:5], v[6:7], v[4:5]
	s_nop 0
	v_pk_add_f32 v[4:5], v[4:5], v[4:5] op_sel_hi:[0,1]
	v_sub_f32_e32 v4, v24, v127
	v_exp_f32_e32 v4, v4
	s_nop 0
	v_add_f32_e32 v7, v2, v4
	v_sub_f32_e32 v2, v9, v127
	v_exp_f32_e32 v6, v2
	v_sub_f32_e32 v2, v25, v127
	v_exp_f32_e32 v4, v2
	v_sub_f32_e32 v2, v10, v127
	v_exp_f32_e32 v2, v2
	v_pk_add_f32 v[4:5], v[6:7], v[4:5]
	s_nop 0
	v_pk_add_f32 v[4:5], v[4:5], v[4:5] op_sel_hi:[0,1]
	v_sub_f32_e32 v4, v26, v127
	v_exp_f32_e32 v4, v4
	s_nop 0
	v_add_f32_e32 v7, v2, v4
	v_sub_f32_e32 v2, v11, v127
	v_exp_f32_e32 v6, v2
	v_sub_f32_e32 v2, v27, v127
	v_exp_f32_e32 v4, v2
	v_sub_f32_e32 v2, v12, v127
	v_exp_f32_e32 v2, v2
	v_pk_add_f32 v[4:5], v[6:7], v[4:5]
	s_nop 0
	v_pk_add_f32 v[4:5], v[4:5], v[4:5] op_sel_hi:[0,1]
	v_sub_f32_e32 v4, v28, v127
	v_exp_f32_e32 v4, v4
	s_nop 0
	v_add_f32_e32 v7, v2, v4
	v_sub_f32_e32 v2, v13, v127
	v_exp_f32_e32 v6, v2
	v_sub_f32_e32 v2, v29, v127
	v_exp_f32_e32 v4, v2
	v_sub_f32_e32 v2, v14, v127
	v_exp_f32_e32 v2, v2
	v_pk_add_f32 v[4:5], v[6:7], v[4:5]
	s_nop 0
	v_pk_add_f32 v[4:5], v[4:5], v[4:5] op_sel_hi:[0,1]
	v_sub_f32_e32 v4, v30, v127
	v_exp_f32_e32 v4, v4
	s_nop 0
	v_add_f32_e32 v7, v2, v4
	v_sub_f32_e32 v2, v15, v127
	v_exp_f32_e32 v6, v2
	v_sub_f32_e32 v2, v31, v127
	v_exp_f32_e32 v4, v2
	v_sub_f32_e32 v2, v16, v127
	v_exp_f32_e32 v2, v2
	v_pk_add_f32 v[4:5], v[6:7], v[4:5]
	s_nop 0
	v_pk_add_f32 v[4:5], v[4:5], v[4:5] op_sel_hi:[0,1]
	v_sub_f32_e32 v4, v32, v127
	v_exp_f32_e32 v4, v4
	s_nop 0
	v_add_f32_e32 v7, v2, v4
	v_sub_f32_e32 v2, v17, v127
	v_exp_f32_e32 v6, v2
	v_sub_f32_e32 v2, v33, v127
	v_exp_f32_e32 v4, v2
	v_sub_f32_e32 v2, v18, v127
	v_exp_f32_e32 v2, v2
	v_pk_add_f32 v[4:5], v[6:7], v[4:5]
	s_nop 0
	v_pk_add_f32 v[4:5], v[4:5], v[4:5] op_sel_hi:[0,1]
	v_sub_f32_e32 v4, v34, v127
	v_exp_f32_e32 v4, v4
	s_nop 0
	v_add_f32_e32 v7, v2, v4
	v_sub_f32_e32 v2, v19, v127
	v_exp_f32_e32 v6, v2
	v_sub_f32_e32 v2, v35, v127
	v_exp_f32_e32 v4, v2
	s_nop 0
	v_pk_add_f32 v[4:5], v[6:7], v[4:5]
	s_nop 0
	v_add_f32_e32 v2, v4, v5
	v_sub_f32_e32 v4, v41, v127
	v_exp_f32_e32 v4, v4
	v_mov_b32_e32 v5, v39
	v_mov_b32_e32 v39, v2
	v_fmac_f32_e32 v39, v5, v4
	s_cbranch_scc0 .LBB0_1779
	v_mov_b32_e32 v2, v39
	s_nop 1
	v_permlane32_swap_b32_e32 v39, v2
	v_add_f32_e32 v2, v39, v2
	v_div_scale_f32 v5, s[0:1], v2, v2, 1.0
	v_rcp_f32_e32 v6, v5
	v_lshlrev_b32_e32 v4, 3, v109
	v_and_b32_e32 v7, 24, v4
	v_mov_b32_e32 v4, 0
	v_fma_f32 v8, -v5, v6, 1.0
	v_fmac_f32_e32 v6, v8, v6
	v_div_scale_f32 v8, vcc, 1.0, v2, 1.0
	v_mul_f32_e32 v9, v8, v6
	v_fma_f32 v10, -v5, v9, v8
	v_fmac_f32_e32 v9, v10, v6
	v_fma_f32 v5, -v5, v9, v8
	v_div_fmas_f32 v5, v5, v6, v9
	v_div_fixup_f32 v5, v5, v2, 1.0
	v_cmp_lt_f32_e32 vcc, 0, v2
	v_lshlrev_b32_e32 v6, 4, v109
	v_and_b32_e32 v6, 0xc0, v6
	v_cndmask_b32_e32 v2, 0, v5, vcc
	v_lshlrev_b32_e32 v5, 1, v109
	v_and_b32_e32 v5, 32, v5
	v_lshl_or_b32 v6, v70, 8, v6
	s_movk_i32 s0, 0x104
	v_or3_b32 v128, v6, v5, v7
	v_subrev_u32_e32 v129, 49, v70
	v_mad_u32_u24 v130, v68, s0, v71
	v_add_u32_e32 v131, v36, v37
	v_mov_b32_e32 v5, v4
	v_mov_b32_e32 v6, v4
	v_mov_b32_e32 v7, v4
	v_mov_b32_e32 v8, v4
	v_mov_b32_e32 v9, v4
	v_mov_b32_e32 v10, v4
	v_mov_b32_e32 v11, v4
	v_mov_b32_e32 v12, v4
	v_mov_b32_e32 v13, v4
	v_mov_b32_e32 v14, v4
	v_mov_b32_e32 v15, v4
	v_mov_b32_e32 v16, v4
	v_mov_b32_e32 v17, v4
	v_mov_b32_e32 v18, v4
	v_mov_b32_e32 v19, v4
	v_mov_b32_e32 v20, v4
	v_mov_b32_e32 v21, v4
	v_mov_b32_e32 v22, v4
	v_mov_b32_e32 v23, v4
	v_mov_b32_e32 v24, v4
	v_mov_b32_e32 v25, v4
	v_mov_b32_e32 v26, v4
	v_mov_b32_e32 v27, v4
	v_mov_b32_e32 v28, v4
	v_mov_b32_e32 v29, v4
	v_mov_b32_e32 v30, v4
	v_mov_b32_e32 v31, v4
	v_mov_b32_e32 v32, v4
	v_mov_b32_e32 v33, v4
	v_mov_b32_e32 v34, v4
	v_mov_b32_e32 v35, v4
	s_branch .LBB0_1782
	.p2align	6

.LBB0_1861:
	v_mov_b32_e32 v1, s2
	s_waitcnt vmcnt(0) lgkmcnt(0)
	s_barrier
	ds_read_b32 v1, v1
	s_mov_b32 s5, 0
	s_andn2_b64 vcc, exec, s[0:1]
	s_mov_b32 s12, 0
	s_waitcnt lgkmcnt(0)
	v_readfirstlane_b32 s2, v1
	s_cbranch_vccz .LBB0_1950
	s_cmp_lt_u32 s4, 3
	s_cbranch_scc0 .LBB0_1951
	.p2align	6
.LBB0_1863:
	s_cmp_lt_u32 s4, 4
	s_mov_b32 s6, 0
	s_cbranch_scc1 .LBB0_1865
	.p2align	6
.LBB0_1864:
	v_readlane_b32 s0, v254, 20
	s_nop 1
	v_mov_b32_e32 v1, s0
	ds_read_b32 v1, v1
	s_waitcnt lgkmcnt(0)
	v_readfirstlane_b32 s6, v1
	.p2align	6
.LBB0_1865:
	v_or_b32_e32 v1, 32, v104
	v_cvt_f32_u32_e32 v1, v1
	v_cmp_gt_u32_e64 s[36:37], 32, v104
	v_and_b32_e32 v4, 31, v104
	v_cvt_f32_ubyte0_e32 v5, v4
	v_and_b32_e32 v125, 0x7fff0000, v1
	v_cndmask_b32_e64 v6, 0, v125, s[36:37]
	v_or_b32_sdwa v128, v6, v6 dst_sel:DWORD dst_unused:UNUSED_PAD src0_sel:WORD_1 src1_sel:DWORD
	v_lshlrev_b32_e32 v6, 4, v4
	v_lshl_add_u32 v162, v4, 2, s96
	v_lshlrev_b32_e32 v4, 1, v104
	s_add_i32 s0, s4, 1
	v_and_b32_e32 v124, 0x7fff0000, v5
	v_mov_b32_e32 v5, 0xffff
	v_and_b32_e32 v4, 32, v4
	s_lshr_b32 s7, s0, 1
	v_ashrrev_i32_e32 v1, 5, v104
	v_cndmask_b32_e64 v126, 0, v5, s[36:37]
	v_cndmask_b32_e64 v5, 0, v124, s[36:37]
	s_movk_i32 s0, 0x410
	v_add3_u32 v0, 0, v4, v0
	v_lshlrev_b32_e32 v4, 4, v104
	v_lshl_add_u64 v[112:113], s[50:51], 0, v[2:3]
	v_or_b32_sdwa v2, v5, v5 dst_sel:DWORD dst_unused:UNUSED_PAD src0_sel:WORD_1 src1_sel:DWORD
	v_mul_lo_u32 v5, v1, s0
	v_lshlrev_b32_e32 v130, 2, v1
	v_lshlrev_b32_e32 v163, 4, v1
	v_lshlrev_b32_e32 v1, 8, v1
	v_and_b32_e32 v4, 0xc0, v4
	v_mov_b32_e32 v18, v3
	v_mov_b32_e32 v19, v3
	v_add3_u32 v129, 0, v5, v6
	v_add3_u32 v164, v0, v1, v4
	v_mov_b32_e32 v4, v3
	v_mov_b32_e32 v5, v3
	v_mov_b32_e32 v6, v3
	v_mov_b32_e32 v7, v3
	v_mov_b32_e32 v8, v3
	v_mov_b32_e32 v9, v3
	v_mov_b32_e32 v10, v3
	v_mov_b32_e32 v11, v3
	v_mov_b32_e32 v12, v3
	v_mov_b32_e32 v13, v3
	v_mov_b32_e32 v14, v3
	v_mov_b32_e32 v15, v3
	v_mov_b32_e32 v16, v3
	v_mov_b32_e32 v17, v3
	v_mov_b64_e32 v[34:35], v[18:19]
	v_mov_b64_e32 v[50:51], v[18:19]
	v_cndmask_b32_e64 v100, 0, v107, s[36:37]
	v_cndmask_b32_e64 v101, 0, v114, s[36:37]
	v_cndmask_b32_e64 v102, 0, v115, s[36:37]
	v_mov_b32_e32 v103, v3
	s_mov_b32 s8, 5
	v_add_u32_e32 v127, 0xc0000001, v108
	v_add_u32_e32 v131, 32, v130
	v_or_b32_e32 v132, 1, v130
	v_add_u32_e32 v133, 33, v130
	v_or_b32_e32 v134, 2, v130
	v_add_u32_e32 v135, 34, v130
	v_or_b32_e32 v136, 3, v130
	v_add_u32_e32 v137, 35, v130
	v_add_u32_e32 v138, 8, v130
	v_add_u32_e32 v139, 40, v130
	v_add_u32_e32 v140, 9, v130
	v_add_u32_e32 v141, 41, v130
	v_add_u32_e32 v142, 10, v130
	v_add_u32_e32 v143, 42, v130
	v_add_u32_e32 v144, 11, v130
	v_add_u32_e32 v145, 43, v130
	v_add_u32_e32 v146, 16, v130
	v_add_u32_e32 v147, 48, v130
	v_add_u32_e32 v148, 17, v130
	v_add_u32_e32 v149, 49, v130
	v_add_u32_e32 v150, 18, v130
	v_add_u32_e32 v151, 50, v130
	v_add_u32_e32 v152, 19, v130
	v_add_u32_e32 v153, 51, v130
	v_add_u32_e32 v154, 24, v130
	v_add_u32_e32 v155, 56, v130
	v_add_u32_e32 v156, 25, v130
	v_add_u32_e32 v157, 57, v130
	v_add_u32_e32 v158, 26, v130
	v_add_u32_e32 v159, 58, v130
	v_add_u32_e32 v160, 27, v130
	v_add_u32_e32 v161, 59, v130
	s_add_i32 s9, 0, 0x21c14
	s_mov_b64 s[38:39], -1
	v_mov_b32_e32 v165, 0
	v_mov_b64_e32 v[32:33], v[16:17]
	v_mov_b64_e32 v[30:31], v[14:15]
	v_mov_b64_e32 v[28:29], v[12:13]
	v_mov_b64_e32 v[26:27], v[10:11]
	v_mov_b64_e32 v[24:25], v[8:9]
	v_mov_b64_e32 v[22:23], v[6:7]
	v_mov_b64_e32 v[20:21], v[4:5]
	v_mov_b64_e32 v[48:49], v[16:17]
	v_mov_b64_e32 v[46:47], v[14:15]
	v_mov_b64_e32 v[44:45], v[12:13]
	v_mov_b64_e32 v[42:43], v[10:11]
	v_mov_b64_e32 v[40:41], v[8:9]
	v_mov_b64_e32 v[38:39], v[6:7]
	v_mov_b64_e32 v[36:37], v[4:5]
	.p2align	6
.LBB0_1866:
	s_add_i32 s0, s8, -1
	s_and_b32 s13, s0, 2
	s_add_i32 s1, s8, -3
	s_cmp_ge_i32 s1, s4
	s_cbranch_scc0 .LBB0_1894
	s_add_i32 s1, s8, -2
	s_cmp_ge_i32 s1, s4
	s_cbranch_scc0 .LBB0_1895
	.p2align	6
.LBB0_1868:
	s_cmp_ge_i32 s0, s4
	v_mov_b32_e32 v166, 0
	v_mov_b32_e32 v167, 0
	s_cbranch_scc0 .LBB0_1896
	.p2align	6
.LBB0_1869:
	s_cmp_ge_i32 s8, s4
	s_cbranch_scc1 .LBB0_1871
	.p2align	6

.LBB0_1915:
	v_or_b32_e32 v1, 32, v109
	v_cvt_f32_u32_e32 v1, v1
	v_cmp_gt_u32_e64 s[36:37], 32, v109
	v_and_b32_e32 v4, 31, v109
	v_cvt_f32_ubyte0_e32 v5, v4
	v_and_b32_e32 v112, 0x7fff0000, v1
	v_cndmask_b32_e64 v6, 0, v112, s[36:37]
	v_or_b32_sdwa v123, v6, v6 dst_sel:DWORD dst_unused:UNUSED_PAD src0_sel:WORD_1 src1_sel:DWORD
	v_lshlrev_b32_e32 v6, 4, v4
	v_lshl_add_u32 v157, v4, 2, s96
	v_lshlrev_b32_e32 v4, 1, v109
	s_add_i32 s0, s4, 1
	v_and_b32_e32 v111, 0x7fff0000, v5
	v_mov_b32_e32 v5, 0xffff
	v_and_b32_e32 v4, 32, v4
	s_lshr_b32 s7, s0, 1
	v_ashrrev_i32_e32 v1, 5, v109
	v_cndmask_b32_e64 v113, 0, v5, s[36:37]
	v_cndmask_b32_e64 v5, 0, v111, s[36:37]
	s_movk_i32 s0, 0x410
	v_add3_u32 v0, 0, v4, v0
	v_lshlrev_b32_e32 v4, 4, v109
	v_lshl_add_u64 v[104:105], s[54:55], 0, v[2:3]
	v_or_b32_sdwa v2, v5, v5 dst_sel:DWORD dst_unused:UNUSED_PAD src0_sel:WORD_1 src1_sel:DWORD
	v_mul_lo_u32 v5, v1, s0
	v_lshlrev_b32_e32 v125, 2, v1
	v_lshlrev_b32_e32 v158, 4, v1
	v_lshlrev_b32_e32 v1, 8, v1
	v_and_b32_e32 v4, 0xc0, v4
	v_mov_b32_e32 v18, v3
	v_mov_b32_e32 v19, v3
	v_add3_u32 v124, 0, v5, v6
	v_add3_u32 v159, v0, v1, v4
	v_mov_b32_e32 v4, v3
	v_mov_b32_e32 v5, v3
	v_mov_b32_e32 v6, v3
	v_mov_b32_e32 v7, v3
	v_mov_b32_e32 v8, v3
	v_mov_b32_e32 v9, v3
	v_mov_b32_e32 v10, v3
	v_mov_b32_e32 v11, v3
	v_mov_b32_e32 v12, v3
	v_mov_b32_e32 v13, v3
	v_mov_b32_e32 v14, v3
	v_mov_b32_e32 v15, v3
	v_mov_b32_e32 v16, v3
	v_mov_b32_e32 v17, v3
	v_mov_b64_e32 v[34:35], v[18:19]
	v_mov_b64_e32 v[50:51], v[18:19]
	v_cndmask_b32_e64 v100, 0, v107, s[36:37]
	v_cndmask_b32_e64 v101, 0, v114, s[36:37]
	v_cndmask_b32_e64 v102, 0, v115, s[36:37]
	v_mov_b32_e32 v103, v3
	s_mov_b32 s8, 5
	v_add_u32_e32 v116, 0xfffffe01, v108
	v_add_u32_e32 v126, 32, v125
	v_or_b32_e32 v127, 1, v125
	v_add_u32_e32 v128, 33, v125
	v_or_b32_e32 v129, 2, v125
	v_add_u32_e32 v130, 34, v125
	v_or_b32_e32 v131, 3, v125
	v_add_u32_e32 v132, 35, v125
	v_add_u32_e32 v133, 8, v125
	v_add_u32_e32 v134, 40, v125
	v_add_u32_e32 v135, 9, v125
	v_add_u32_e32 v136, 41, v125
	v_add_u32_e32 v137, 10, v125
	v_add_u32_e32 v138, 42, v125
	v_add_u32_e32 v139, 11, v125
	v_add_u32_e32 v140, 43, v125
	v_add_u32_e32 v141, 16, v125
	v_add_u32_e32 v142, 48, v125
	v_add_u32_e32 v143, 17, v125
	v_add_u32_e32 v144, 49, v125
	v_add_u32_e32 v145, 18, v125
	v_add_u32_e32 v146, 50, v125
	v_add_u32_e32 v147, 19, v125
	v_add_u32_e32 v148, 51, v125
	v_add_u32_e32 v149, 24, v125
	v_add_u32_e32 v150, 56, v125
	v_add_u32_e32 v151, 25, v125
	v_add_u32_e32 v152, 57, v125
	v_add_u32_e32 v153, 26, v125
	v_add_u32_e32 v154, 58, v125
	v_add_u32_e32 v155, 27, v125
	v_add_u32_e32 v156, 59, v125
	s_mov_b64 s[38:39], -1
	v_mov_b32_e32 v160, 0
	v_readlane_b32 s9, v254, 22
	v_mov_b64_e32 v[32:33], v[16:17]
	v_mov_b64_e32 v[30:31], v[14:15]
	v_mov_b64_e32 v[28:29], v[12:13]
	v_mov_b64_e32 v[26:27], v[10:11]
	v_mov_b64_e32 v[24:25], v[8:9]
	v_mov_b64_e32 v[22:23], v[6:7]
	v_mov_b64_e32 v[20:21], v[4:5]
	v_mov_b64_e32 v[48:49], v[16:17]
	v_mov_b64_e32 v[46:47], v[14:15]
	v_mov_b64_e32 v[44:45], v[12:13]
	v_mov_b64_e32 v[42:43], v[10:11]
	v_mov_b64_e32 v[40:41], v[8:9]
	v_mov_b64_e32 v[38:39], v[6:7]
	v_mov_b64_e32 v[36:37], v[4:5]
	.p2align	6

.LBB0_1918:
	s_cmp_ge_i32 s0, s4
	v_mov_b32_e32 v161, 0
	v_mov_b32_e32 v162, 0
	s_cbranch_scc0 .LBB0_1946
	.p2align	6

.LBB0_1920:
	v_mov_b32_e32 v0, s9
	ds_read_b32 v161, v0
	.p2align	6

.LBB0_2027:
	s_add_u32 s40, s4, 0x50988000
	s_addc_u32 s41, s5, 0
	s_add_u32 s42, s4, 0x631c8000
	s_addc_u32 s43, s5, 0
	s_add_i32 m0, s23, 0x18000
	v_lshl_add_u64 v[4:5], v[4:5], 0, s[24:25]
	s_waitcnt vmcnt(2)
	s_barrier
	global_load_lds_dwordx4 v[4:5], off
	v_lshl_add_u64 v[4:5], v[6:7], 0, s[24:25]
	s_add_i32 m0, s23, 0x1a000
	s_add_i32 s56, s23, 0x8000
	global_load_lds_dwordx4 v[4:5], off
	v_lshl_add_u64 v[4:5], v[12:13], 0, s[24:25]
	s_mov_b32 m0, s56
	s_add_i32 s57, s23, 0xa000
	global_load_lds_dwordx4 v[4:5], off
	v_lshl_add_u64 v[4:5], v[14:15], 0, s[24:25]
	s_mov_b32 m0, s57
	s_lshr_b32 s3, s3, 26
	global_load_lds_dwordx4 v[4:5], off
	s_add_i32 m0, s23, 0x1c000
	v_lshl_add_u64 v[4:5], v[8:9], 0, s[24:25]
	global_load_lds_dwordx4 v[4:5], off
	v_lshl_add_u64 v[4:5], v[10:11], 0, s[24:25]
	s_add_i32 m0, s23, 0x1e000
	s_add_i32 s3, s2, s3
	global_load_lds_dwordx4 v[4:5], off
	v_bfe_u32 v5, v2, 4, 2
	v_and_b32_e32 v4, 15, v2
	v_lshlrev_b32_e32 v7, 4, v5
	v_lshlrev_b32_e32 v8, 2, v2
	s_and_b32 s4, s35, 3
	s_ashr_i32 s58, s3, 6
	v_lshl_or_b32 v7, v4, 6, v7
	s_lshl_b32 s3, s30, 13
	v_and_b32_e32 v8, 32, v8
	s_sext_i32_i8 s66, s6
	s_ashr_i32 s6, s9, 31
	v_bitop3_b32 v9, v7, s3, v8 bitop3:0xde
	s_lshl_b32 s3, s4, 12
	s_cmp_gt_i32 s2, 63
	s_cselect_b64 s[44:45], -1, 0
	s_or_b32 s59, s4, 64
	s_add_i32 s60, s58, -2
	v_bitop3_b32 v156, v7, s3, v8 bitop3:0xde
	v_lshlrev_b32_e32 v7, 4, v4
	s_cmpk_lt_u32 s34, 0x100
	v_bfe_u32 v4, v2, 2, 4
	s_cselect_b64 s[46:47], -1, 0
	v_and_b32_e32 v8, 63, v2
	v_and_b32_e32 v10, 3, v2
	v_and_b32_e32 v2, 60, v2
	s_mul_i32 s61, s30, 0x180
	v_lshl_or_b32 v159, s30, 6, v4
	s_mul_i32 s30, s30, 0x60000
	s_lshl_b32 s2, s4, 10
	v_lshlrev_b32_e32 v6, 3, v5
	v_lshl_or_b32 v158, v10, 6, v2
	v_sub_u32_e32 v2, v10, v5
	s_or_b32 s2, s30, s2
	v_lshl_or_b32 v157, s4, 5, v6
	v_lshlrev_b32_e32 v6, 8, v5
	v_lshlrev_b32_e32 v4, 3, v2
	v_lshlrev_b32_e32 v2, 4, v8
	s_add_i32 s2, s2, 0x101000
	s_movk_i32 s4, 0x600
	v_lshl_add_u64 v[146:147], s[40:41], 0, v[2:3]
	v_or3_b32 v160, s2, v6, v7
	v_lshrrev_b32_e32 v6, 1, v21
	v_mul_lo_u32 v2, v20, s4
	v_mad_u64_u32 v[6:7], s[2:3], v6, s77, v[2:3]
	v_or_b32_e32 v2, v6, v22
	v_add_lshl_u32 v2, v2, v23, 1
	s_mov_b64 s[34:35], 0x60080
	v_lshl_add_u64 v[148:149], v[2:3], 0, s[34:35]
	v_lshrrev_b32_e32 v6, 1, v16
	v_mul_lo_u32 v2, v17, s4
	v_mad_u64_u32 v[6:7], s[2:3], v6, s77, v[2:3]
	s_waitcnt vmcnt(6)
	v_or_b32_e32 v2, v6, v18
	v_ashrrev_i32_e32 v5, 31, v4
	v_add_lshl_u32 v2, v2, v19, 1
	v_lshl_add_u64 v[150:151], v[2:3], 0, s[34:35]
	s_mov_b32 s62, 0
	v_add_u32_e32 v161, 0, v9
	v_lshlrev_b64 v[152:153], 1, v[4:5]
	s_barrier
	s_branch .LBB0_2030
	.p2align	6

.LBB0_2041:
	v_mov_b32_e32 v127, 0
	s_andn2_b64 vcc, exec, s[44:45]
	v_mov_b32_e32 v126, v127
	v_mov_b32_e32 v125, v127
	v_mov_b32_e32 v124, v127
	v_mov_b32_e32 v131, v127
	v_mov_b32_e32 v130, v127
	v_mov_b32_e32 v129, v127
	v_mov_b32_e32 v128, v127
	v_mov_b32_e32 v115, v127
	v_mov_b32_e32 v114, v127
	v_mov_b32_e32 v113, v127
	v_mov_b32_e32 v112, v127
	v_mov_b32_e32 v111, v127
	v_mov_b32_e32 v110, v127
	v_mov_b32_e32 v109, v127
	v_mov_b32_e32 v108, v127
	v_mov_b32_e32 v99, v127
	v_mov_b32_e32 v98, v127
	v_mov_b32_e32 v97, v127
	v_mov_b32_e32 v96, v127
	v_mov_b32_e32 v95, v127
	v_mov_b32_e32 v94, v127
	v_mov_b32_e32 v93, v127
	v_mov_b32_e32 v92, v127
	v_mov_b32_e32 v83, v127
	v_mov_b32_e32 v82, v127
	v_mov_b32_e32 v81, v127
	v_mov_b32_e32 v80, v127
	v_mov_b32_e32 v79, v127
	v_mov_b32_e32 v78, v127
	v_mov_b32_e32 v77, v127
	v_mov_b32_e32 v76, v127
	v_mov_b32_e32 v123, v127
	v_mov_b32_e32 v122, v127
	v_mov_b32_e32 v121, v127
	v_mov_b32_e32 v120, v127
	v_mov_b32_e32 v119, v127
	v_mov_b32_e32 v118, v127
	v_mov_b32_e32 v117, v127
	v_mov_b32_e32 v116, v127
	v_mov_b32_e32 v107, v127
	v_mov_b32_e32 v106, v127
	v_mov_b32_e32 v105, v127
	v_mov_b32_e32 v104, v127
	v_mov_b32_e32 v103, v127
	v_mov_b32_e32 v102, v127
	v_mov_b32_e32 v101, v127
	v_mov_b32_e32 v100, v127
	v_mov_b32_e32 v91, v127
	v_mov_b32_e32 v90, v127
	v_mov_b32_e32 v89, v127
	v_mov_b32_e32 v88, v127
	v_mov_b32_e32 v87, v127
	v_mov_b32_e32 v86, v127
	v_mov_b32_e32 v85, v127
	v_mov_b32_e32 v84, v127
	v_mov_b32_e32 v75, v127
	v_mov_b32_e32 v74, v127
	v_mov_b32_e32 v73, v127
	v_mov_b32_e32 v72, v127
	v_mov_b32_e32 v71, v127
	v_mov_b32_e32 v70, v127
	v_mov_b32_e32 v69, v127
	v_mov_b32_e32 v68, v127
	v_mov_b32_e32 v67, v127
	v_mov_b32_e32 v66, v127
	v_mov_b32_e32 v65, v127
	v_mov_b32_e32 v64, v127
	v_mov_b32_e32 v63, v127
	v_mov_b32_e32 v62, v127
	v_mov_b32_e32 v61, v127
	v_mov_b32_e32 v60, v127
	v_mov_b32_e32 v51, v127
	v_mov_b32_e32 v50, v127
	v_mov_b32_e32 v49, v127
	v_mov_b32_e32 v48, v127
	v_mov_b32_e32 v47, v127
	v_mov_b32_e32 v46, v127
	v_mov_b32_e32 v45, v127
	v_mov_b32_e32 v44, v127
	v_mov_b32_e32 v35, v127
	v_mov_b32_e32 v34, v127
	v_mov_b32_e32 v33, v127
	v_mov_b32_e32 v32, v127
	v_mov_b32_e32 v31, v127
	v_mov_b32_e32 v30, v127
	v_mov_b32_e32 v29, v127
	v_mov_b32_e32 v28, v127
	v_mov_b32_e32 v19, v127
	v_mov_b32_e32 v18, v127
	v_mov_b32_e32 v17, v127
	v_mov_b32_e32 v16, v127
	v_mov_b32_e32 v15, v127
	v_mov_b32_e32 v14, v127
	v_mov_b32_e32 v13, v127
	v_mov_b32_e32 v12, v127
	v_mov_b32_e32 v59, v127
	v_mov_b32_e32 v58, v127
	v_mov_b32_e32 v57, v127
	v_mov_b32_e32 v56, v127
	v_mov_b32_e32 v55, v127
	v_mov_b32_e32 v54, v127
	v_mov_b32_e32 v53, v127
	v_mov_b32_e32 v52, v127
	v_mov_b32_e32 v43, v127
	v_mov_b32_e32 v42, v127
	v_mov_b32_e32 v41, v127
	v_mov_b32_e32 v40, v127
	v_mov_b32_e32 v39, v127
	v_mov_b32_e32 v38, v127
	v_mov_b32_e32 v37, v127
	v_mov_b32_e32 v36, v127
	v_mov_b32_e32 v27, v127
	v_mov_b32_e32 v26, v127
	v_mov_b32_e32 v25, v127
	v_mov_b32_e32 v24, v127
	v_mov_b32_e32 v23, v127
	v_mov_b32_e32 v22, v127
	v_mov_b32_e32 v21, v127
	v_mov_b32_e32 v20, v127
	v_mov_b32_e32 v11, v127
	v_mov_b32_e32 v10, v127
	v_mov_b32_e32 v9, v127
	v_mov_b32_e32 v8, v127
	v_mov_b32_e32 v7, v127
	v_mov_b32_e32 v6, v127
	v_mov_b32_e32 v5, v127
	v_mov_b32_e32 v4, v127
	s_cbranch_vccnz .LBB0_2051
	s_mul_i32 s2, s65, 0x180000
	s_lshl_b32 s3, s66, 13
	s_add_i32 s3, s3, s2
	s_add_u32 s4, s0, 0x100
	v_mov_b32_e32 v4, 0
	v_add_u32_e32 v154, s3, v160
	s_addc_u32 s5, s1, 0
	s_mov_b32 s67, 0
	v_mov_b32_e32 v5, v4
	v_mov_b32_e32 v6, v4
	v_mov_b32_e32 v7, v4
	v_mov_b32_e32 v8, v4
	v_mov_b32_e32 v9, v4
	v_mov_b32_e32 v10, v4
	v_mov_b32_e32 v11, v4
	v_mov_b32_e32 v20, v4
	v_mov_b32_e32 v21, v4
	v_mov_b32_e32 v22, v4
	v_mov_b32_e32 v23, v4
	v_mov_b32_e32 v24, v4
	v_mov_b32_e32 v25, v4
	v_mov_b32_e32 v26, v4
	v_mov_b32_e32 v27, v4
	v_mov_b32_e32 v36, v4
	v_mov_b32_e32 v37, v4
	v_mov_b32_e32 v38, v4
	v_mov_b32_e32 v39, v4
	v_mov_b32_e32 v40, v4
	v_mov_b32_e32 v41, v4
	v_mov_b32_e32 v42, v4
	v_mov_b32_e32 v43, v4
	v_mov_b32_e32 v52, v4
	v_mov_b32_e32 v53, v4
	v_mov_b32_e32 v54, v4
	v_mov_b32_e32 v55, v4
	v_mov_b32_e32 v56, v4
	v_mov_b32_e32 v57, v4
	v_mov_b32_e32 v58, v4
	v_mov_b32_e32 v59, v4
	v_mov_b32_e32 v12, v4
	v_mov_b32_e32 v13, v4
	v_mov_b32_e32 v14, v4
	v_mov_b32_e32 v15, v4
	v_mov_b32_e32 v16, v4
	v_mov_b32_e32 v17, v4
	v_mov_b32_e32 v18, v4
	v_mov_b32_e32 v19, v4
	v_mov_b32_e32 v28, v4
	v_mov_b32_e32 v29, v4
	v_mov_b32_e32 v30, v4
	v_mov_b32_e32 v31, v4
	v_mov_b32_e32 v32, v4
	v_mov_b32_e32 v33, v4
	v_mov_b32_e32 v34, v4
	v_mov_b32_e32 v35, v4
	v_mov_b32_e32 v44, v4
	v_mov_b32_e32 v45, v4
	v_mov_b32_e32 v46, v4
	v_mov_b32_e32 v47, v4
	v_mov_b32_e32 v48, v4
	v_mov_b32_e32 v49, v4
	v_mov_b32_e32 v50, v4
	v_mov_b32_e32 v51, v4
	v_mov_b32_e32 v60, v4
	v_mov_b32_e32 v61, v4
	v_mov_b32_e32 v62, v4
	v_mov_b32_e32 v63, v4
	v_mov_b32_e32 v64, v4
	v_mov_b32_e32 v65, v4
	v_mov_b32_e32 v66, v4
	v_mov_b32_e32 v67, v4
	v_mov_b32_e32 v68, v4
	v_mov_b32_e32 v69, v4
	v_mov_b32_e32 v70, v4
	v_mov_b32_e32 v71, v4
	v_mov_b32_e32 v72, v4
	v_mov_b32_e32 v73, v4
	v_mov_b32_e32 v74, v4
	v_mov_b32_e32 v75, v4
	v_mov_b32_e32 v84, v4
	v_mov_b32_e32 v85, v4
	v_mov_b32_e32 v86, v4
	v_mov_b32_e32 v87, v4
	v_mov_b32_e32 v88, v4
	v_mov_b32_e32 v89, v4
	v_mov_b32_e32 v90, v4
	v_mov_b32_e32 v91, v4
	v_mov_b32_e32 v100, v4
	v_mov_b32_e32 v101, v4
	v_mov_b32_e32 v102, v4
	v_mov_b32_e32 v103, v4
	v_mov_b32_e32 v104, v4
	v_mov_b32_e32 v105, v4
	v_mov_b32_e32 v106, v4
	v_mov_b32_e32 v107, v4
	v_mov_b32_e32 v116, v4
	v_mov_b32_e32 v117, v4
	v_mov_b32_e32 v118, v4
	v_mov_b32_e32 v119, v4
	v_mov_b32_e32 v120, v4
	v_mov_b32_e32 v121, v4
	v_mov_b32_e32 v122, v4
	v_mov_b32_e32 v123, v4
	v_mov_b32_e32 v76, v4
	v_mov_b32_e32 v77, v4
	v_mov_b32_e32 v78, v4
	v_mov_b32_e32 v79, v4
	v_mov_b32_e32 v80, v4
	v_mov_b32_e32 v81, v4
	v_mov_b32_e32 v82, v4
	v_mov_b32_e32 v83, v4
	v_mov_b32_e32 v92, v4
	v_mov_b32_e32 v93, v4
	v_mov_b32_e32 v94, v4
	v_mov_b32_e32 v95, v4
	v_mov_b32_e32 v96, v4
	v_mov_b32_e32 v97, v4
	v_mov_b32_e32 v98, v4
	v_mov_b32_e32 v99, v4
	v_mov_b32_e32 v108, v4
	v_mov_b32_e32 v109, v4
	v_mov_b32_e32 v110, v4
	v_mov_b32_e32 v111, v4
	v_mov_b32_e32 v112, v4
	v_mov_b32_e32 v113, v4
	v_mov_b32_e32 v114, v4
	v_mov_b32_e32 v115, v4
	v_mov_b32_e32 v128, v4
	v_mov_b32_e32 v129, v4
	v_mov_b32_e32 v130, v4
	v_mov_b32_e32 v131, v4
	v_mov_b32_e32 v124, v4
	v_mov_b32_e32 v125, v4
	v_mov_b32_e32 v126, v4
	v_mov_b32_e32 v127, v4
	s_cmp_lt_i32 s67, 16
	s_cbranch_scc1 .LBB0_2044
	.p2align	6
.LBB0_2043:
	s_cmp_eq_u32 s67, 16
	s_cselect_b64 s[0:1], -1, 0
	s_cbranch_execz .LBB0_2045
	s_branch .LBB0_2046
	.p2align	6

.LBB0_2128:
	s_add_u32 s40, s6, 0x6f1c8000
	s_addc_u32 s41, s7, 0
	s_add_i32 m0, s31, 0x18000
	v_lshl_add_u64 v[4:5], v[4:5], 0, s[24:25]
	s_waitcnt vmcnt(2)
	s_barrier
	global_load_lds_dwordx4 v[4:5], off
	v_lshl_add_u64 v[4:5], v[6:7], 0, s[24:25]
	s_add_i32 m0, s31, 0x1a000
	s_add_i32 s58, s31, 0x8000
	global_load_lds_dwordx4 v[4:5], off
	v_lshl_add_u64 v[4:5], v[12:13], 0, s[24:25]
	s_mov_b32 m0, s58
	s_add_i32 s59, s31, 0xa000
	global_load_lds_dwordx4 v[4:5], off
	v_lshl_add_u64 v[4:5], v[14:15], 0, s[24:25]
	s_mov_b32 m0, s59
	s_lshr_b32 s5, s5, 26
	global_load_lds_dwordx4 v[4:5], off
	s_add_i32 m0, s31, 0x1c000
	v_lshl_add_u64 v[4:5], v[8:9], 0, s[24:25]
	global_load_lds_dwordx4 v[4:5], off
	v_lshl_add_u64 v[4:5], v[10:11], 0, s[24:25]
	s_add_i32 m0, s31, 0x1e000
	s_movk_i32 s6, 0x3c0
	global_load_lds_dwordx4 v[4:5], off
	v_and_b32_e32 v4, 48, v2
	v_lshlrev_b32_e32 v5, 6, v2
	s_add_i32 s5, s4, s5
	v_and_or_b32 v4, v5, s6, v4
	v_lshlrev_b32_e32 v5, 2, v2
	s_ashr_i32 s60, s5, 6
	s_lshl_b32 s5, s35, 13
	v_and_b32_e32 v5, 32, v5
	v_bitop3_b32 v6, v4, s5, v5 bitop3:0xde
	s_lshl_b32 s5, s42, 5
	s_and_b32 s5, s5, 0x60
	s_lshl_b32 s6, s5, 7
	v_bitop3_b32 v144, s6, v4, v5 bitop3:0xf6
	v_bfe_u32 v4, v2, 2, 4
	v_lshl_or_b32 v146, s35, 6, v4
	v_lshlrev_b32_e32 v4, 14, v20
	v_and_b32_e32 v5, 3, v2
	v_and_b32_e32 v2, 60, v2
	v_and_b32_e32 v4, 0xffff8000, v4
	v_lshl_or_b32 v145, v5, 6, v2
	v_lshlrev_b32_e32 v2, 3, v5
	v_lshl_add_u32 v4, v19, 11, v4
	v_and_b32_e32 v5, 1, v20
	v_lshl_or_b32 v4, v5, 6, v4
	s_sext_i32_i8 s47, s8
	s_ashr_i32 s8, s13, 31
	v_lshl_add_u32 v138, v21, 1, v4
	v_lshlrev_b32_e32 v4, 14, v16
	s_cmp_gt_i32 s4, 63
	v_and_b32_e32 v4, 0xffff8000, v4
	s_waitcnt vmcnt(6)
	s_cselect_b64 s[42:43], -1, 0
	s_add_i32 s61, s60, -2
	v_lshl_add_u32 v4, v17, 11, v4
	v_and_b32_e32 v5, 1, v16
	s_cmpk_lt_u32 s34, 0x100
	v_lshl_or_b32 v4, v5, 6, v4
	s_cselect_b64 s[44:45], -1, 0
	v_mov_b32_e32 v139, v3
	v_lshl_add_u32 v140, v18, 1, v4
	v_mov_b32_e32 v141, v3
	s_mov_b32 s62, 0
	v_add_u32_e32 v147, 0, v6
	s_lshl_b32 s46, s5, 1
	v_lshlrev_b32_e32 v2, 1, v2
	s_barrier
	s_branch .LBB0_2131
	.p2align	6

.LBB0_2140:
	s_ashr_i32 s49, s48, 31
	s_lshl_b64 s[6:7], s[48:49], 19
	s_add_u32 s54, s15, s6
	v_mov_b32_e32 v127, 0
	s_addc_u32 s55, s20, s7
	s_andn2_b64 vcc, exec, s[42:43]
	v_mov_b32_e32 v126, v127
	v_mov_b32_e32 v125, v127
	v_mov_b32_e32 v124, v127
	v_mov_b32_e32 v131, v127
	v_mov_b32_e32 v130, v127
	v_mov_b32_e32 v129, v127
	v_mov_b32_e32 v128, v127
	v_mov_b32_e32 v115, v127
	v_mov_b32_e32 v114, v127
	v_mov_b32_e32 v113, v127
	v_mov_b32_e32 v112, v127
	v_mov_b32_e32 v111, v127
	v_mov_b32_e32 v110, v127
	v_mov_b32_e32 v109, v127
	v_mov_b32_e32 v108, v127
	v_mov_b32_e32 v99, v127
	v_mov_b32_e32 v98, v127
	v_mov_b32_e32 v97, v127
	v_mov_b32_e32 v96, v127
	v_mov_b32_e32 v95, v127
	v_mov_b32_e32 v94, v127
	v_mov_b32_e32 v93, v127
	v_mov_b32_e32 v92, v127
	v_mov_b32_e32 v83, v127
	v_mov_b32_e32 v82, v127
	v_mov_b32_e32 v81, v127
	v_mov_b32_e32 v80, v127
	v_mov_b32_e32 v79, v127
	v_mov_b32_e32 v78, v127
	v_mov_b32_e32 v77, v127
	v_mov_b32_e32 v76, v127
	v_mov_b32_e32 v123, v127
	v_mov_b32_e32 v122, v127
	v_mov_b32_e32 v121, v127
	v_mov_b32_e32 v120, v127
	v_mov_b32_e32 v119, v127
	v_mov_b32_e32 v118, v127
	v_mov_b32_e32 v117, v127
	v_mov_b32_e32 v116, v127
	v_mov_b32_e32 v107, v127
	v_mov_b32_e32 v106, v127
	v_mov_b32_e32 v105, v127
	v_mov_b32_e32 v104, v127
	v_mov_b32_e32 v103, v127
	v_mov_b32_e32 v102, v127
	v_mov_b32_e32 v101, v127
	v_mov_b32_e32 v100, v127
	v_mov_b32_e32 v91, v127
	v_mov_b32_e32 v90, v127
	v_mov_b32_e32 v89, v127
	v_mov_b32_e32 v88, v127
	v_mov_b32_e32 v87, v127
	v_mov_b32_e32 v86, v127
	v_mov_b32_e32 v85, v127
	v_mov_b32_e32 v84, v127
	v_mov_b32_e32 v75, v127
	v_mov_b32_e32 v74, v127
	v_mov_b32_e32 v73, v127
	v_mov_b32_e32 v72, v127
	v_mov_b32_e32 v71, v127
	v_mov_b32_e32 v70, v127
	v_mov_b32_e32 v69, v127
	v_mov_b32_e32 v68, v127
	v_mov_b32_e32 v67, v127
	v_mov_b32_e32 v66, v127
	v_mov_b32_e32 v65, v127
	v_mov_b32_e32 v64, v127
	v_mov_b32_e32 v63, v127
	v_mov_b32_e32 v62, v127
	v_mov_b32_e32 v61, v127
	v_mov_b32_e32 v60, v127
	v_mov_b32_e32 v51, v127
	v_mov_b32_e32 v50, v127
	v_mov_b32_e32 v49, v127
	v_mov_b32_e32 v48, v127
	v_mov_b32_e32 v47, v127
	v_mov_b32_e32 v46, v127
	v_mov_b32_e32 v45, v127
	v_mov_b32_e32 v44, v127
	v_mov_b32_e32 v35, v127
	v_mov_b32_e32 v34, v127
	v_mov_b32_e32 v33, v127
	v_mov_b32_e32 v32, v127
	v_mov_b32_e32 v31, v127
	v_mov_b32_e32 v30, v127
	v_mov_b32_e32 v29, v127
	v_mov_b32_e32 v28, v127
	v_mov_b32_e32 v19, v127
	v_mov_b32_e32 v18, v127
	v_mov_b32_e32 v17, v127
	v_mov_b32_e32 v16, v127
	v_mov_b32_e32 v15, v127
	v_mov_b32_e32 v14, v127
	v_mov_b32_e32 v13, v127
	v_mov_b32_e32 v12, v127
	v_mov_b32_e32 v59, v127
	v_mov_b32_e32 v58, v127
	v_mov_b32_e32 v57, v127
	v_mov_b32_e32 v56, v127
	v_mov_b32_e32 v55, v127
	v_mov_b32_e32 v54, v127
	v_mov_b32_e32 v53, v127
	v_mov_b32_e32 v52, v127
	v_mov_b32_e32 v43, v127
	v_mov_b32_e32 v42, v127
	v_mov_b32_e32 v41, v127
	v_mov_b32_e32 v40, v127
	v_mov_b32_e32 v39, v127
	v_mov_b32_e32 v38, v127
	v_mov_b32_e32 v37, v127
	v_mov_b32_e32 v36, v127
	v_mov_b32_e32 v27, v127
	v_mov_b32_e32 v26, v127
	v_mov_b32_e32 v25, v127
	v_mov_b32_e32 v24, v127
	v_mov_b32_e32 v23, v127
	v_mov_b32_e32 v22, v127
	v_mov_b32_e32 v21, v127
	v_mov_b32_e32 v20, v127
	v_mov_b32_e32 v11, v127
	v_mov_b32_e32 v10, v127
	v_mov_b32_e32 v9, v127
	v_mov_b32_e32 v8, v127
	v_mov_b32_e32 v7, v127
	v_mov_b32_e32 v6, v127
	v_mov_b32_e32 v5, v127
	v_mov_b32_e32 v4, v127
	s_cbranch_vccnz .LBB0_2144
	s_and_b64 s[4:5], s[4:5], exec
	s_cselect_b32 s4, s55, s1
	s_cselect_b32 s5, s54, s0
	s_add_u32 s0, s0, 0x40080
	s_addc_u32 s1, s1, 0
	s_add_u32 s6, s2, 0x100
	v_mov_b32_e32 v4, 0
	s_addc_u32 s7, s3, 0
	s_mov_b32 s2, 0
	v_mov_b32_e32 v5, v4
	v_mov_b32_e32 v6, v4
	v_mov_b32_e32 v7, v4
	v_mov_b32_e32 v8, v4
	v_mov_b32_e32 v9, v4
	v_mov_b32_e32 v10, v4
	v_mov_b32_e32 v11, v4
	v_mov_b32_e32 v20, v4
	v_mov_b32_e32 v21, v4
	v_mov_b32_e32 v22, v4
	v_mov_b32_e32 v23, v4
	v_mov_b32_e32 v24, v4
	v_mov_b32_e32 v25, v4
	v_mov_b32_e32 v26, v4
	v_mov_b32_e32 v27, v4
	v_mov_b32_e32 v36, v4
	v_mov_b32_e32 v37, v4
	v_mov_b32_e32 v38, v4
	v_mov_b32_e32 v39, v4
	v_mov_b32_e32 v40, v4
	v_mov_b32_e32 v41, v4
	v_mov_b32_e32 v42, v4
	v_mov_b32_e32 v43, v4
	v_mov_b32_e32 v52, v4
	v_mov_b32_e32 v53, v4
	v_mov_b32_e32 v54, v4
	v_mov_b32_e32 v55, v4
	v_mov_b32_e32 v56, v4
	v_mov_b32_e32 v57, v4
	v_mov_b32_e32 v58, v4
	v_mov_b32_e32 v59, v4
	v_mov_b32_e32 v12, v4
	v_mov_b32_e32 v13, v4
	v_mov_b32_e32 v14, v4
	v_mov_b32_e32 v15, v4
	v_mov_b32_e32 v16, v4
	v_mov_b32_e32 v17, v4
	v_mov_b32_e32 v18, v4
	v_mov_b32_e32 v19, v4
	v_mov_b32_e32 v28, v4
	v_mov_b32_e32 v29, v4
	v_mov_b32_e32 v30, v4
	v_mov_b32_e32 v31, v4
	v_mov_b32_e32 v32, v4
	v_mov_b32_e32 v33, v4
	v_mov_b32_e32 v34, v4
	v_mov_b32_e32 v35, v4
	v_mov_b32_e32 v44, v4
	v_mov_b32_e32 v45, v4
	v_mov_b32_e32 v46, v4
	v_mov_b32_e32 v47, v4
	v_mov_b32_e32 v48, v4
	v_mov_b32_e32 v49, v4
	v_mov_b32_e32 v50, v4
	v_mov_b32_e32 v51, v4
	v_mov_b32_e32 v60, v4
	v_mov_b32_e32 v61, v4
	v_mov_b32_e32 v62, v4
	v_mov_b32_e32 v63, v4
	v_mov_b32_e32 v64, v4
	v_mov_b32_e32 v65, v4
	v_mov_b32_e32 v66, v4
	v_mov_b32_e32 v67, v4
	v_mov_b32_e32 v68, v4
	v_mov_b32_e32 v69, v4
	v_mov_b32_e32 v70, v4
	v_mov_b32_e32 v71, v4
	v_mov_b32_e32 v72, v4
	v_mov_b32_e32 v73, v4
	v_mov_b32_e32 v74, v4
	v_mov_b32_e32 v75, v4
	v_mov_b32_e32 v84, v4
	v_mov_b32_e32 v85, v4
	v_mov_b32_e32 v86, v4
	v_mov_b32_e32 v87, v4
	v_mov_b32_e32 v88, v4
	v_mov_b32_e32 v89, v4
	v_mov_b32_e32 v90, v4
	v_mov_b32_e32 v91, v4
	v_mov_b32_e32 v100, v4
	v_mov_b32_e32 v101, v4
	v_mov_b32_e32 v102, v4
	v_mov_b32_e32 v103, v4
	v_mov_b32_e32 v104, v4
	v_mov_b32_e32 v105, v4
	v_mov_b32_e32 v106, v4
	v_mov_b32_e32 v107, v4
	v_mov_b32_e32 v116, v4
	v_mov_b32_e32 v117, v4
	v_mov_b32_e32 v118, v4
	v_mov_b32_e32 v119, v4
	v_mov_b32_e32 v120, v4
	v_mov_b32_e32 v121, v4
	v_mov_b32_e32 v122, v4
	v_mov_b32_e32 v123, v4
	v_mov_b32_e32 v76, v4
	v_mov_b32_e32 v77, v4
	v_mov_b32_e32 v78, v4
	v_mov_b32_e32 v79, v4
	v_mov_b32_e32 v80, v4
	v_mov_b32_e32 v81, v4
	v_mov_b32_e32 v82, v4
	v_mov_b32_e32 v83, v4
	v_mov_b32_e32 v92, v4
	v_mov_b32_e32 v93, v4
	v_mov_b32_e32 v94, v4
	v_mov_b32_e32 v95, v4
	v_mov_b32_e32 v96, v4
	v_mov_b32_e32 v97, v4
	v_mov_b32_e32 v98, v4
	v_mov_b32_e32 v99, v4
	v_mov_b32_e32 v108, v4
	v_mov_b32_e32 v109, v4
	v_mov_b32_e32 v110, v4
	v_mov_b32_e32 v111, v4
	v_mov_b32_e32 v112, v4
	v_mov_b32_e32 v113, v4
	v_mov_b32_e32 v114, v4
	v_mov_b32_e32 v115, v4
	v_mov_b32_e32 v128, v4
	v_mov_b32_e32 v129, v4
	v_mov_b32_e32 v130, v4
	v_mov_b32_e32 v131, v4
	v_mov_b32_e32 v124, v4
	v_mov_b32_e32 v125, v4
	v_mov_b32_e32 v126, v4
	v_mov_b32_e32 v127, v4
	.p2align	6

.LBB0_2298:
	s_add_u32 s40, s6, 0x731c8000
	s_addc_u32 s41, s7, 0
	s_add_i32 m0, s31, 0x18000
	v_lshl_add_u64 v[4:5], v[4:5], 0, s[24:25]
	s_waitcnt vmcnt(2)
	s_barrier
	global_load_lds_dwordx4 v[4:5], off
	v_lshl_add_u64 v[4:5], v[6:7], 0, s[24:25]
	s_add_i32 m0, s31, 0x1a000
	s_add_i32 s58, s31, 0x8000
	global_load_lds_dwordx4 v[4:5], off
	v_lshl_add_u64 v[4:5], v[12:13], 0, s[24:25]
	s_mov_b32 m0, s58
	s_add_i32 s59, s31, 0xa000
	global_load_lds_dwordx4 v[4:5], off
	v_lshl_add_u64 v[4:5], v[14:15], 0, s[24:25]
	s_mov_b32 m0, s59
	s_lshr_b32 s5, s5, 26
	global_load_lds_dwordx4 v[4:5], off
	s_add_i32 m0, s31, 0x1c000
	v_lshl_add_u64 v[4:5], v[8:9], 0, s[24:25]
	global_load_lds_dwordx4 v[4:5], off
	v_lshl_add_u64 v[4:5], v[10:11], 0, s[24:25]
	s_add_i32 m0, s31, 0x1e000
	s_movk_i32 s6, 0x3c0
	global_load_lds_dwordx4 v[4:5], off
	v_and_b32_e32 v4, 48, v2
	v_lshlrev_b32_e32 v5, 6, v2
	s_add_i32 s5, s4, s5
	v_and_or_b32 v4, v5, s6, v4
	v_lshlrev_b32_e32 v5, 2, v2
	s_ashr_i32 s60, s5, 6
	s_lshl_b32 s5, s35, 13
	v_and_b32_e32 v5, 32, v5
	v_bitop3_b32 v6, v4, s5, v5 bitop3:0xde
	s_lshl_b32 s5, s42, 5
	s_and_b32 s5, s5, 0x60
	s_lshl_b32 s6, s5, 7
	v_bitop3_b32 v150, s6, v4, v5 bitop3:0xf6
	v_bfe_u32 v4, v2, 2, 4
	v_lshl_or_b32 v152, s35, 6, v4
	v_lshlrev_b32_e32 v4, 14, v20
	v_and_b32_e32 v5, 3, v2
	v_and_b32_e32 v2, 60, v2
	v_and_b32_e32 v4, 0xffff8000, v4
	v_lshl_or_b32 v151, v5, 6, v2
	v_lshlrev_b32_e32 v2, 3, v5
	v_lshl_add_u32 v4, v19, 11, v4
	v_and_b32_e32 v5, 1, v20
	v_lshl_or_b32 v4, v5, 6, v4
	s_sext_i32_i8 s47, s8
	s_ashr_i32 s8, s13, 31
	v_lshl_add_u32 v138, v21, 1, v4
	v_lshlrev_b32_e32 v4, 14, v16
	s_cmp_gt_i32 s4, 63
	v_and_b32_e32 v4, 0xffff8000, v4
	s_waitcnt vmcnt(6)
	s_cselect_b64 s[42:43], -1, 0
	s_add_i32 s61, s60, -2
	v_lshl_add_u32 v4, v17, 11, v4
	v_and_b32_e32 v5, 1, v16
	s_cmpk_lt_u32 s34, 0x100
	v_lshl_or_b32 v4, v5, 6, v4
	s_cselect_b64 s[44:45], -1, 0
	v_mov_b32_e32 v139, v3
	v_lshl_add_u32 v140, v18, 1, v4
	v_mov_b32_e32 v141, v3
	s_mov_b32 s62, 0
	v_add_u32_e32 v153, 0, v6
	s_lshl_b32 s46, s5, 1
	v_lshlrev_b32_e32 v2, 1, v2
	s_barrier
	s_branch .LBB0_2301
	.p2align	6

.LBB0_2310:
	s_ashr_i32 s49, s48, 31
	s_lshl_b64 s[6:7], s[48:49], 19
	s_add_u32 s54, s15, s6
	s_addc_u32 s55, s20, s7
	v_mov_b32_e32 v131, 0
	s_andn2_b64 vcc, exec, s[42:43]
	v_mov_b32_e32 v130, 0
	v_mov_b32_e32 v129, 0
	v_mov_b32_e32 v128, 0
	v_mov_b32_e32 v127, 0
	v_mov_b32_e32 v126, 0
	v_mov_b32_e32 v125, 0
	v_mov_b32_e32 v124, 0
	v_mov_b32_e32 v105, 0
	v_mov_b32_e32 v104, 0
	v_mov_b32_e32 v107, 0
	v_mov_b32_e32 v106, 0
	v_mov_b32_e32 v113, 0
	v_mov_b32_e32 v112, 0
	v_mov_b32_e32 v115, 0
	v_mov_b32_e32 v114, 0
	v_mov_b32_e32 v89, 0
	v_mov_b32_e32 v88, 0
	v_mov_b32_e32 v91, 0
	v_mov_b32_e32 v90, 0
	v_mov_b32_e32 v97, 0
	v_mov_b32_e32 v96, 0
	v_mov_b32_e32 v99, 0
	v_mov_b32_e32 v98, 0
	v_mov_b32_e32 v77, 0
	v_mov_b32_e32 v76, 0
	v_mov_b32_e32 v79, 0
	v_mov_b32_e32 v78, 0
	v_mov_b32_e32 v81, 0
	v_mov_b32_e32 v80, 0
	v_mov_b32_e32 v83, 0
	v_mov_b32_e32 v82, 0
	v_mov_b32_e32 v143, 0
	v_mov_b32_e32 v142, 0
	v_mov_b32_e32 v145, 0
	v_mov_b32_e32 v144, 0
	v_mov_b32_e32 v147, 0
	v_mov_b32_e32 v146, 0
	v_mov_b32_e32 v149, 0
	v_mov_b32_e32 v148, 0
	v_mov_b32_e32 v117, 0
	v_mov_b32_e32 v116, 0
	v_mov_b32_e32 v119, 0
	v_mov_b32_e32 v118, 0
	v_mov_b32_e32 v121, 0
	v_mov_b32_e32 v120, 0
	v_mov_b32_e32 v123, 0
	v_mov_b32_e32 v122, 0
	v_mov_b32_e32 v101, 0
	v_mov_b32_e32 v100, 0
	v_mov_b32_e32 v103, 0
	v_mov_b32_e32 v102, 0
	v_mov_b32_e32 v109, 0
	v_mov_b32_e32 v108, 0
	v_mov_b32_e32 v111, 0
	v_mov_b32_e32 v110, 0
	v_mov_b32_e32 v75, 0
	v_mov_b32_e32 v74, 0
	v_mov_b32_e32 v73, 0
	v_mov_b32_e32 v72, 0
	v_mov_b32_e32 v71, 0
	v_mov_b32_e32 v70, 0
	v_mov_b32_e32 v69, 0
	v_mov_b32_e32 v68, 0
	v_mov_b32_e32 v67, 0
	v_mov_b32_e32 v66, 0
	v_mov_b32_e32 v65, 0
	v_mov_b32_e32 v64, 0
	v_mov_b32_e32 v63, 0
	v_mov_b32_e32 v62, 0
	v_mov_b32_e32 v61, 0
	v_mov_b32_e32 v60, 0
	v_mov_b32_e32 v41, 0
	v_mov_b32_e32 v40, 0
	v_mov_b32_e32 v43, 0
	v_mov_b32_e32 v42, 0
	v_mov_b32_e32 v49, 0
	v_mov_b32_e32 v48, 0
	v_mov_b32_e32 v51, 0
	v_mov_b32_e32 v50, 0
	v_mov_b32_e32 v25, 0
	v_mov_b32_e32 v24, 0
	v_mov_b32_e32 v27, 0
	v_mov_b32_e32 v26, 0
	v_mov_b32_e32 v33, 0
	v_mov_b32_e32 v32, 0
	v_mov_b32_e32 v35, 0
	v_mov_b32_e32 v34, 0
	v_mov_b32_e32 v13, 0
	v_mov_b32_e32 v12, 0
	v_mov_b32_e32 v15, 0
	v_mov_b32_e32 v14, 0
	v_mov_b32_e32 v17, 0
	v_mov_b32_e32 v16, 0
	v_mov_b32_e32 v19, 0
	v_mov_b32_e32 v18, 0
	v_mov_b32_e32 v85, 0
	v_mov_b32_e32 v84, 0
	v_mov_b32_e32 v87, 0
	v_mov_b32_e32 v86, 0
	v_mov_b32_e32 v93, 0
	v_mov_b32_e32 v92, 0
	v_mov_b32_e32 v95, 0
	v_mov_b32_e32 v94, 0
	v_mov_b32_e32 v53, 0
	v_mov_b32_e32 v52, 0
	v_mov_b32_e32 v55, 0
	v_mov_b32_e32 v54, 0
	v_mov_b32_e32 v57, 0
	v_mov_b32_e32 v56, 0
	v_mov_b32_e32 v59, 0
	v_mov_b32_e32 v58, 0
	v_mov_b32_e32 v37, 0
	v_mov_b32_e32 v36, 0
	v_mov_b32_e32 v39, 0
	v_mov_b32_e32 v38, 0
	v_mov_b32_e32 v45, 0
	v_mov_b32_e32 v44, 0
	v_mov_b32_e32 v47, 0
	v_mov_b32_e32 v46, 0
	v_mov_b32_e32 v11, 0
	v_mov_b32_e32 v10, 0
	v_mov_b32_e32 v9, 0
	v_mov_b32_e32 v8, 0
	v_mov_b32_e32 v7, 0
	v_mov_b32_e32 v6, 0
	v_mov_b32_e32 v5, 0
	v_mov_b32_e32 v4, 0
	s_cbranch_vccnz .LBB0_2314
	s_and_b64 s[4:5], s[4:5], exec
	s_cselect_b32 s4, s55, s1
	s_cselect_b32 s5, s54, s0
	s_add_u32 s0, s0, 0x40080
	s_addc_u32 s1, s1, 0
	s_add_u32 s6, s2, 0x100
	v_mov_b32_e32 v4, 0
	s_addc_u32 s7, s3, 0
	s_mov_b32 s2, 0
	v_mov_b32_e32 v5, v4
	v_mov_b32_e32 v6, v4
	v_mov_b32_e32 v7, v4
	v_mov_b32_e32 v8, v4
	v_mov_b32_e32 v9, v4
	v_mov_b32_e32 v10, v4
	v_mov_b32_e32 v11, v4
	v_mov_b32_e32 v12, v4
	v_mov_b32_e32 v13, v4
	v_mov_b32_e32 v14, v4
	v_mov_b32_e32 v15, v4
	v_mov_b32_e32 v16, v4
	v_mov_b32_e32 v17, v4
	v_mov_b32_e32 v18, v4
	v_mov_b32_e32 v19, v4
	v_mov_b32_e32 v24, v4
	v_mov_b32_e32 v25, v4
	v_mov_b32_e32 v26, v4
	v_mov_b32_e32 v27, v4
	v_mov_b32_e32 v32, v4
	v_mov_b32_e32 v33, v4
	v_mov_b32_e32 v34, v4
	v_mov_b32_e32 v35, v4
	v_mov_b32_e32 v40, v4
	v_mov_b32_e32 v41, v4
	v_mov_b32_e32 v42, v4
	v_mov_b32_e32 v43, v4
	v_mov_b32_e32 v48, v4
	v_mov_b32_e32 v49, v4
	v_mov_b32_e32 v50, v4
	v_mov_b32_e32 v51, v4
	v_mov_b32_e32 v20, v4
	v_mov_b32_e32 v21, v4
	v_mov_b32_e32 v22, v4
	v_mov_b32_e32 v23, v4
	v_mov_b32_e32 v28, v4
	v_mov_b32_e32 v29, v4
	v_mov_b32_e32 v30, v4
	v_mov_b32_e32 v31, v4
	v_mov_b32_e32 v36, v4
	v_mov_b32_e32 v37, v4
	v_mov_b32_e32 v38, v4
	v_mov_b32_e32 v39, v4
	v_mov_b32_e32 v44, v4
	v_mov_b32_e32 v45, v4
	v_mov_b32_e32 v46, v4
	v_mov_b32_e32 v47, v4
	v_mov_b32_e32 v52, v4
	v_mov_b32_e32 v53, v4
	v_mov_b32_e32 v54, v4
	v_mov_b32_e32 v55, v4
	v_mov_b32_e32 v56, v4
	v_mov_b32_e32 v57, v4
	v_mov_b32_e32 v58, v4
	v_mov_b32_e32 v59, v4
	v_mov_b32_e32 v60, v4
	v_mov_b32_e32 v61, v4
	v_mov_b32_e32 v62, v4
	v_mov_b32_e32 v63, v4
	v_mov_b32_e32 v64, v4
	v_mov_b32_e32 v65, v4
	v_mov_b32_e32 v66, v4
	v_mov_b32_e32 v67, v4
	v_mov_b32_e32 v68, v4
	v_mov_b32_e32 v69, v4
	v_mov_b32_e32 v70, v4
	v_mov_b32_e32 v71, v4
	v_mov_b32_e32 v72, v4
	v_mov_b32_e32 v73, v4
	v_mov_b32_e32 v74, v4
	v_mov_b32_e32 v75, v4
	v_mov_b32_e32 v76, v4
	v_mov_b32_e32 v77, v4
	v_mov_b32_e32 v78, v4
	v_mov_b32_e32 v79, v4
	v_mov_b32_e32 v80, v4
	v_mov_b32_e32 v81, v4
	v_mov_b32_e32 v82, v4
	v_mov_b32_e32 v83, v4
	v_mov_b32_e32 v88, v4
	v_mov_b32_e32 v89, v4
	v_mov_b32_e32 v90, v4
	v_mov_b32_e32 v91, v4
	v_mov_b32_e32 v96, v4
	v_mov_b32_e32 v97, v4
	v_mov_b32_e32 v98, v4
	v_mov_b32_e32 v99, v4
	v_mov_b32_e32 v104, v4
	v_mov_b32_e32 v105, v4
	v_mov_b32_e32 v106, v4
	v_mov_b32_e32 v107, v4
	v_mov_b32_e32 v112, v4
	v_mov_b32_e32 v113, v4
	v_mov_b32_e32 v114, v4
	v_mov_b32_e32 v115, v4
	v_mov_b32_e32 v84, v4
	v_mov_b32_e32 v85, v4
	v_mov_b32_e32 v86, v4
	v_mov_b32_e32 v87, v4
	v_mov_b32_e32 v92, v4
	v_mov_b32_e32 v93, v4
	v_mov_b32_e32 v94, v4
	v_mov_b32_e32 v95, v4
	v_mov_b32_e32 v100, v4
	v_mov_b32_e32 v101, v4
	v_mov_b32_e32 v102, v4
	v_mov_b32_e32 v103, v4
	v_mov_b32_e32 v108, v4
	v_mov_b32_e32 v109, v4
	v_mov_b32_e32 v110, v4
	v_mov_b32_e32 v111, v4
	v_mov_b32_e32 v116, v4
	v_mov_b32_e32 v117, v4
	v_mov_b32_e32 v118, v4
	v_mov_b32_e32 v119, v4
	v_mov_b32_e32 v120, v4
	v_mov_b32_e32 v121, v4
	v_mov_b32_e32 v122, v4
	v_mov_b32_e32 v123, v4
	v_mov_b32_e32 v124, v4
	v_mov_b32_e32 v125, v4
	v_mov_b32_e32 v126, v4
	v_mov_b32_e32 v127, v4
	v_mov_b32_e32 v128, v4
	v_mov_b32_e32 v129, v4
	v_mov_b32_e32 v130, v4
	v_mov_b32_e32 v131, v4
	.p2align	6

.LBB0_2390:
	v_readlane_b32 s0, v252, 52
	v_readlane_b32 s1, v252, 53
	v_readlane_b32 s2, v252, 54
	v_readlane_b32 s3, v252, 55
	s_mov_b64 s[0:1], s[2:3]
	s_add_u32 s28, s0, 0x731c8000
	v_readlane_b32 s2, v254, 43
	s_addc_u32 s29, s1, 0
	s_lshl_b32 s2, s2, 22
	v_readlane_b32 s3, v254, 44
	s_add_u32 s2, s0, s2
	s_addc_u32 s3, s1, 0
	s_add_u32 s13, s2, 0x755c8000
	s_addc_u32 s20, s3, 0
	s_add_u32 s9, s0, 0x75dc8000
	s_addc_u32 s12, s1, 0
	s_cmpk_lg_i32 s7, 0x100
	s_mov_b64 s[0:1], -1
	s_cbranch_scc0 .LBB0_2393
	s_cmpk_gt_i32 s6, 0x1ff
	s_mov_b32 s21, s6
	s_cbranch_scc0 .LBB0_2405
	.p2align	6

.LBB0_2393:
	s_andn2_b64 vcc, exec, s[0:1]
	s_cbranch_vccnz .LBB0_2413
	s_ashr_i32 s0, s6, 5
	s_lshl_b32 s1, s0, 12
	s_lshl_b32 s2, s6, 8
	s_add_i32 s7, s1, s92
	s_lshl_b32 s1, s6, 3
	s_and_b32 s4, s2, 0xf00
	s_and_b32 s6, s1, 0x80
	s_ashr_i32 s1, s0, 31
	s_add_i32 s7, s7, s4
	s_lshl_b64 s[2:3], s[0:1], 19
	s_add_u32 s13, s13, s2
	s_addc_u32 s20, s20, s3
	s_lshl_b64 s[0:1], s[0:1], 12
	s_add_u32 s0, s0, s92
	s_addc_u32 s1, s1, 0
	s_add_u32 s0, s0, s4
	s_addc_u32 s1, s1, 0
	s_lshl_b64 s[0:1], s[0:1], 10
	s_add_u32 s9, s9, s0
	s_addc_u32 s12, s12, s1
	s_mov_b32 s2, 0
	s_mov_b64 s[0:1], -1
	s_branch .LBB0_2396
	.p2align	6

.LBB0_2396:
	v_mbcnt_lo_u32_b32 v0, -1, 0
	v_mbcnt_hi_u32_b32 v0, -1, v0
	s_xor_b64 s[40:41], s[0:1], -1
	v_and_b32_e32 v139, 31, v0
	v_and_b32_e32 v137, 63, v0
	v_bfe_u32 v138, v0, 5, 1
	v_or_b32_e32 v0, s7, v139
	v_ashrrev_i32_e32 v1, 31, v0
	v_lshlrev_b64 v[0:1], 10, v[0:1]
	s_or_b32 s0, s2, s6
	s_mov_b32 s1, s11
	v_lshl_add_u64 v[0:1], s[28:29], 0, v[0:1]
	s_lshl_b64 s[0:1], s[0:1], 1
	v_lshl_add_u64 v[0:1], v[0:1], 0, s[0:1]
	v_lshlrev_b32_e32 v2, 4, v138
	v_lshl_add_u64 v[0:1], v[0:1], 0, v[2:3]
	v_mov_b32_e32 v4, v137
	global_load_dwordx4 v[100:103], v[0:1], off
	global_load_dwordx4 v[104:107], v[0:1], off offset:32
	global_load_dwordx4 v[108:111], v[0:1], off offset:64
	global_load_dwordx4 v[112:115], v[0:1], off offset:96
	global_load_dwordx4 v[116:119], v[0:1], off offset:128
	global_load_dwordx4 v[120:123], v[0:1], off offset:160
	global_load_dwordx4 v[124:127], v[0:1], off offset:192
	global_load_dwordx4 v[128:131], v[0:1], off offset:224
	s_add_u32 s2, s13, s0
	v_ashrrev_i32_e32 v0, 2, v4
	v_lshlrev_b32_e32 v1, 3, v4
	v_add_u32_e32 v0, s71, v0
	v_and_b32_e32 v14, 24, v1
	v_ashrrev_i32_e32 v5, 31, v4
	s_addc_u32 s3, s20, s1
	v_lshlrev_b32_e32 v2, 1, v14
	s_waitcnt vmcnt(0)
	v_lshlrev_b64 v[8:9], 11, v[4:5]
	v_ashrrev_i32_e32 v1, 31, v0
	v_readlane_b32 s14, v254, 36
	v_lshl_add_u64 v[6:7], s[2:3], 0, v[2:3]
	v_lshl_add_u64 v[8:9], s[2:3], 0, v[8:9]
	v_lshlrev_b64 v[0:1], 11, v[0:1]
	v_readlane_b32 s15, v254, 37
	s_mov_b32 m0, s91
	v_lshl_add_u64 v[0:1], v[6:7], 0, v[0:1]
	v_lshl_add_u64 v[6:7], v[8:9], 0, s[10:11]
	s_mov_b32 s15, s11
	v_readlane_b32 s22, v254, 38
	global_load_lds_dwordx4 v[6:7], off
	v_lshl_add_u64 v[6:7], v[0:1], 0, s[14:15]
	s_mov_b64 s[36:37], 0x400
	v_readlane_b32 s23, v254, 39
	v_readlane_b32 s30, v254, 40
	v_lshl_add_u64 v[6:7], v[6:7], 0, s[36:37]
	s_mov_b32 m0, s97
	s_mov_b32 s23, s11
	v_readlane_b32 s2, v254, 23
	v_readlane_b32 s31, v254, 41
	global_load_lds_dwordx4 v[6:7], off
	v_lshl_add_u64 v[6:7], v[8:9], 0, s[22:23]
	s_mov_b32 m0, s2
	s_mov_b32 s31, s11
	global_load_lds_dwordx4 v[6:7], off
	v_lshl_add_u64 v[6:7], v[0:1], 0, s[30:31]
	v_readlane_b32 s3, v253, 51
	v_lshl_add_u64 v[6:7], v[6:7], 0, s[36:37]
	s_add_i32 m0, s94, s3
	s_mov_b64 s[4:5], 0x20000
	global_load_lds_dwordx4 v[6:7], off
	v_lshl_add_u64 v[6:7], v[8:9], 0, s[4:5]
	v_readlane_b32 s2, v254, 24
	v_lshl_add_u64 v[10:11], v[0:1], 0, s[4:5]
	v_lshl_add_u64 v[12:13], v[6:7], 0, s[10:11]
	s_mov_b32 m0, s2
	s_add_i32 s2, 0, 0x14400
	global_load_lds_dwordx4 v[12:13], off
	v_lshl_add_u64 v[12:13], v[10:11], 0, s[14:15]
	v_readlane_b32 s4, v254, 2
	v_lshl_add_u64 v[12:13], v[12:13], 0, s[36:37]
	s_add_i32 m0, s2, s4
	v_readlane_b32 s5, v254, 25
	global_load_lds_dwordx4 v[12:13], off
	v_lshl_add_u64 v[6:7], v[6:7], 0, s[22:23]
	s_mov_b32 m0, s5
	s_mov_b64 s[34:35], 0x40000
	global_load_lds_dwordx4 v[6:7], off
	v_lshl_add_u64 v[6:7], v[10:11], 0, s[30:31]
	v_lshl_add_u64 v[6:7], v[6:7], 0, s[36:37]
	s_add_i32 m0, s2, s3
	v_readlane_b32 s2, v254, 30
	global_load_lds_dwordx4 v[6:7], off
	v_lshl_add_u64 v[6:7], v[8:9], 0, s[34:35]
	v_lshl_add_u64 v[10:11], v[0:1], 0, s[34:35]
	v_lshl_add_u64 v[12:13], v[6:7], 0, s[10:11]
	s_mov_b32 m0, s2
	v_readlane_b32 s2, v254, 31
	global_load_lds_dwordx4 v[12:13], off
	v_lshl_add_u64 v[12:13], v[10:11], 0, s[14:15]
	v_lshl_add_u64 v[12:13], v[12:13], 0, s[36:37]
	s_add_i32 m0, s2, s4
	v_readlane_b32 s5, v254, 32
	global_load_lds_dwordx4 v[12:13], off
	v_lshl_add_u64 v[6:7], v[6:7], 0, s[22:23]
	s_mov_b32 m0, s5
	s_mov_b64 s[34:35], 0x60000
	global_load_lds_dwordx4 v[6:7], off
	v_lshl_add_u64 v[6:7], v[10:11], 0, s[30:31]
	v_lshl_add_u64 v[6:7], v[6:7], 0, s[36:37]
	s_add_i32 m0, s2, s3
	v_readlane_b32 s2, v254, 33
	global_load_lds_dwordx4 v[6:7], off
	s_mov_b32 m0, s2
	s_mov_b32 s2, s14
	v_writelane_b32 v254, s2, 36
	v_lshl_add_u64 v[6:7], v[8:9], 0, s[34:35]
	v_lshl_add_u64 v[8:9], v[6:7], 0, s[10:11]
	v_writelane_b32 v254, s3, 37
	global_load_lds_dwordx4 v[8:9], off
	v_readlane_b32 s2, v254, 34
	s_add_i32 m0, s2, s4
	s_mov_b32 s4, s22
	v_lshl_add_u64 v[0:1], v[0:1], 0, s[34:35]
	v_writelane_b32 v254, s4, 38
	v_lshl_add_u64 v[8:9], v[0:1], 0, s[14:15]
	v_lshl_add_u64 v[8:9], v[8:9], 0, s[36:37]
	v_writelane_b32 v254, s5, 39
	global_load_lds_dwordx4 v[8:9], off
	v_readlane_b32 s4, v254, 35
	v_lshl_add_u64 v[6:7], v[6:7], 0, s[22:23]
	s_mov_b32 m0, s4
	v_lshl_add_u64 v[0:1], v[0:1], 0, s[30:31]
	global_load_lds_dwordx4 v[6:7], off
	v_lshl_add_u64 v[0:1], v[0:1], 0, s[36:37]
	s_add_i32 m0, s2, s3
	v_and_b32_e32 v5, 31, v4
	global_load_lds_dwordx4 v[0:1], off
	v_ashrrev_i32_e32 v6, 5, v4
	v_cmp_gt_u32_e64 s[34:35], 32, v4
	v_lshlrev_b32_e32 v8, 1, v4
	v_lshlrev_b32_e32 v4, 4, v4
	s_movk_i32 s2, 0x410
	v_and_b32_e32 v4, 0xc0, v4
	s_mov_b32 s4, s30
	v_mul_lo_u32 v7, v6, s2
	v_lshlrev_b32_e32 v20, 4, v6
	v_and_b32_e32 v8, 32, v8
	v_lshl_or_b32 v4, v6, 8, v4
	v_mov_b32_e32 v18, v3
	v_mov_b32_e32 v19, v3
	v_writelane_b32 v254, s4, 40
	v_lshl_add_u32 v140, v5, 2, s33
	v_or3_b32 v141, v4, v8, v14
	v_lshl_add_u32 v142, v5, 4, v7
	v_mov_b32_e32 v4, v3
	v_mov_b32_e32 v5, v3
	v_mov_b32_e32 v6, v3
	v_mov_b32_e32 v7, v3
	v_mov_b32_e32 v8, v3
	v_mov_b32_e32 v9, v3
	v_mov_b32_e32 v10, v3
	v_mov_b32_e32 v11, v3
	v_mov_b32_e32 v12, v3
	v_mov_b32_e32 v13, v3
	v_mov_b32_e32 v14, v3
	v_mov_b32_e32 v15, v3
	v_mov_b32_e32 v16, v3
	v_mov_b32_e32 v17, v3
	v_add_u32_e32 v144, s33, v20
	v_mov_b64_e32 v[34:35], v[18:19]
	v_mov_b64_e32 v[50:51], v[18:19]
	v_mov_b64_e32 v[66:67], v[18:19]
	v_writelane_b32 v254, s5, 41
	s_mov_b32 s15, 4
	v_cndmask_b32_e64 v0, v212, 0, s[34:35]
	v_cndmask_b32_e64 v1, v213, 0, s[34:35]
	v_mov_b32_e32 v2, v3
	v_mov_b32_e32 v132, v3
	v_mov_b32_e32 v133, v3
	v_mov_b32_e32 v134, v3
	v_mov_b32_e32 v135, v3
	v_mov_b32_e32 v143, 0
	s_mov_b64 s[36:37], -1
	v_mov_b64_e32 v[32:33], v[16:17]
	v_mov_b64_e32 v[30:31], v[14:15]
	v_mov_b64_e32 v[28:29], v[12:13]
	v_mov_b64_e32 v[26:27], v[10:11]
	v_mov_b64_e32 v[24:25], v[8:9]
	v_mov_b64_e32 v[22:23], v[6:7]
	v_mov_b64_e32 v[20:21], v[4:5]
	v_mov_b64_e32 v[48:49], v[16:17]
	v_mov_b64_e32 v[46:47], v[14:15]
	v_mov_b64_e32 v[44:45], v[12:13]
	v_mov_b64_e32 v[42:43], v[10:11]
	v_mov_b64_e32 v[40:41], v[8:9]
	v_mov_b64_e32 v[38:39], v[6:7]
	v_mov_b64_e32 v[36:37], v[4:5]
	v_mov_b64_e32 v[64:65], v[16:17]
	v_mov_b64_e32 v[62:63], v[14:15]
	v_mov_b64_e32 v[60:61], v[12:13]
	v_mov_b64_e32 v[58:59], v[10:11]
	v_mov_b64_e32 v[56:57], v[8:9]
	v_mov_b64_e32 v[54:55], v[6:7]
	v_mov_b64_e32 v[52:53], v[4:5]
	v_mov_b32_e32 v145, 0
	s_waitcnt vmcnt(0) lgkmcnt(0)
	s_barrier
	s_branch .LBB0_2399
	.p2align	6
.LBB0_2397:
	s_or_b64 exec, exec, s[4:5]
	v_add_f32_e32 v145, v145, v136
	v_pk_add_f32 v[68:69], v[68:69], v[136:137] op_sel_hi:[1,0] neg_lo:[0,1] neg_hi:[0,1]
	v_pk_add_f32 v[84:85], v[84:85], v[136:137] op_sel_hi:[1,0] neg_lo:[0,1] neg_hi:[0,1]
	v_pk_add_f32 v[70:71], v[70:71], v[136:137] op_sel_hi:[1,0] neg_lo:[0,1] neg_hi:[0,1]
	v_pk_add_f32 v[86:87], v[86:87], v[136:137] op_sel_hi:[1,0] neg_lo:[0,1] neg_hi:[0,1]
	v_pk_add_f32 v[72:73], v[72:73], v[136:137] op_sel_hi:[1,0] neg_lo:[0,1] neg_hi:[0,1]
	v_pk_add_f32 v[88:89], v[88:89], v[136:137] op_sel_hi:[1,0] neg_lo:[0,1] neg_hi:[0,1]
	v_pk_add_f32 v[74:75], v[74:75], v[136:137] op_sel_hi:[1,0] neg_lo:[0,1] neg_hi:[0,1]
	v_pk_add_f32 v[90:91], v[90:91], v[136:137] op_sel_hi:[1,0] neg_lo:[0,1] neg_hi:[0,1]
	v_pk_add_f32 v[76:77], v[76:77], v[136:137] op_sel_hi:[1,0] neg_lo:[0,1] neg_hi:[0,1]
	v_pk_add_f32 v[92:93], v[92:93], v[136:137] op_sel_hi:[1,0] neg_lo:[0,1] neg_hi:[0,1]
	v_pk_add_f32 v[78:79], v[78:79], v[136:137] op_sel_hi:[1,0] neg_lo:[0,1] neg_hi:[0,1]
	v_pk_add_f32 v[94:95], v[94:95], v[136:137] op_sel_hi:[1,0] neg_lo:[0,1] neg_hi:[0,1]
	v_pk_add_f32 v[80:81], v[80:81], v[136:137] op_sel_hi:[1,0] neg_lo:[0,1] neg_hi:[0,1]
	v_pk_add_f32 v[96:97], v[96:97], v[136:137] op_sel_hi:[1,0] neg_lo:[0,1] neg_hi:[0,1]
	v_pk_add_f32 v[82:83], v[82:83], v[136:137] op_sel_hi:[1,0] neg_lo:[0,1] neg_hi:[0,1]
	v_pk_add_f32 v[98:99], v[98:99], v[136:137] op_sel_hi:[1,0] neg_lo:[0,1] neg_hi:[0,1]
	v_xor_b32_e32 v136, 0x80000000, v145
	v_and_b32_e32 v147, 0xffff0000, v136
	v_sub_f32_e64 v147, -v145, v147
	v_and_b32_e32 v148, 0xffff0000, v147
	v_sub_f32_e32 v147, v147, v148
	v_lshrrev_b32_e32 v147, 16, v147
	s_waitcnt lgkmcnt(0)
	v_or_b32_sdwa v136, v148, v136 dst_sel:DWORD dst_unused:UNUSED_PAD src0_sel:DWORD src1_sel:WORD_1
	v_cndmask_b32_e64 v133, v147, v133, s[34:35]
	v_mul_f32_e32 v143, v143, v146
	ds_read_b128 v[146:149], v144
	ds_read_b128 v[150:153], v144 offset:32
	ds_read_b128 v[154:157], v144 offset:64
	ds_read_b128 v[158:161], v144 offset:96
	s_waitcnt lgkmcnt(0)
	s_and_b64 s[36:37], s[36:37], s[2:3]
	v_cndmask_b32_e64 v132, v136, v132, s[34:35]
	s_waitcnt lgkmcnt(1)
	v_pk_mul_f32 v[60:61], v[60:61], v[154:155]
	s_waitcnt lgkmcnt(0)
	v_pk_mul_f32 v[64:65], v[64:65], v[158:159]
	v_pk_mul_f32 v[56:57], v[56:57], v[150:151]
	v_pk_mul_f32 v[66:67], v[66:67], v[160:161]
	v_pk_mul_f32 v[62:63], v[62:63], v[156:157]
	v_pk_mul_f32 v[58:59], v[58:59], v[152:153]
	v_pk_mul_f32 v[54:55], v[54:55], v[148:149]
	v_pk_mul_f32 v[52:53], v[52:53], v[146:147]
	v_pk_mul_f32 v[48:49], v[48:49], v[158:159]
	v_pk_mul_f32 v[44:45], v[44:45], v[154:155]
	v_pk_mul_f32 v[40:41], v[40:41], v[150:151]
	v_pk_mul_f32 v[50:51], v[50:51], v[160:161]
	v_pk_mul_f32 v[46:47], v[46:47], v[156:157]
	v_pk_mul_f32 v[42:43], v[42:43], v[152:153]
	v_pk_mul_f32 v[38:39], v[38:39], v[148:149]
	v_pk_mul_f32 v[36:37], v[36:37], v[146:147]
	v_pk_mul_f32 v[32:33], v[32:33], v[158:159]
	v_pk_mul_f32 v[28:29], v[28:29], v[154:155]
	v_pk_mul_f32 v[24:25], v[24:25], v[150:151]
	v_pk_mul_f32 v[34:35], v[34:35], v[160:161]
	v_pk_mul_f32 v[30:31], v[30:31], v[156:157]
	v_pk_mul_f32 v[26:27], v[26:27], v[152:153]
	v_pk_mul_f32 v[22:23], v[22:23], v[148:149]
	v_pk_mul_f32 v[20:21], v[20:21], v[146:147]
	v_pk_mul_f32 v[16:17], v[16:17], v[158:159]
	v_pk_mul_f32 v[12:13], v[12:13], v[154:155]
	v_pk_mul_f32 v[8:9], v[8:9], v[150:151]
	v_pk_mul_f32 v[18:19], v[18:19], v[160:161]
	v_pk_mul_f32 v[14:15], v[14:15], v[156:157]
	v_pk_mul_f32 v[10:11], v[10:11], v[152:153]
	v_pk_mul_f32 v[6:7], v[6:7], v[148:149]
	v_pk_mul_f32 v[4:5], v[4:5], v[146:147]
	.p2align	6

.LBB0_2402:
	v_mov_b32_e32 v0, v143
	s_nop 1
	v_permlane32_swap_b32_e32 v143, v0
	v_cmp_gt_u32_e32 vcc, 32, v137
	s_barrier
	s_and_saveexec_b64 s[2:3], vcc
	s_cbranch_execz .LBB0_2395
	v_add_f32_e32 v0, v143, v0
	v_div_scale_f32 v1, s[4:5], v0, v0, 1.0
	v_rcp_f32_e32 v2, v1
	v_lshl_add_u32 v68, v139, 2, s33
	v_fma_f32 v69, -v1, v2, 1.0
	v_fmac_f32_e32 v2, v69, v2
	v_div_scale_f32 v69, vcc, 1.0, v0, 1.0
	v_mul_f32_e32 v70, v69, v2
	v_fma_f32 v71, -v1, v70, v69
	v_fmac_f32_e32 v70, v71, v2
	v_fma_f32 v1, -v1, v70, v69
	v_div_fmas_f32 v1, v1, v2, v70
	v_div_fixup_f32 v0, v1, v0, 1.0
	ds_write_b32 v68, v0
	s_branch .LBB0_2395
	.p2align	6

.LBB0_2405:
	s_ashr_i32 s0, s21, 6
	s_lshl_b32 s1, s0, 12
	s_lshl_b32 s2, s21, 8
	s_and_b32 s22, s2, 0xf00
	s_add_i32 s1, s1, s92
	v_mbcnt_lo_u32_b32 v0, -1, 0
	v_mbcnt_hi_u32_b32 v0, -1, v0
	s_add_i32 s1, s1, s22
	v_and_b32_e32 v139, 31, v0
	v_and_b32_e32 v137, 63, v0
	v_bfe_u32 v138, v0, 5, 1
	v_or_b32_e32 v0, s1, v139
	v_ashrrev_i32_e32 v1, 31, v0
	s_lshl_b32 s1, s21, 3
	v_lshlrev_b64 v[0:1], 10, v[0:1]
	s_and_b32 s23, s1, 0x180
	v_lshl_add_u64 v[0:1], s[28:29], 0, v[0:1]
	s_lshl_b32 s2, s23, 1
	s_mov_b32 s3, s11
	s_ashr_i32 s1, s0, 31
	v_lshl_add_u64 v[0:1], v[0:1], 0, s[2:3]
	v_lshlrev_b32_e32 v2, 4, v138
	s_lshl_b64 s[4:5], s[0:1], 19
	v_lshl_add_u64 v[0:1], v[0:1], 0, v[2:3]
	s_add_u32 s3, s13, s4
	v_mov_b32_e32 v4, v137
	global_load_dwordx4 v[100:103], v[0:1], off
	global_load_dwordx4 v[104:107], v[0:1], off offset:32
	global_load_dwordx4 v[108:111], v[0:1], off offset:64
	global_load_dwordx4 v[112:115], v[0:1], off offset:96
	global_load_dwordx4 v[116:119], v[0:1], off offset:128
	global_load_dwordx4 v[120:123], v[0:1], off offset:160
	global_load_dwordx4 v[124:127], v[0:1], off offset:192
	global_load_dwordx4 v[128:131], v[0:1], off offset:224
	s_addc_u32 s4, s20, s5
	s_add_u32 s2, s3, s2
	v_ashrrev_i32_e32 v0, 2, v4
	v_lshlrev_b32_e32 v1, 3, v4
	v_add_u32_e32 v0, s71, v0
	v_and_b32_e32 v14, 24, v1
	v_ashrrev_i32_e32 v5, 31, v4
	s_addc_u32 s3, s4, 0
	v_lshlrev_b32_e32 v2, 1, v14
	s_waitcnt vmcnt(0)
	v_lshlrev_b64 v[8:9], 11, v[4:5]
	v_ashrrev_i32_e32 v1, 31, v0
	v_readlane_b32 s14, v254, 36
	v_lshl_add_u64 v[6:7], s[2:3], 0, v[2:3]
	v_lshl_add_u64 v[8:9], s[2:3], 0, v[8:9]
	v_lshlrev_b64 v[0:1], 11, v[0:1]
	v_readlane_b32 s15, v254, 37
	s_mov_b32 m0, s91
	v_lshl_add_u64 v[0:1], v[6:7], 0, v[0:1]
	v_lshl_add_u64 v[6:7], v[8:9], 0, s[10:11]
	s_mov_b32 s15, s11
	v_readlane_b32 s30, v254, 38
	global_load_lds_dwordx4 v[6:7], off
	v_lshl_add_u64 v[6:7], v[0:1], 0, s[14:15]
	s_mov_b64 s[38:39], 0x400
	v_readlane_b32 s31, v254, 39
	v_readlane_b32 s34, v254, 40
	v_lshl_add_u64 v[6:7], v[6:7], 0, s[38:39]
	s_mov_b32 m0, s97
	s_mov_b32 s31, s11
	v_readlane_b32 s2, v254, 23
	v_readlane_b32 s35, v254, 41
	global_load_lds_dwordx4 v[6:7], off
	v_lshl_add_u64 v[6:7], v[8:9], 0, s[30:31]
	s_mov_b32 m0, s2
	s_mov_b32 s35, s11
	global_load_lds_dwordx4 v[6:7], off
	v_lshl_add_u64 v[6:7], v[0:1], 0, s[34:35]
	v_readlane_b32 s3, v253, 51
	v_lshl_add_u64 v[6:7], v[6:7], 0, s[38:39]
	s_add_i32 m0, s94, s3
	s_mov_b64 s[4:5], 0x20000
	global_load_lds_dwordx4 v[6:7], off
	v_lshl_add_u64 v[6:7], v[8:9], 0, s[4:5]
	v_readlane_b32 s2, v254, 24
	v_lshl_add_u64 v[10:11], v[0:1], 0, s[4:5]
	v_lshl_add_u64 v[12:13], v[6:7], 0, s[10:11]
	s_mov_b32 m0, s2
	s_add_i32 s2, 0, 0x14400
	global_load_lds_dwordx4 v[12:13], off
	v_lshl_add_u64 v[12:13], v[10:11], 0, s[14:15]
	v_readlane_b32 s4, v254, 2
	v_lshl_add_u64 v[12:13], v[12:13], 0, s[38:39]
	s_add_i32 m0, s2, s4
	v_readlane_b32 s5, v254, 25
	global_load_lds_dwordx4 v[12:13], off
	v_lshl_add_u64 v[6:7], v[6:7], 0, s[30:31]
	s_mov_b32 m0, s5
	s_mov_b64 s[36:37], 0x40000
	global_load_lds_dwordx4 v[6:7], off
	v_lshl_add_u64 v[6:7], v[10:11], 0, s[34:35]
	v_lshl_add_u64 v[6:7], v[6:7], 0, s[38:39]
	s_add_i32 m0, s2, s3
	v_readlane_b32 s2, v254, 30
	global_load_lds_dwordx4 v[6:7], off
	v_lshl_add_u64 v[6:7], v[8:9], 0, s[36:37]
	v_lshl_add_u64 v[10:11], v[0:1], 0, s[36:37]
	v_lshl_add_u64 v[12:13], v[6:7], 0, s[10:11]
	s_mov_b32 m0, s2
	v_readlane_b32 s2, v254, 31
	global_load_lds_dwordx4 v[12:13], off
	v_lshl_add_u64 v[12:13], v[10:11], 0, s[14:15]
	v_lshl_add_u64 v[12:13], v[12:13], 0, s[38:39]
	s_add_i32 m0, s2, s4
	v_readlane_b32 s5, v254, 32
	global_load_lds_dwordx4 v[12:13], off
	v_lshl_add_u64 v[6:7], v[6:7], 0, s[30:31]
	s_mov_b32 m0, s5
	s_mov_b64 s[36:37], 0x60000
	global_load_lds_dwordx4 v[6:7], off
	v_lshl_add_u64 v[6:7], v[10:11], 0, s[34:35]
	v_lshl_add_u64 v[6:7], v[6:7], 0, s[38:39]
	s_add_i32 m0, s2, s3
	v_readlane_b32 s2, v254, 33
	global_load_lds_dwordx4 v[6:7], off
	s_mov_b32 m0, s2
	s_mov_b32 s2, s14
	v_writelane_b32 v254, s2, 36
	v_lshl_add_u64 v[6:7], v[8:9], 0, s[36:37]
	v_lshl_add_u64 v[8:9], v[6:7], 0, s[10:11]
	v_writelane_b32 v254, s3, 37
	global_load_lds_dwordx4 v[8:9], off
	v_readlane_b32 s2, v254, 34
	s_add_i32 m0, s2, s4
	s_mov_b32 s4, s30
	v_lshl_add_u64 v[0:1], v[0:1], 0, s[36:37]
	v_writelane_b32 v254, s4, 38
	v_lshl_add_u64 v[8:9], v[0:1], 0, s[14:15]
	v_lshl_add_u64 v[8:9], v[8:9], 0, s[38:39]
	v_writelane_b32 v254, s5, 39
	global_load_lds_dwordx4 v[8:9], off
	v_readlane_b32 s4, v254, 35
	v_lshl_add_u64 v[6:7], v[6:7], 0, s[30:31]
	s_mov_b32 m0, s4
	v_lshl_add_u64 v[0:1], v[0:1], 0, s[34:35]
	global_load_lds_dwordx4 v[6:7], off
	v_lshl_add_u64 v[0:1], v[0:1], 0, s[38:39]
	s_add_i32 m0, s2, s3
	s_mov_b32 s4, s34
	global_load_lds_dwordx4 v[0:1], off
	v_and_b32_e32 v5, 31, v4
	v_ashrrev_i32_e32 v6, 5, v4
	v_cmp_gt_u32_e64 s[34:35], 32, v4
	v_lshlrev_b32_e32 v8, 1, v4
	v_lshlrev_b32_e32 v4, 4, v4
	s_movk_i32 s2, 0x410
	v_and_b32_e32 v4, 0xc0, v4
	v_mul_lo_u32 v7, v6, s2
	v_lshlrev_b32_e32 v20, 4, v6
	v_and_b32_e32 v8, 32, v8
	v_lshl_or_b32 v4, v6, 8, v4
	v_mov_b32_e32 v18, v3
	v_mov_b32_e32 v19, v3
	v_writelane_b32 v254, s4, 40
	v_lshl_add_u32 v140, v5, 2, s33
	v_or3_b32 v141, v4, v8, v14
	v_lshl_add_u32 v142, v5, 4, v7
	v_mov_b32_e32 v4, v3
	v_mov_b32_e32 v5, v3
	v_mov_b32_e32 v6, v3
	v_mov_b32_e32 v7, v3
	v_mov_b32_e32 v8, v3
	v_mov_b32_e32 v9, v3
	v_mov_b32_e32 v10, v3
	v_mov_b32_e32 v11, v3
	v_mov_b32_e32 v12, v3
	v_mov_b32_e32 v13, v3
	v_mov_b32_e32 v14, v3
	v_mov_b32_e32 v15, v3
	v_mov_b32_e32 v16, v3
	v_mov_b32_e32 v17, v3
	v_add_u32_e32 v144, s33, v20
	v_mov_b64_e32 v[34:35], v[18:19]
	v_mov_b64_e32 v[50:51], v[18:19]
	v_mov_b64_e32 v[66:67], v[18:19]
	v_writelane_b32 v254, s5, 41
	s_mov_b32 s15, 4
	v_cndmask_b32_e64 v0, v212, 0, s[34:35]
	v_cndmask_b32_e64 v1, v213, 0, s[34:35]
	v_mov_b32_e32 v2, v3
	v_mov_b32_e32 v132, v3
	v_mov_b32_e32 v133, v3
	v_mov_b32_e32 v134, v3
	v_mov_b32_e32 v135, v3
	s_mov_b64 s[36:37], -1
	v_mov_b32_e32 v143, 0
	v_mov_b64_e32 v[32:33], v[16:17]
	v_mov_b64_e32 v[30:31], v[14:15]
	v_mov_b64_e32 v[28:29], v[12:13]
	v_mov_b64_e32 v[26:27], v[10:11]
	v_mov_b64_e32 v[24:25], v[8:9]
	v_mov_b64_e32 v[22:23], v[6:7]
	v_mov_b64_e32 v[20:21], v[4:5]
	v_mov_b64_e32 v[48:49], v[16:17]
	v_mov_b64_e32 v[46:47], v[14:15]
	v_mov_b64_e32 v[44:45], v[12:13]
	v_mov_b64_e32 v[42:43], v[10:11]
	v_mov_b64_e32 v[40:41], v[8:9]
	v_mov_b64_e32 v[38:39], v[6:7]
	v_mov_b64_e32 v[36:37], v[4:5]
	v_mov_b64_e32 v[64:65], v[16:17]
	v_mov_b64_e32 v[62:63], v[14:15]
	v_mov_b64_e32 v[60:61], v[12:13]
	v_mov_b64_e32 v[58:59], v[10:11]
	v_mov_b64_e32 v[56:57], v[8:9]
	v_mov_b64_e32 v[54:55], v[6:7]
	v_mov_b64_e32 v[52:53], v[4:5]
	v_mov_b32_e32 v145, 0
	s_waitcnt vmcnt(0) lgkmcnt(0)
	s_barrier
	s_branch .LBB0_2408
	.p2align	6

.LBB0_2484:
	s_add_u32 s40, s6, 0x6f1c8000
	s_addc_u32 s41, s7, 0
	s_add_i32 m0, s31, 0x18000
	v_lshl_add_u64 v[4:5], v[4:5], 0, s[24:25]
	s_waitcnt vmcnt(2)
	s_barrier
	global_load_lds_dwordx4 v[4:5], off
	v_lshl_add_u64 v[4:5], v[6:7], 0, s[24:25]
	s_add_i32 m0, s31, 0x1a000
	s_add_i32 s58, s31, 0x8000
	global_load_lds_dwordx4 v[4:5], off
	v_lshl_add_u64 v[4:5], v[12:13], 0, s[24:25]
	s_mov_b32 m0, s58
	s_add_i32 s59, s31, 0xa000
	global_load_lds_dwordx4 v[4:5], off
	v_lshl_add_u64 v[4:5], v[14:15], 0, s[24:25]
	s_mov_b32 m0, s59
	s_lshr_b32 s5, s5, 26
	global_load_lds_dwordx4 v[4:5], off
	s_add_i32 m0, s31, 0x1c000
	v_lshl_add_u64 v[4:5], v[8:9], 0, s[24:25]
	global_load_lds_dwordx4 v[4:5], off
	v_lshl_add_u64 v[4:5], v[10:11], 0, s[24:25]
	s_add_i32 m0, s31, 0x1e000
	s_movk_i32 s6, 0x3c0
	global_load_lds_dwordx4 v[4:5], off
	v_and_b32_e32 v4, 48, v2
	v_lshlrev_b32_e32 v5, 6, v2
	s_add_i32 s5, s4, s5
	v_and_or_b32 v4, v5, s6, v4
	v_lshlrev_b32_e32 v5, 2, v2
	s_ashr_i32 s60, s5, 6
	s_lshl_b32 s5, s35, 13
	v_and_b32_e32 v5, 32, v5
	v_bitop3_b32 v6, v4, s5, v5 bitop3:0xde
	s_lshl_b32 s5, s42, 5
	s_and_b32 s5, s5, 0x60
	s_lshl_b32 s6, s5, 7
	v_bitop3_b32 v144, s6, v4, v5 bitop3:0xf6
	v_bfe_u32 v4, v2, 2, 4
	v_lshl_or_b32 v146, s35, 6, v4
	v_lshlrev_b32_e32 v4, 13, v20
	v_and_b32_e32 v5, 3, v2
	v_and_b32_e32 v2, 60, v2
	v_and_b32_e32 v4, 0xffffc000, v4
	v_lshl_or_b32 v145, v5, 6, v2
	v_lshlrev_b32_e32 v2, 3, v5
	v_lshl_add_u32 v4, v19, 10, v4
	v_and_b32_e32 v5, 1, v20
	v_lshl_or_b32 v4, v5, 6, v4
	s_sext_i32_i8 s47, s8
	s_ashr_i32 s8, s13, 31
	v_lshl_add_u32 v138, v21, 1, v4
	v_lshlrev_b32_e32 v4, 13, v16
	s_cmp_gt_i32 s4, 63
	v_and_b32_e32 v4, 0xffffc000, v4
	s_waitcnt vmcnt(6)
	s_cselect_b64 s[42:43], -1, 0
	s_add_i32 s61, s60, -2
	v_lshl_add_u32 v4, v17, 10, v4
	v_and_b32_e32 v5, 1, v16
	s_cmpk_lt_u32 s34, 0x100
	v_lshl_or_b32 v4, v5, 6, v4
	s_cselect_b64 s[44:45], -1, 0
	v_mov_b32_e32 v139, v3
	v_lshl_add_u32 v140, v18, 1, v4
	v_mov_b32_e32 v141, v3
	s_mov_b32 s62, 0
	v_add_u32_e32 v147, 0, v6
	s_lshl_b32 s46, s5, 1
	v_lshlrev_b32_e32 v2, 1, v2
	s_barrier
	s_branch .LBB0_2487
	.p2align	6

.LBB0_2496:
	s_ashr_i32 s49, s48, 31
	s_lshl_b64 s[6:7], s[48:49], 18
	s_add_u32 s54, s15, s6
	v_mov_b32_e32 v127, 0
	s_addc_u32 s55, s20, s7
	s_andn2_b64 vcc, exec, s[42:43]
	v_mov_b32_e32 v126, v127
	v_mov_b32_e32 v125, v127
	v_mov_b32_e32 v124, v127
	v_mov_b32_e32 v131, v127
	v_mov_b32_e32 v130, v127
	v_mov_b32_e32 v129, v127
	v_mov_b32_e32 v128, v127
	v_mov_b32_e32 v115, v127
	v_mov_b32_e32 v114, v127
	v_mov_b32_e32 v113, v127
	v_mov_b32_e32 v112, v127
	v_mov_b32_e32 v111, v127
	v_mov_b32_e32 v110, v127
	v_mov_b32_e32 v109, v127
	v_mov_b32_e32 v108, v127
	v_mov_b32_e32 v99, v127
	v_mov_b32_e32 v98, v127
	v_mov_b32_e32 v97, v127
	v_mov_b32_e32 v96, v127
	v_mov_b32_e32 v95, v127
	v_mov_b32_e32 v94, v127
	v_mov_b32_e32 v93, v127
	v_mov_b32_e32 v92, v127
	v_mov_b32_e32 v83, v127
	v_mov_b32_e32 v82, v127
	v_mov_b32_e32 v81, v127
	v_mov_b32_e32 v80, v127
	v_mov_b32_e32 v79, v127
	v_mov_b32_e32 v78, v127
	v_mov_b32_e32 v77, v127
	v_mov_b32_e32 v76, v127
	v_mov_b32_e32 v123, v127
	v_mov_b32_e32 v122, v127
	v_mov_b32_e32 v121, v127
	v_mov_b32_e32 v120, v127
	v_mov_b32_e32 v119, v127
	v_mov_b32_e32 v118, v127
	v_mov_b32_e32 v117, v127
	v_mov_b32_e32 v116, v127
	v_mov_b32_e32 v107, v127
	v_mov_b32_e32 v106, v127
	v_mov_b32_e32 v105, v127
	v_mov_b32_e32 v104, v127
	v_mov_b32_e32 v103, v127
	v_mov_b32_e32 v102, v127
	v_mov_b32_e32 v101, v127
	v_mov_b32_e32 v100, v127
	v_mov_b32_e32 v91, v127
	v_mov_b32_e32 v90, v127
	v_mov_b32_e32 v89, v127
	v_mov_b32_e32 v88, v127
	v_mov_b32_e32 v87, v127
	v_mov_b32_e32 v86, v127
	v_mov_b32_e32 v85, v127
	v_mov_b32_e32 v84, v127
	v_mov_b32_e32 v75, v127
	v_mov_b32_e32 v74, v127
	v_mov_b32_e32 v73, v127
	v_mov_b32_e32 v72, v127
	v_mov_b32_e32 v71, v127
	v_mov_b32_e32 v70, v127
	v_mov_b32_e32 v69, v127
	v_mov_b32_e32 v68, v127
	v_mov_b32_e32 v67, v127
	v_mov_b32_e32 v66, v127
	v_mov_b32_e32 v65, v127
	v_mov_b32_e32 v64, v127
	v_mov_b32_e32 v63, v127
	v_mov_b32_e32 v62, v127
	v_mov_b32_e32 v61, v127
	v_mov_b32_e32 v60, v127
	v_mov_b32_e32 v51, v127
	v_mov_b32_e32 v50, v127
	v_mov_b32_e32 v49, v127
	v_mov_b32_e32 v48, v127
	v_mov_b32_e32 v47, v127
	v_mov_b32_e32 v46, v127
	v_mov_b32_e32 v45, v127
	v_mov_b32_e32 v44, v127
	v_mov_b32_e32 v35, v127
	v_mov_b32_e32 v34, v127
	v_mov_b32_e32 v33, v127
	v_mov_b32_e32 v32, v127
	v_mov_b32_e32 v31, v127
	v_mov_b32_e32 v30, v127
	v_mov_b32_e32 v29, v127
	v_mov_b32_e32 v28, v127
	v_mov_b32_e32 v19, v127
	v_mov_b32_e32 v18, v127
	v_mov_b32_e32 v17, v127
	v_mov_b32_e32 v16, v127
	v_mov_b32_e32 v15, v127
	v_mov_b32_e32 v14, v127
	v_mov_b32_e32 v13, v127
	v_mov_b32_e32 v12, v127
	v_mov_b32_e32 v59, v127
	v_mov_b32_e32 v58, v127
	v_mov_b32_e32 v57, v127
	v_mov_b32_e32 v56, v127
	v_mov_b32_e32 v55, v127
	v_mov_b32_e32 v54, v127
	v_mov_b32_e32 v53, v127
	v_mov_b32_e32 v52, v127
	v_mov_b32_e32 v43, v127
	v_mov_b32_e32 v42, v127
	v_mov_b32_e32 v41, v127
	v_mov_b32_e32 v40, v127
	v_mov_b32_e32 v39, v127
	v_mov_b32_e32 v38, v127
	v_mov_b32_e32 v37, v127
	v_mov_b32_e32 v36, v127
	v_mov_b32_e32 v27, v127
	v_mov_b32_e32 v26, v127
	v_mov_b32_e32 v25, v127
	v_mov_b32_e32 v24, v127
	v_mov_b32_e32 v23, v127
	v_mov_b32_e32 v22, v127
	v_mov_b32_e32 v21, v127
	v_mov_b32_e32 v20, v127
	v_mov_b32_e32 v11, v127
	v_mov_b32_e32 v10, v127
	v_mov_b32_e32 v9, v127
	v_mov_b32_e32 v8, v127
	v_mov_b32_e32 v7, v127
	v_mov_b32_e32 v6, v127
	v_mov_b32_e32 v5, v127
	v_mov_b32_e32 v4, v127
	s_cbranch_vccnz .LBB0_2500
	s_and_b64 s[4:5], s[4:5], exec
	s_cselect_b32 s4, s55, s1
	s_cselect_b32 s5, s54, s0
	s_add_u32 s0, s0, 0x20080
	s_addc_u32 s1, s1, 0
	s_add_u32 s6, s2, 0x100
	v_mov_b32_e32 v4, 0
	s_addc_u32 s7, s3, 0
	s_mov_b32 s2, 0
	v_mov_b32_e32 v5, v4
	v_mov_b32_e32 v6, v4
	v_mov_b32_e32 v7, v4
	v_mov_b32_e32 v8, v4
	v_mov_b32_e32 v9, v4
	v_mov_b32_e32 v10, v4
	v_mov_b32_e32 v11, v4
	v_mov_b32_e32 v20, v4
	v_mov_b32_e32 v21, v4
	v_mov_b32_e32 v22, v4
	v_mov_b32_e32 v23, v4
	v_mov_b32_e32 v24, v4
	v_mov_b32_e32 v25, v4
	v_mov_b32_e32 v26, v4
	v_mov_b32_e32 v27, v4
	v_mov_b32_e32 v36, v4
	v_mov_b32_e32 v37, v4
	v_mov_b32_e32 v38, v4
	v_mov_b32_e32 v39, v4
	v_mov_b32_e32 v40, v4
	v_mov_b32_e32 v41, v4
	v_mov_b32_e32 v42, v4
	v_mov_b32_e32 v43, v4
	v_mov_b32_e32 v52, v4
	v_mov_b32_e32 v53, v4
	v_mov_b32_e32 v54, v4
	v_mov_b32_e32 v55, v4
	v_mov_b32_e32 v56, v4
	v_mov_b32_e32 v57, v4
	v_mov_b32_e32 v58, v4
	v_mov_b32_e32 v59, v4
	v_mov_b32_e32 v12, v4
	v_mov_b32_e32 v13, v4
	v_mov_b32_e32 v14, v4
	v_mov_b32_e32 v15, v4
	v_mov_b32_e32 v16, v4
	v_mov_b32_e32 v17, v4
	v_mov_b32_e32 v18, v4
	v_mov_b32_e32 v19, v4
	v_mov_b32_e32 v28, v4
	v_mov_b32_e32 v29, v4
	v_mov_b32_e32 v30, v4
	v_mov_b32_e32 v31, v4
	v_mov_b32_e32 v32, v4
	v_mov_b32_e32 v33, v4
	v_mov_b32_e32 v34, v4
	v_mov_b32_e32 v35, v4
	v_mov_b32_e32 v44, v4
	v_mov_b32_e32 v45, v4
	v_mov_b32_e32 v46, v4
	v_mov_b32_e32 v47, v4
	v_mov_b32_e32 v48, v4
	v_mov_b32_e32 v49, v4
	v_mov_b32_e32 v50, v4
	v_mov_b32_e32 v51, v4
	v_mov_b32_e32 v60, v4
	v_mov_b32_e32 v61, v4
	v_mov_b32_e32 v62, v4
	v_mov_b32_e32 v63, v4
	v_mov_b32_e32 v64, v4
	v_mov_b32_e32 v65, v4
	v_mov_b32_e32 v66, v4
	v_mov_b32_e32 v67, v4
	v_mov_b32_e32 v68, v4
	v_mov_b32_e32 v69, v4
	v_mov_b32_e32 v70, v4
	v_mov_b32_e32 v71, v4
	v_mov_b32_e32 v72, v4
	v_mov_b32_e32 v73, v4
	v_mov_b32_e32 v74, v4
	v_mov_b32_e32 v75, v4
	v_mov_b32_e32 v84, v4
	v_mov_b32_e32 v85, v4
	v_mov_b32_e32 v86, v4
	v_mov_b32_e32 v87, v4
	v_mov_b32_e32 v88, v4
	v_mov_b32_e32 v89, v4
	v_mov_b32_e32 v90, v4
	v_mov_b32_e32 v91, v4
	v_mov_b32_e32 v100, v4
	v_mov_b32_e32 v101, v4
	v_mov_b32_e32 v102, v4
	v_mov_b32_e32 v103, v4
	v_mov_b32_e32 v104, v4
	v_mov_b32_e32 v105, v4
	v_mov_b32_e32 v106, v4
	v_mov_b32_e32 v107, v4
	v_mov_b32_e32 v116, v4
	v_mov_b32_e32 v117, v4
	v_mov_b32_e32 v118, v4
	v_mov_b32_e32 v119, v4
	v_mov_b32_e32 v120, v4
	v_mov_b32_e32 v121, v4
	v_mov_b32_e32 v122, v4
	v_mov_b32_e32 v123, v4
	v_mov_b32_e32 v76, v4
	v_mov_b32_e32 v77, v4
	v_mov_b32_e32 v78, v4
	v_mov_b32_e32 v79, v4
	v_mov_b32_e32 v80, v4
	v_mov_b32_e32 v81, v4
	v_mov_b32_e32 v82, v4
	v_mov_b32_e32 v83, v4
	v_mov_b32_e32 v92, v4
	v_mov_b32_e32 v93, v4
	v_mov_b32_e32 v94, v4
	v_mov_b32_e32 v95, v4
	v_mov_b32_e32 v96, v4
	v_mov_b32_e32 v97, v4
	v_mov_b32_e32 v98, v4
	v_mov_b32_e32 v99, v4
	v_mov_b32_e32 v108, v4
	v_mov_b32_e32 v109, v4
	v_mov_b32_e32 v110, v4
	v_mov_b32_e32 v111, v4
	v_mov_b32_e32 v112, v4
	v_mov_b32_e32 v113, v4
	v_mov_b32_e32 v114, v4
	v_mov_b32_e32 v115, v4
	v_mov_b32_e32 v128, v4
	v_mov_b32_e32 v129, v4
	v_mov_b32_e32 v130, v4
	v_mov_b32_e32 v131, v4
	v_mov_b32_e32 v124, v4
	v_mov_b32_e32 v125, v4
	v_mov_b32_e32 v126, v4
	v_mov_b32_e32 v127, v4
	.p2align	6

.LBB0_2653:
	s_add_i32 s15, s56, 11
	s_cmp_ge_i32 s15, s79
	s_cbranch_scc1 .LBB0_2719
	.p2align	6

.LBB0_2670:
	s_add_u32 s42, s4, 0x79dc8000
	s_addc_u32 s43, s5, 0
	s_add_i32 m0, s30, 0x18000
	v_lshl_add_u64 v[4:5], v[4:5], 0, s[24:25]
	s_waitcnt vmcnt(2)
	s_barrier
	global_load_lds_dwordx4 v[4:5], off
	v_lshl_add_u64 v[4:5], v[6:7], 0, s[24:25]
	s_add_i32 m0, s30, 0x1a000
	s_add_i32 s58, s30, 0x8000
	global_load_lds_dwordx4 v[4:5], off
	v_lshl_add_u64 v[4:5], v[12:13], 0, s[24:25]
	s_mov_b32 m0, s58
	s_add_i32 s59, s30, 0xa000
	global_load_lds_dwordx4 v[4:5], off
	v_lshl_add_u64 v[4:5], v[14:15], 0, s[24:25]
	s_mov_b32 m0, s59
	s_lshr_b32 s7, s7, 26
	global_load_lds_dwordx4 v[4:5], off
	s_add_i32 m0, s30, 0x1c000
	v_lshl_add_u64 v[4:5], v[8:9], 0, s[24:25]
	global_load_lds_dwordx4 v[4:5], off
	v_lshl_add_u64 v[4:5], v[10:11], 0, s[24:25]
	s_add_i32 m0, s30, 0x1e000
	v_and_b32_e32 v139, 15, v2
	global_load_lds_dwordx4 v[4:5], off
	v_bfe_u32 v4, v2, 4, 2
	s_add_i32 s7, s6, s7
	v_lshlrev_b32_e32 v5, 4, v4
	v_lshlrev_b32_e32 v6, 2, v2
	s_ashr_i32 s61, s7, 6
	v_lshl_or_b32 v5, v139, 6, v5
	s_lshl_b32 s7, s35, 13
	v_and_b32_e32 v6, 32, v6
	v_bitop3_b32 v7, v5, s7, v6 bitop3:0xde
	s_lshl_b32 s7, s44, 5
	s_and_b32 s63, s7, 0x60
	s_ashr_i32 s60, s12, 31
	s_lshl_b32 s62, s35, 6
	s_lshl_b32 s7, s63, 7
	s_cmp_gt_i32 s6, 63
	s_cselect_b64 s[44:45], -1, 0
	s_add_i32 s64, s61, -2
	s_cmpk_lt_u32 s34, 0x100
	s_cselect_b64 s[46:47], -1, 0
	s_lshl_b32 s6, s63, 2
	v_bitop3_b32 v146, v5, s7, v6 bitop3:0xde
	v_bfe_u32 v147, v2, 2, 4
	v_and_b32_e32 v5, 3, v2
	v_and_b32_e32 v2, 60, v2
	s_add_u32 s4, s4, s6
	v_lshl_or_b32 v148, v5, 6, v2
	s_addc_u32 s5, s5, 0
	v_lshlrev_b32_e32 v2, 5, v4
	v_lshlrev_b32_e32 v138, 3, v5
	v_lshl_add_u64 v[4:5], s[4:5], 0, v[2:3]
	v_lshlrev_b32_e32 v2, 14, v16
	s_mov_b64 s[4:5], 0x77dc8000
	v_and_b32_e32 v2, 0xffff8000, v2
	v_lshl_add_u64 v[140:141], v[4:5], 0, s[4:5]
	v_lshl_add_u32 v2, v17, 11, v2
	v_and_b32_e32 v4, 1, v16
	v_lshl_or_b32 v2, v4, 6, v2
	v_lshl_add_u32 v142, v18, 1, v2
	v_lshlrev_b32_e32 v2, 14, v19
	v_and_b32_e32 v2, 0xffff8000, v2
	s_waitcnt vmcnt(6)
	v_lshl_add_u32 v2, v20, 11, v2
	v_and_b32_e32 v4, 1, v19
	v_lshl_or_b32 v2, v4, 6, v2
	v_mov_b32_e32 v143, v3
	v_lshl_add_u32 v144, v21, 1, v2
	v_mov_b32_e32 v145, v3
	s_mov_b32 s65, 0
	v_add_u32_e32 v149, 0, v7
	s_barrier
	s_branch .LBB0_2673
	.p2align	6

.LBB0_2678:
	s_ashr_i32 s49, s48, 31
	s_lshl_b64 s[6:7], s[48:49], 19
	s_add_u32 s52, s15, s6
	v_mov_b32_e32 v131, 0
	s_addc_u32 s53, s20, s7
	s_andn2_b64 vcc, exec, s[44:45]
	v_mov_b32_e32 v130, v131
	v_mov_b32_e32 v129, v131
	v_mov_b32_e32 v128, v131
	v_mov_b32_e32 v127, v131
	v_mov_b32_e32 v126, v131
	v_mov_b32_e32 v125, v131
	v_mov_b32_e32 v124, v131
	v_mov_b32_e32 v115, v131
	v_mov_b32_e32 v114, v131
	v_mov_b32_e32 v113, v131
	v_mov_b32_e32 v112, v131
	v_mov_b32_e32 v111, v131
	v_mov_b32_e32 v110, v131
	v_mov_b32_e32 v109, v131
	v_mov_b32_e32 v108, v131
	v_mov_b32_e32 v99, v131
	v_mov_b32_e32 v98, v131
	v_mov_b32_e32 v97, v131
	v_mov_b32_e32 v96, v131
	v_mov_b32_e32 v95, v131
	v_mov_b32_e32 v94, v131
	v_mov_b32_e32 v93, v131
	v_mov_b32_e32 v92, v131
	v_mov_b32_e32 v83, v131
	v_mov_b32_e32 v82, v131
	v_mov_b32_e32 v81, v131
	v_mov_b32_e32 v80, v131
	v_mov_b32_e32 v79, v131
	v_mov_b32_e32 v78, v131
	v_mov_b32_e32 v77, v131
	v_mov_b32_e32 v76, v131
	v_mov_b32_e32 v123, v131
	v_mov_b32_e32 v122, v131
	v_mov_b32_e32 v121, v131
	v_mov_b32_e32 v120, v131
	v_mov_b32_e32 v119, v131
	v_mov_b32_e32 v118, v131
	v_mov_b32_e32 v117, v131
	v_mov_b32_e32 v116, v131
	v_mov_b32_e32 v107, v131
	v_mov_b32_e32 v106, v131
	v_mov_b32_e32 v105, v131
	v_mov_b32_e32 v104, v131
	v_mov_b32_e32 v103, v131
	v_mov_b32_e32 v102, v131
	v_mov_b32_e32 v101, v131
	v_mov_b32_e32 v100, v131
	v_mov_b32_e32 v91, v131
	v_mov_b32_e32 v90, v131
	v_mov_b32_e32 v89, v131
	v_mov_b32_e32 v88, v131
	v_mov_b32_e32 v87, v131
	v_mov_b32_e32 v86, v131
	v_mov_b32_e32 v85, v131
	v_mov_b32_e32 v84, v131
	v_mov_b32_e32 v75, v131
	v_mov_b32_e32 v74, v131
	v_mov_b32_e32 v73, v131
	v_mov_b32_e32 v72, v131
	v_mov_b32_e32 v71, v131
	v_mov_b32_e32 v70, v131
	v_mov_b32_e32 v69, v131
	v_mov_b32_e32 v68, v131
	v_mov_b32_e32 v67, v131
	v_mov_b32_e32 v66, v131
	v_mov_b32_e32 v65, v131
	v_mov_b32_e32 v64, v131
	v_mov_b32_e32 v63, v131
	v_mov_b32_e32 v62, v131
	v_mov_b32_e32 v61, v131
	v_mov_b32_e32 v60, v131
	v_mov_b32_e32 v51, v131
	v_mov_b32_e32 v50, v131
	v_mov_b32_e32 v49, v131
	v_mov_b32_e32 v48, v131
	v_mov_b32_e32 v47, v131
	v_mov_b32_e32 v46, v131
	v_mov_b32_e32 v45, v131
	v_mov_b32_e32 v44, v131
	v_mov_b32_e32 v35, v131
	v_mov_b32_e32 v34, v131
	v_mov_b32_e32 v33, v131
	v_mov_b32_e32 v32, v131
	v_mov_b32_e32 v31, v131
	v_mov_b32_e32 v30, v131
	v_mov_b32_e32 v29, v131
	v_mov_b32_e32 v28, v131
	v_mov_b32_e32 v19, v131
	v_mov_b32_e32 v18, v131
	v_mov_b32_e32 v17, v131
	v_mov_b32_e32 v16, v131
	v_mov_b32_e32 v15, v131
	v_mov_b32_e32 v14, v131
	v_mov_b32_e32 v13, v131
	v_mov_b32_e32 v12, v131
	v_mov_b32_e32 v59, v131
	v_mov_b32_e32 v58, v131
	v_mov_b32_e32 v57, v131
	v_mov_b32_e32 v56, v131
	v_mov_b32_e32 v55, v131
	v_mov_b32_e32 v54, v131
	v_mov_b32_e32 v53, v131
	v_mov_b32_e32 v52, v131
	v_mov_b32_e32 v43, v131
	v_mov_b32_e32 v42, v131
	v_mov_b32_e32 v41, v131
	v_mov_b32_e32 v40, v131
	v_mov_b32_e32 v39, v131
	v_mov_b32_e32 v38, v131
	v_mov_b32_e32 v37, v131
	v_mov_b32_e32 v36, v131
	v_mov_b32_e32 v27, v131
	v_mov_b32_e32 v26, v131
	v_mov_b32_e32 v25, v131
	v_mov_b32_e32 v24, v131
	v_mov_b32_e32 v23, v131
	v_mov_b32_e32 v22, v131
	v_mov_b32_e32 v21, v131
	v_mov_b32_e32 v20, v131
	v_mov_b32_e32 v11, v131
	v_mov_b32_e32 v10, v131
	v_mov_b32_e32 v9, v131
	v_mov_b32_e32 v8, v131
	v_mov_b32_e32 v7, v131
	v_mov_b32_e32 v6, v131
	v_mov_b32_e32 v5, v131
	v_mov_b32_e32 v4, v131
	s_cbranch_vccnz .LBB0_2681
	s_and_b64 s[4:5], s[4:5], exec
	s_cselect_b32 s4, s53, s1
	s_cselect_b32 s5, s52, s0
	s_add_u32 s0, s0, 0x40080
	s_addc_u32 s1, s1, 0
	s_add_u32 s6, s2, 0x100
	v_mov_b32_e32 v4, 0
	s_addc_u32 s7, s3, 0
	s_mov_b32 s2, 0
	v_mov_b32_e32 v5, v4
	v_mov_b32_e32 v6, v4
	v_mov_b32_e32 v7, v4
	v_mov_b32_e32 v8, v4
	v_mov_b32_e32 v9, v4
	v_mov_b32_e32 v10, v4
	v_mov_b32_e32 v11, v4
	v_mov_b32_e32 v20, v4
	v_mov_b32_e32 v21, v4
	v_mov_b32_e32 v22, v4
	v_mov_b32_e32 v23, v4
	v_mov_b32_e32 v24, v4
	v_mov_b32_e32 v25, v4
	v_mov_b32_e32 v26, v4
	v_mov_b32_e32 v27, v4
	v_mov_b32_e32 v36, v4
	v_mov_b32_e32 v37, v4
	v_mov_b32_e32 v38, v4
	v_mov_b32_e32 v39, v4
	v_mov_b32_e32 v40, v4
	v_mov_b32_e32 v41, v4
	v_mov_b32_e32 v42, v4
	v_mov_b32_e32 v43, v4
	v_mov_b32_e32 v52, v4
	v_mov_b32_e32 v53, v4
	v_mov_b32_e32 v54, v4
	v_mov_b32_e32 v55, v4
	v_mov_b32_e32 v56, v4
	v_mov_b32_e32 v57, v4
	v_mov_b32_e32 v58, v4
	v_mov_b32_e32 v59, v4
	v_mov_b32_e32 v12, v4
	v_mov_b32_e32 v13, v4
	v_mov_b32_e32 v14, v4
	v_mov_b32_e32 v15, v4
	v_mov_b32_e32 v16, v4
	v_mov_b32_e32 v17, v4
	v_mov_b32_e32 v18, v4
	v_mov_b32_e32 v19, v4
	v_mov_b32_e32 v28, v4
	v_mov_b32_e32 v29, v4
	v_mov_b32_e32 v30, v4
	v_mov_b32_e32 v31, v4
	v_mov_b32_e32 v32, v4
	v_mov_b32_e32 v33, v4
	v_mov_b32_e32 v34, v4
	v_mov_b32_e32 v35, v4
	v_mov_b32_e32 v44, v4
	v_mov_b32_e32 v45, v4
	v_mov_b32_e32 v46, v4
	v_mov_b32_e32 v47, v4
	v_mov_b32_e32 v48, v4
	v_mov_b32_e32 v49, v4
	v_mov_b32_e32 v50, v4
	v_mov_b32_e32 v51, v4
	v_mov_b32_e32 v60, v4
	v_mov_b32_e32 v61, v4
	v_mov_b32_e32 v62, v4
	v_mov_b32_e32 v63, v4
	v_mov_b32_e32 v64, v4
	v_mov_b32_e32 v65, v4
	v_mov_b32_e32 v66, v4
	v_mov_b32_e32 v67, v4
	v_mov_b32_e32 v68, v4
	v_mov_b32_e32 v69, v4
	v_mov_b32_e32 v70, v4
	v_mov_b32_e32 v71, v4
	v_mov_b32_e32 v72, v4
	v_mov_b32_e32 v73, v4
	v_mov_b32_e32 v74, v4
	v_mov_b32_e32 v75, v4
	v_mov_b32_e32 v84, v4
	v_mov_b32_e32 v85, v4
	v_mov_b32_e32 v86, v4
	v_mov_b32_e32 v87, v4
	v_mov_b32_e32 v88, v4
	v_mov_b32_e32 v89, v4
	v_mov_b32_e32 v90, v4
	v_mov_b32_e32 v91, v4
	v_mov_b32_e32 v100, v4
	v_mov_b32_e32 v101, v4
	v_mov_b32_e32 v102, v4
	v_mov_b32_e32 v103, v4
	v_mov_b32_e32 v104, v4
	v_mov_b32_e32 v105, v4
	v_mov_b32_e32 v106, v4
	v_mov_b32_e32 v107, v4
	v_mov_b32_e32 v116, v4
	v_mov_b32_e32 v117, v4
	v_mov_b32_e32 v118, v4
	v_mov_b32_e32 v119, v4
	v_mov_b32_e32 v120, v4
	v_mov_b32_e32 v121, v4
	v_mov_b32_e32 v122, v4
	v_mov_b32_e32 v123, v4
	v_mov_b32_e32 v76, v4
	v_mov_b32_e32 v77, v4
	v_mov_b32_e32 v78, v4
	v_mov_b32_e32 v79, v4
	v_mov_b32_e32 v80, v4
	v_mov_b32_e32 v81, v4
	v_mov_b32_e32 v82, v4
	v_mov_b32_e32 v83, v4
	v_mov_b32_e32 v92, v4
	v_mov_b32_e32 v93, v4
	v_mov_b32_e32 v94, v4
	v_mov_b32_e32 v95, v4
	v_mov_b32_e32 v96, v4
	v_mov_b32_e32 v97, v4
	v_mov_b32_e32 v98, v4
	v_mov_b32_e32 v99, v4
	v_mov_b32_e32 v108, v4
	v_mov_b32_e32 v109, v4
	v_mov_b32_e32 v110, v4
	v_mov_b32_e32 v111, v4
	v_mov_b32_e32 v112, v4
	v_mov_b32_e32 v113, v4
	v_mov_b32_e32 v114, v4
	v_mov_b32_e32 v115, v4
	v_mov_b32_e32 v124, v4
	v_mov_b32_e32 v125, v4
	v_mov_b32_e32 v126, v4
	v_mov_b32_e32 v127, v4
	v_mov_b32_e32 v128, v4
	v_mov_b32_e32 v129, v4
	v_mov_b32_e32 v130, v4
	v_mov_b32_e32 v131, v4
	.p2align	6

.LBB0_2779:
	s_add_u32 s42, s28, 0x6f1c8000
	s_addc_u32 s43, s29, 0
	s_add_i32 m0, s31, 0x18000
	v_lshl_add_u64 v[4:5], v[4:5], 0, s[24:25]
	s_waitcnt vmcnt(2)
	s_barrier
	global_load_lds_dwordx4 v[4:5], off
	v_lshl_add_u64 v[4:5], v[6:7], 0, s[24:25]
	s_add_i32 m0, s31, 0x1a000
	s_add_i32 s60, s31, 0x8000
	global_load_lds_dwordx4 v[4:5], off
	v_lshl_add_u64 v[4:5], v[12:13], 0, s[24:25]
	s_mov_b32 m0, s60
	s_add_i32 s61, s31, 0xa000
	global_load_lds_dwordx4 v[4:5], off
	v_lshl_add_u64 v[4:5], v[14:15], 0, s[24:25]
	s_mov_b32 m0, s61
	s_sext_i32_i8 s49, s6
	global_load_lds_dwordx4 v[4:5], off
	s_add_i32 m0, s31, 0x1c000
	v_lshl_add_u64 v[4:5], v[8:9], 0, s[24:25]
	global_load_lds_dwordx4 v[4:5], off
	v_lshl_add_u64 v[4:5], v[10:11], 0, s[24:25]
	s_add_i32 m0, s31, 0x1e000
	v_and_b32_e32 v1, 48, v2
	global_load_lds_dwordx4 v[4:5], off
	s_lshr_b32 s5, s5, 26
	v_lshlrev_b32_e32 v4, 6, v2
	s_movk_i32 s6, 0x3c0
	s_add_i32 s5, s4, s5
	v_and_or_b32 v1, v4, s6, v1
	v_lshlrev_b32_e32 v4, 2, v2
	s_ashr_i32 s63, s5, 6
	s_lshl_b32 s5, s34, 13
	v_and_b32_e32 v4, 32, v4
	v_bitop3_b32 v5, v1, s5, v4 bitop3:0xde
	s_lshl_b32 s5, s35, 5
	s_and_b32 s5, s5, 0x60
	s_lshl_b32 s6, s5, 7
	v_bitop3_b32 v1, s6, v1, v4 bitop3:0xf6
	v_bfe_u32 v4, v2, 2, 4
	v_lshl_or_b32 v147, s34, 6, v4
	v_lshlrev_b32_e32 v4, 12, v20
	v_and_b32_e32 v6, 3, v2
	v_and_b32_e32 v2, 60, v2
	v_and_b32_e32 v4, 0xffffe000, v4
	v_lshl_or_b32 v146, v6, 6, v2
	v_lshlrev_b32_e32 v2, 3, v6
	v_lshl_add_u32 v4, v19, 9, v4
	v_and_b32_e32 v6, 1, v20
	v_lshl_or_b32 v4, v6, 6, v4
	s_ashr_i32 s62, s12, 31
	v_lshl_add_u32 v140, v21, 1, v4
	v_lshlrev_b32_e32 v4, 12, v16
	s_cmp_gt_i32 s4, 63
	v_and_b32_e32 v4, 0xffffe000, v4
	s_waitcnt vmcnt(6)
	s_cselect_b64 s[44:45], -1, 0
	s_add_i32 s64, s63, -2
	v_lshl_add_u32 v4, v17, 9, v4
	v_and_b32_e32 v6, 1, v16
	s_cmpk_lt_u32 s7, 0x100
	v_lshl_or_b32 v4, v6, 6, v4
	s_cselect_b64 s[46:47], -1, 0
	v_mov_b32_e32 v141, v3
	v_lshl_add_u32 v142, v18, 1, v4
	v_mov_b32_e32 v143, v3
	s_mov_b32 s65, 0
	v_add_u32_e32 v148, 0, v5
	s_lshl_b32 s48, s5, 1
	v_lshlrev_b32_e32 v2, 1, v2
	s_barrier
	s_branch .LBB0_2782
	.p2align	6

.LBB0_2791:
	s_ashr_i32 s51, s50, 31
	s_lshl_b64 s[6:7], s[50:51], 17
	s_add_u32 s56, s13, s6
	v_mov_b32_e32 v127, 0
	s_addc_u32 s57, s20, s7
	s_andn2_b64 vcc, exec, s[44:45]
	v_mov_b32_e32 v126, v127
	v_mov_b32_e32 v125, v127
	v_mov_b32_e32 v124, v127
	v_mov_b32_e32 v131, v127
	v_mov_b32_e32 v130, v127
	v_mov_b32_e32 v129, v127
	v_mov_b32_e32 v128, v127
	v_mov_b32_e32 v115, v127
	v_mov_b32_e32 v114, v127
	v_mov_b32_e32 v113, v127
	v_mov_b32_e32 v112, v127
	v_mov_b32_e32 v111, v127
	v_mov_b32_e32 v110, v127
	v_mov_b32_e32 v109, v127
	v_mov_b32_e32 v108, v127
	v_mov_b32_e32 v99, v127
	v_mov_b32_e32 v98, v127
	v_mov_b32_e32 v97, v127
	v_mov_b32_e32 v96, v127
	v_mov_b32_e32 v95, v127
	v_mov_b32_e32 v94, v127
	v_mov_b32_e32 v93, v127
	v_mov_b32_e32 v92, v127
	v_mov_b32_e32 v83, v127
	v_mov_b32_e32 v82, v127
	v_mov_b32_e32 v81, v127
	v_mov_b32_e32 v80, v127
	v_mov_b32_e32 v79, v127
	v_mov_b32_e32 v78, v127
	v_mov_b32_e32 v77, v127
	v_mov_b32_e32 v76, v127
	v_mov_b32_e32 v123, v127
	v_mov_b32_e32 v122, v127
	v_mov_b32_e32 v121, v127
	v_mov_b32_e32 v120, v127
	v_mov_b32_e32 v119, v127
	v_mov_b32_e32 v118, v127
	v_mov_b32_e32 v117, v127
	v_mov_b32_e32 v116, v127
	v_mov_b32_e32 v107, v127
	v_mov_b32_e32 v106, v127
	v_mov_b32_e32 v105, v127
	v_mov_b32_e32 v104, v127
	v_mov_b32_e32 v103, v127
	v_mov_b32_e32 v102, v127
	v_mov_b32_e32 v101, v127
	v_mov_b32_e32 v100, v127
	v_mov_b32_e32 v91, v127
	v_mov_b32_e32 v90, v127
	v_mov_b32_e32 v89, v127
	v_mov_b32_e32 v88, v127
	v_mov_b32_e32 v87, v127
	v_mov_b32_e32 v86, v127
	v_mov_b32_e32 v85, v127
	v_mov_b32_e32 v84, v127
	v_mov_b32_e32 v75, v127
	v_mov_b32_e32 v74, v127
	v_mov_b32_e32 v73, v127
	v_mov_b32_e32 v72, v127
	v_mov_b32_e32 v71, v127
	v_mov_b32_e32 v70, v127
	v_mov_b32_e32 v69, v127
	v_mov_b32_e32 v68, v127
	v_mov_b32_e32 v67, v127
	v_mov_b32_e32 v66, v127
	v_mov_b32_e32 v65, v127
	v_mov_b32_e32 v64, v127
	v_mov_b32_e32 v63, v127
	v_mov_b32_e32 v62, v127
	v_mov_b32_e32 v61, v127
	v_mov_b32_e32 v60, v127
	v_mov_b32_e32 v51, v127
	v_mov_b32_e32 v50, v127
	v_mov_b32_e32 v49, v127
	v_mov_b32_e32 v48, v127
	v_mov_b32_e32 v47, v127
	v_mov_b32_e32 v46, v127
	v_mov_b32_e32 v45, v127
	v_mov_b32_e32 v44, v127
	v_mov_b32_e32 v35, v127
	v_mov_b32_e32 v34, v127
	v_mov_b32_e32 v33, v127
	v_mov_b32_e32 v32, v127
	v_mov_b32_e32 v31, v127
	v_mov_b32_e32 v30, v127
	v_mov_b32_e32 v29, v127
	v_mov_b32_e32 v28, v127
	v_mov_b32_e32 v19, v127
	v_mov_b32_e32 v18, v127
	v_mov_b32_e32 v17, v127
	v_mov_b32_e32 v16, v127
	v_mov_b32_e32 v15, v127
	v_mov_b32_e32 v14, v127
	v_mov_b32_e32 v13, v127
	v_mov_b32_e32 v12, v127
	v_mov_b32_e32 v59, v127
	v_mov_b32_e32 v58, v127
	v_mov_b32_e32 v57, v127
	v_mov_b32_e32 v56, v127
	v_mov_b32_e32 v55, v127
	v_mov_b32_e32 v54, v127
	v_mov_b32_e32 v53, v127
	v_mov_b32_e32 v52, v127
	v_mov_b32_e32 v43, v127
	v_mov_b32_e32 v42, v127
	v_mov_b32_e32 v41, v127
	v_mov_b32_e32 v40, v127
	v_mov_b32_e32 v39, v127
	v_mov_b32_e32 v38, v127
	v_mov_b32_e32 v37, v127
	v_mov_b32_e32 v36, v127
	v_mov_b32_e32 v27, v127
	v_mov_b32_e32 v26, v127
	v_mov_b32_e32 v25, v127
	v_mov_b32_e32 v24, v127
	v_mov_b32_e32 v23, v127
	v_mov_b32_e32 v22, v127
	v_mov_b32_e32 v21, v127
	v_mov_b32_e32 v20, v127
	v_mov_b32_e32 v11, v127
	v_mov_b32_e32 v10, v127
	v_mov_b32_e32 v9, v127
	v_mov_b32_e32 v8, v127
	v_mov_b32_e32 v7, v127
	v_mov_b32_e32 v6, v127
	v_mov_b32_e32 v5, v127
	v_mov_b32_e32 v4, v127
	s_cbranch_vccnz .LBB0_2795
	s_and_b64 s[4:5], s[4:5], exec
	s_cselect_b32 s4, s57, s1
	s_cselect_b32 s5, s56, s0
	s_add_u32 s0, s0, 0x10080
	s_addc_u32 s1, s1, 0
	s_add_u32 s6, s2, 0x100
	v_mov_b32_e32 v4, 0
	s_addc_u32 s7, s3, 0
	s_mov_b32 s2, 0
	v_mov_b32_e32 v5, v4
	v_mov_b32_e32 v6, v4
	v_mov_b32_e32 v7, v4
	v_mov_b32_e32 v8, v4
	v_mov_b32_e32 v9, v4
	v_mov_b32_e32 v10, v4
	v_mov_b32_e32 v11, v4
	v_mov_b32_e32 v20, v4
	v_mov_b32_e32 v21, v4
	v_mov_b32_e32 v22, v4
	v_mov_b32_e32 v23, v4
	v_mov_b32_e32 v24, v4
	v_mov_b32_e32 v25, v4
	v_mov_b32_e32 v26, v4
	v_mov_b32_e32 v27, v4
	v_mov_b32_e32 v36, v4
	v_mov_b32_e32 v37, v4
	v_mov_b32_e32 v38, v4
	v_mov_b32_e32 v39, v4
	v_mov_b32_e32 v40, v4
	v_mov_b32_e32 v41, v4
	v_mov_b32_e32 v42, v4
	v_mov_b32_e32 v43, v4
	v_mov_b32_e32 v52, v4
	v_mov_b32_e32 v53, v4
	v_mov_b32_e32 v54, v4
	v_mov_b32_e32 v55, v4
	v_mov_b32_e32 v56, v4
	v_mov_b32_e32 v57, v4
	v_mov_b32_e32 v58, v4
	v_mov_b32_e32 v59, v4
	v_mov_b32_e32 v12, v4
	v_mov_b32_e32 v13, v4
	v_mov_b32_e32 v14, v4
	v_mov_b32_e32 v15, v4
	v_mov_b32_e32 v16, v4
	v_mov_b32_e32 v17, v4
	v_mov_b32_e32 v18, v4
	v_mov_b32_e32 v19, v4
	v_mov_b32_e32 v28, v4
	v_mov_b32_e32 v29, v4
	v_mov_b32_e32 v30, v4
	v_mov_b32_e32 v31, v4
	v_mov_b32_e32 v32, v4
	v_mov_b32_e32 v33, v4
	v_mov_b32_e32 v34, v4
	v_mov_b32_e32 v35, v4
	v_mov_b32_e32 v44, v4
	v_mov_b32_e32 v45, v4
	v_mov_b32_e32 v46, v4
	v_mov_b32_e32 v47, v4
	v_mov_b32_e32 v48, v4
	v_mov_b32_e32 v49, v4
	v_mov_b32_e32 v50, v4
	v_mov_b32_e32 v51, v4
	v_mov_b32_e32 v60, v4
	v_mov_b32_e32 v61, v4
	v_mov_b32_e32 v62, v4
	v_mov_b32_e32 v63, v4
	v_mov_b32_e32 v64, v4
	v_mov_b32_e32 v65, v4
	v_mov_b32_e32 v66, v4
	v_mov_b32_e32 v67, v4
	v_mov_b32_e32 v68, v4
	v_mov_b32_e32 v69, v4
	v_mov_b32_e32 v70, v4
	v_mov_b32_e32 v71, v4
	v_mov_b32_e32 v72, v4
	v_mov_b32_e32 v73, v4
	v_mov_b32_e32 v74, v4
	v_mov_b32_e32 v75, v4
	v_mov_b32_e32 v84, v4
	v_mov_b32_e32 v85, v4
	v_mov_b32_e32 v86, v4
	v_mov_b32_e32 v87, v4
	v_mov_b32_e32 v88, v4
	v_mov_b32_e32 v89, v4
	v_mov_b32_e32 v90, v4
	v_mov_b32_e32 v91, v4
	v_mov_b32_e32 v100, v4
	v_mov_b32_e32 v101, v4
	v_mov_b32_e32 v102, v4
	v_mov_b32_e32 v103, v4
	v_mov_b32_e32 v104, v4
	v_mov_b32_e32 v105, v4
	v_mov_b32_e32 v106, v4
	v_mov_b32_e32 v107, v4
	v_mov_b32_e32 v116, v4
	v_mov_b32_e32 v117, v4
	v_mov_b32_e32 v118, v4
	v_mov_b32_e32 v119, v4
	v_mov_b32_e32 v120, v4
	v_mov_b32_e32 v121, v4
	v_mov_b32_e32 v122, v4
	v_mov_b32_e32 v123, v4
	v_mov_b32_e32 v76, v4
	v_mov_b32_e32 v77, v4
	v_mov_b32_e32 v78, v4
	v_mov_b32_e32 v79, v4
	v_mov_b32_e32 v80, v4
	v_mov_b32_e32 v81, v4
	v_mov_b32_e32 v82, v4
	v_mov_b32_e32 v83, v4
	v_mov_b32_e32 v92, v4
	v_mov_b32_e32 v93, v4
	v_mov_b32_e32 v94, v4
	v_mov_b32_e32 v95, v4
	v_mov_b32_e32 v96, v4
	v_mov_b32_e32 v97, v4
	v_mov_b32_e32 v98, v4
	v_mov_b32_e32 v99, v4
	v_mov_b32_e32 v108, v4
	v_mov_b32_e32 v109, v4
	v_mov_b32_e32 v110, v4
	v_mov_b32_e32 v111, v4
	v_mov_b32_e32 v112, v4
	v_mov_b32_e32 v113, v4
	v_mov_b32_e32 v114, v4
	v_mov_b32_e32 v115, v4
	v_mov_b32_e32 v128, v4
	v_mov_b32_e32 v129, v4
	v_mov_b32_e32 v130, v4
	v_mov_b32_e32 v131, v4
	v_mov_b32_e32 v124, v4
	v_mov_b32_e32 v125, v4
	v_mov_b32_e32 v126, v4
	v_mov_b32_e32 v127, v4
	.p2align	6

.LBB0_2990:
	s_lshr_b32 s1, s1, 26
	s_lshl_b32 s3, s6, 5
	s_add_i32 s1, s0, s1
	s_and_b32 s64, s3, 0x60
	s_ashr_i32 s63, s1, 6
	s_lshl_b32 s1, s7, 6
	s_lshl_b32 s2, s7, 13
	s_lshl_b32 s3, s64, 7
	s_add_u32 s44, s34, 0x3b982080
	s_addc_u32 s45, s35, 0
	s_add_i32 m0, s59, 0x18000
	v_lshl_add_u64 v[4:5], v[4:5], 0, s[24:25]
	v_mov_b32_e32 v135, v3
	s_waitcnt vmcnt(2)
	s_barrier
	global_load_lds_dwordx4 v[4:5], off
	v_lshl_add_u64 v[4:5], v[6:7], 0, s[24:25]
	s_add_i32 m0, s59, 0x1a000
	s_add_i32 s65, s59, 0x8000
	v_mov_b32_e32 v139, v3
	global_load_lds_dwordx4 v[4:5], off
	v_lshl_add_u64 v[4:5], s[44:45], 0, v[134:135]
	s_mov_b32 m0, s65
	s_add_i32 s66, s59, 0xa000
	global_load_lds_dwordx4 v[4:5], off
	v_lshl_add_u64 v[4:5], s[44:45], 0, v[138:139]
	s_mov_b32 m0, s66
	v_and_b32_e32 v2, 48, v145
	global_load_lds_dwordx4 v[4:5], off
	s_add_i32 m0, s59, 0x1c000
	v_lshl_add_u64 v[4:5], v[8:9], 0, s[24:25]
	global_load_lds_dwordx4 v[4:5], off
	v_lshl_add_u64 v[4:5], v[10:11], 0, s[24:25]
	s_add_i32 m0, s59, 0x1e000
	s_movk_i32 s6, 0x3c0
	global_load_lds_dwordx4 v[4:5], off
	v_lshlrev_b32_e32 v4, 6, v145
	s_cmp_gt_i32 s0, 63
	v_and_or_b32 v2, v4, s6, v2
	v_lshlrev_b32_e32 v4, 2, v145
	s_cselect_b64 s[46:47], -1, 0
	s_add_i32 s67, s63, -2
	v_and_b32_e32 v4, 32, v4
	s_cmpk_lt_u32 s5, 0x100
	v_bitop3_b32 v6, v2, s2, v4 bitop3:0xde
	v_bitop3_b32 v135, s3, v2, v4 bitop3:0xf6
	s_cselect_b64 s[48:49], -1, 0
	v_bfe_u32 v2, v145, 2, 4
	s_ashr_i32 s0, s1, 31
	v_and_b32_e32 v4, 3, v145
	v_and_b32_e32 v5, 60, v145
	v_or_b32_e32 v142, s1, v2
	v_mov_b32_e32 v143, s0
	s_waitcnt vmcnt(6)
	v_lshl_or_b32 v139, v4, 6, v5
	v_lshlrev_b32_e32 v144, 3, v4
	v_lshlrev_b64 v[4:5], 9, v[142:143]
	v_lshl_add_u64 v[4:5], s[34:35], 0, v[4:5]
	s_mov_b64 s[0:1], 0xa3309500
	v_lshl_add_u64 v[146:147], v[4:5], 0, s[0:1]
	s_mov_b32 s68, 0
	v_readfirstlane_b32 s69, v0
	v_readfirstlane_b32 s50, v0
	v_mov_b32_e32 v155, s4
	v_add_u32_e32 v143, 0, v6
	s_barrier
	s_branch .LBB0_2993
	.p2align	6

.LBB0_2997:
	v_mov_b32_e32 v127, 0
	s_andn2_b64 vcc, exec, s[46:47]
	v_mov_b32_e32 v126, v127
	v_mov_b32_e32 v125, v127
	v_mov_b32_e32 v124, v127
	v_mov_b32_e32 v123, v127
	v_mov_b32_e32 v122, v127
	v_mov_b32_e32 v121, v127
	v_mov_b32_e32 v120, v127
	v_mov_b32_e32 v115, v127
	v_mov_b32_e32 v114, v127
	v_mov_b32_e32 v113, v127
	v_mov_b32_e32 v112, v127
	v_mov_b32_e32 v107, v127
	v_mov_b32_e32 v106, v127
	v_mov_b32_e32 v105, v127
	v_mov_b32_e32 v104, v127
	v_mov_b32_e32 v99, v127
	v_mov_b32_e32 v98, v127
	v_mov_b32_e32 v97, v127
	v_mov_b32_e32 v96, v127
	v_mov_b32_e32 v91, v127
	v_mov_b32_e32 v90, v127
	v_mov_b32_e32 v89, v127
	v_mov_b32_e32 v88, v127
	v_mov_b32_e32 v83, v127
	v_mov_b32_e32 v82, v127
	v_mov_b32_e32 v81, v127
	v_mov_b32_e32 v80, v127
	v_mov_b32_e32 v75, v127
	v_mov_b32_e32 v74, v127
	v_mov_b32_e32 v73, v127
	v_mov_b32_e32 v72, v127
	v_mov_b32_e32 v131, v127
	v_mov_b32_e32 v130, v127
	v_mov_b32_e32 v129, v127
	v_mov_b32_e32 v128, v127
	v_mov_b32_e32 v119, v127
	v_mov_b32_e32 v118, v127
	v_mov_b32_e32 v117, v127
	v_mov_b32_e32 v116, v127
	v_mov_b32_e32 v111, v127
	v_mov_b32_e32 v110, v127
	v_mov_b32_e32 v109, v127
	v_mov_b32_e32 v108, v127
	v_mov_b32_e32 v103, v127
	v_mov_b32_e32 v102, v127
	v_mov_b32_e32 v101, v127
	v_mov_b32_e32 v100, v127
	v_mov_b32_e32 v95, v127
	v_mov_b32_e32 v94, v127
	v_mov_b32_e32 v93, v127
	v_mov_b32_e32 v92, v127
	v_mov_b32_e32 v87, v127
	v_mov_b32_e32 v86, v127
	v_mov_b32_e32 v85, v127
	v_mov_b32_e32 v84, v127
	v_mov_b32_e32 v79, v127
	v_mov_b32_e32 v78, v127
	v_mov_b32_e32 v77, v127
	v_mov_b32_e32 v76, v127
	v_mov_b32_e32 v71, v127
	v_mov_b32_e32 v70, v127
	v_mov_b32_e32 v69, v127
	v_mov_b32_e32 v68, v127
	v_mov_b32_e32 v67, v127
	v_mov_b32_e32 v66, v127
	v_mov_b32_e32 v65, v127
	v_mov_b32_e32 v64, v127
	v_mov_b32_e32 v59, v127
	v_mov_b32_e32 v58, v127
	v_mov_b32_e32 v57, v127
	v_mov_b32_e32 v56, v127
	v_mov_b32_e32 v51, v127
	v_mov_b32_e32 v50, v127
	v_mov_b32_e32 v49, v127
	v_mov_b32_e32 v48, v127
	v_mov_b32_e32 v43, v127
	v_mov_b32_e32 v42, v127
	v_mov_b32_e32 v41, v127
	v_mov_b32_e32 v40, v127
	v_mov_b32_e32 v35, v127
	v_mov_b32_e32 v34, v127
	v_mov_b32_e32 v33, v127
	v_mov_b32_e32 v32, v127
	v_mov_b32_e32 v27, v127
	v_mov_b32_e32 v26, v127
	v_mov_b32_e32 v25, v127
	v_mov_b32_e32 v24, v127
	v_mov_b32_e32 v19, v127
	v_mov_b32_e32 v18, v127
	v_mov_b32_e32 v17, v127
	v_mov_b32_e32 v16, v127
	v_mov_b32_e32 v11, v127
	v_mov_b32_e32 v10, v127
	v_mov_b32_e32 v9, v127
	v_mov_b32_e32 v8, v127
	v_mov_b32_e32 v63, v127
	v_mov_b32_e32 v62, v127
	v_mov_b32_e32 v61, v127
	v_mov_b32_e32 v60, v127
	v_mov_b32_e32 v55, v127
	v_mov_b32_e32 v54, v127
	v_mov_b32_e32 v53, v127
	v_mov_b32_e32 v52, v127
	v_mov_b32_e32 v47, v127
	v_mov_b32_e32 v46, v127
	v_mov_b32_e32 v45, v127
	v_mov_b32_e32 v44, v127
	v_mov_b32_e32 v39, v127
	v_mov_b32_e32 v38, v127
	v_mov_b32_e32 v37, v127
	v_mov_b32_e32 v36, v127
	v_mov_b32_e32 v31, v127
	v_mov_b32_e32 v30, v127
	v_mov_b32_e32 v29, v127
	v_mov_b32_e32 v28, v127
	v_mov_b32_e32 v23, v127
	v_mov_b32_e32 v22, v127
	v_mov_b32_e32 v21, v127
	v_mov_b32_e32 v20, v127
	v_mov_b32_e32 v15, v127
	v_mov_b32_e32 v14, v127
	v_mov_b32_e32 v13, v127
	v_mov_b32_e32 v12, v127
	s_waitcnt lgkmcnt(0)
	v_mov_b32_e32 v7, v127
	v_mov_b32_e32 v6, v127
	v_mov_b32_e32 v5, v127
	v_mov_b32_e32 v4, v127
	s_cbranch_vccnz .LBB0_3003
	s_ashr_i32 s51, s50, 31
	s_lshl_b64 s[2:3], s[50:51], 10
	s_add_u32 s2, s57, s2
	v_mov_b32_e32 v4, 0
	v_mov_b32_e32 v141, v3
	v_mov_b32_e32 v137, v3
	s_addc_u32 s3, s58, s3
	s_mov_b32 s29, 0
	s_mov_b64 s[4:5], 0x100
	s_mov_b64 s[6:7], s[44:45]
	v_mov_b32_e32 v5, v4
	v_mov_b32_e32 v6, v4
	v_mov_b32_e32 v7, v4
	v_mov_b32_e32 v12, v4
	v_mov_b32_e32 v13, v4
	v_mov_b32_e32 v14, v4
	v_mov_b32_e32 v15, v4
	v_mov_b32_e32 v20, v4
	v_mov_b32_e32 v21, v4
	v_mov_b32_e32 v22, v4
	v_mov_b32_e32 v23, v4
	v_mov_b32_e32 v28, v4
	v_mov_b32_e32 v29, v4
	v_mov_b32_e32 v30, v4
	v_mov_b32_e32 v31, v4
	v_mov_b32_e32 v36, v4
	v_mov_b32_e32 v37, v4
	v_mov_b32_e32 v38, v4
	v_mov_b32_e32 v39, v4
	v_mov_b32_e32 v44, v4
	v_mov_b32_e32 v45, v4
	v_mov_b32_e32 v46, v4
	v_mov_b32_e32 v47, v4
	v_mov_b32_e32 v52, v4
	v_mov_b32_e32 v53, v4
	v_mov_b32_e32 v54, v4
	v_mov_b32_e32 v55, v4
	v_mov_b32_e32 v60, v4
	v_mov_b32_e32 v61, v4
	v_mov_b32_e32 v62, v4
	v_mov_b32_e32 v63, v4
	v_mov_b32_e32 v8, v4
	v_mov_b32_e32 v9, v4
	v_mov_b32_e32 v10, v4
	v_mov_b32_e32 v11, v4
	v_mov_b32_e32 v16, v4
	v_mov_b32_e32 v17, v4
	v_mov_b32_e32 v18, v4
	v_mov_b32_e32 v19, v4
	v_mov_b32_e32 v24, v4
	v_mov_b32_e32 v25, v4
	v_mov_b32_e32 v26, v4
	v_mov_b32_e32 v27, v4
	v_mov_b32_e32 v32, v4
	v_mov_b32_e32 v33, v4
	v_mov_b32_e32 v34, v4
	v_mov_b32_e32 v35, v4
	v_mov_b32_e32 v40, v4
	v_mov_b32_e32 v41, v4
	v_mov_b32_e32 v42, v4
	v_mov_b32_e32 v43, v4
	v_mov_b32_e32 v48, v4
	v_mov_b32_e32 v49, v4
	v_mov_b32_e32 v50, v4
	v_mov_b32_e32 v51, v4
	v_mov_b32_e32 v56, v4
	v_mov_b32_e32 v57, v4
	v_mov_b32_e32 v58, v4
	v_mov_b32_e32 v59, v4
	v_mov_b32_e32 v64, v4
	v_mov_b32_e32 v65, v4
	v_mov_b32_e32 v66, v4
	v_mov_b32_e32 v67, v4
	v_mov_b32_e32 v68, v4
	v_mov_b32_e32 v69, v4
	v_mov_b32_e32 v70, v4
	v_mov_b32_e32 v71, v4
	v_mov_b32_e32 v76, v4
	v_mov_b32_e32 v77, v4
	v_mov_b32_e32 v78, v4
	v_mov_b32_e32 v79, v4
	v_mov_b32_e32 v84, v4
	v_mov_b32_e32 v85, v4
	v_mov_b32_e32 v86, v4
	v_mov_b32_e32 v87, v4
	v_mov_b32_e32 v92, v4
	v_mov_b32_e32 v93, v4
	v_mov_b32_e32 v94, v4
	v_mov_b32_e32 v95, v4
	v_mov_b32_e32 v100, v4
	v_mov_b32_e32 v101, v4
	v_mov_b32_e32 v102, v4
	v_mov_b32_e32 v103, v4
	v_mov_b32_e32 v108, v4
	v_mov_b32_e32 v109, v4
	v_mov_b32_e32 v110, v4
	v_mov_b32_e32 v111, v4
	v_mov_b32_e32 v116, v4
	v_mov_b32_e32 v117, v4
	v_mov_b32_e32 v118, v4
	v_mov_b32_e32 v119, v4
	v_mov_b32_e32 v128, v4
	v_mov_b32_e32 v129, v4
	v_mov_b32_e32 v130, v4
	v_mov_b32_e32 v131, v4
	v_mov_b32_e32 v72, v4
	v_mov_b32_e32 v73, v4
	v_mov_b32_e32 v74, v4
	v_mov_b32_e32 v75, v4
	v_mov_b32_e32 v80, v4
	v_mov_b32_e32 v81, v4
	v_mov_b32_e32 v82, v4
	v_mov_b32_e32 v83, v4
	v_mov_b32_e32 v88, v4
	v_mov_b32_e32 v89, v4
	v_mov_b32_e32 v90, v4
	v_mov_b32_e32 v91, v4
	v_mov_b32_e32 v96, v4
	v_mov_b32_e32 v97, v4
	v_mov_b32_e32 v98, v4
	v_mov_b32_e32 v99, v4
	v_mov_b32_e32 v104, v4
	v_mov_b32_e32 v105, v4
	v_mov_b32_e32 v106, v4
	v_mov_b32_e32 v107, v4
	v_mov_b32_e32 v112, v4
	v_mov_b32_e32 v113, v4
	v_mov_b32_e32 v114, v4
	v_mov_b32_e32 v115, v4
	v_mov_b32_e32 v120, v4
	v_mov_b32_e32 v121, v4
	v_mov_b32_e32 v122, v4
	v_mov_b32_e32 v123, v4
	v_mov_b32_e32 v124, v4
	v_mov_b32_e32 v125, v4
	v_mov_b32_e32 v126, v4
	v_mov_b32_e32 v127, v4
	s_branch .LBB0_3000
	.p2align	6

.LBB0_3094:
	s_add_i32 m0, s31, 0x18000
	v_lshl_add_u64 v[4:5], v[4:5], 0, s[24:25]
	s_waitcnt vmcnt(2)
	s_barrier
	global_load_lds_dwordx4 v[4:5], off
	v_lshl_add_u64 v[4:5], v[6:7], 0, s[24:25]
	s_add_i32 m0, s31, 0x1a000
	s_add_i32 s55, s31, 0x8000
	global_load_lds_dwordx4 v[4:5], off
	v_lshl_add_u64 v[4:5], v[12:13], 0, s[24:25]
	s_mov_b32 m0, s55
	s_add_i32 s56, s31, 0xa000
	global_load_lds_dwordx4 v[4:5], off
	v_lshl_add_u64 v[4:5], v[14:15], 0, s[24:25]
	s_mov_b32 m0, s56
	s_lshr_b32 s7, s7, 26
	global_load_lds_dwordx4 v[4:5], off
	s_add_i32 m0, s31, 0x1c000
	v_lshl_add_u64 v[4:5], v[8:9], 0, s[24:25]
	global_load_lds_dwordx4 v[4:5], off
	v_lshl_add_u64 v[4:5], v[10:11], 0, s[24:25]
	s_add_i32 m0, s31, 0x1e000
	s_lshl_b32 s35, s35, 5
	global_load_lds_dwordx4 v[4:5], off
	v_and_b32_e32 v4, 48, v2
	s_add_i32 s7, s6, s7
	v_lshlrev_b32_e32 v5, 6, v2
	s_movk_i32 s41, 0x3c0
	s_and_b32 s57, s35, 0x60
	s_ashr_i32 s7, s7, 6
	s_lshl_b32 s14, s40, 6
	s_lshl_b32 s40, s40, 13
	v_and_or_b32 v4, v5, s41, v4
	v_lshlrev_b32_e32 v5, 2, v2
	s_lshl_b32 s35, s57, 7
	v_and_b32_e32 v5, 32, v5
	s_cmp_gt_i32 s6, 63
	v_bitop3_b32 v6, v4, s40, v5 bitop3:0xde
	s_cselect_b64 s[40:41], -1, 0
	s_add_i32 s6, s7, -2
	s_cmpk_lt_u32 s34, 0x100
	v_bitop3_b32 v141, s35, v4, v5 bitop3:0xf6
	s_cselect_b64 s[42:43], -1, 0
	v_bfe_u32 v4, v2, 2, 4
	s_ashr_i32 s34, s14, 31
	v_and_b32_e32 v5, 3, v2
	v_and_b32_e32 v2, 60, v2
	v_or_b32_e32 v138, s14, v4
	v_mov_b32_e32 v139, s34
	v_lshl_or_b32 v162, v5, 6, v2
	v_lshlrev_b32_e32 v140, 3, v5
	v_lshlrev_b64 v[4:5], 11, v[138:139]
	v_lshl_add_u64 v[4:5], s[0:1], 0, v[4:5]
	s_mov_b64 s[0:1], 0x7b309500
	v_lshl_add_u64 v[142:143], v[4:5], 0, s[0:1]
	s_mov_b64 s[0:1], 0x7b311500
	v_lshl_add_u64 v[144:145], v[4:5], 0, s[0:1]
	s_mov_b64 s[0:1], 0x7b319500
	v_lshl_add_u64 v[146:147], v[4:5], 0, s[0:1]
	s_mov_b64 s[0:1], 0x7b321500
	v_lshl_add_u64 v[148:149], v[4:5], 0, s[0:1]
	s_mov_b64 s[0:1], 0x7b349500
	v_lshl_add_u64 v[150:151], v[4:5], 0, s[0:1]
	s_mov_b64 s[0:1], 0x7b351500
	v_lshl_add_u64 v[152:153], v[4:5], 0, s[0:1]
	s_mov_b64 s[0:1], 0x7b359500
	v_lshlrev_b32_e32 v2, 12, v16
	v_lshl_add_u64 v[154:155], v[4:5], 0, s[0:1]
	s_mov_b64 s[0:1], 0x7b361500
	v_and_b32_e32 v2, 0xffffe000, v2
	v_lshl_add_u64 v[156:157], v[4:5], 0, s[0:1]
	v_lshl_add_u32 v2, v17, 9, v2
	v_and_b32_e32 v4, 1, v16
	v_lshl_or_b32 v2, v4, 6, v2
	v_lshl_add_u32 v158, v18, 1, v2
	v_lshlrev_b32_e32 v2, 12, v19
	v_and_b32_e32 v2, 0xffffe000, v2
	s_waitcnt vmcnt(6)
	v_lshl_add_u32 v2, v20, 9, v2
	v_and_b32_e32 v4, 1, v19
	v_lshl_or_b32 v2, v4, 6, v2
	v_mov_b32_e32 v159, v3
	v_lshl_add_u32 v160, v21, 1, v2
	v_mov_b32_e32 v161, v3
	s_mov_b32 s58, 0
	v_add_u32_e32 v139, 0, v6
	s_barrier
	s_branch .LBB0_3097
	.p2align	6

.LBB0_3101:
	s_ashr_i32 s45, s44, 31
	s_lshl_b64 s[48:49], s[44:45], 17
	s_add_u32 s48, s13, s48
	s_waitcnt lgkmcnt(0)
	v_mov_b32_e32 v127, 0
	s_addc_u32 s49, s22, s49
	s_andn2_b64 vcc, exec, s[40:41]
	v_mov_b32_e32 v126, v127
	v_mov_b32_e32 v125, v127
	v_mov_b32_e32 v124, v127
	v_mov_b32_e32 v131, v127
	v_mov_b32_e32 v130, v127
	v_mov_b32_e32 v129, v127
	v_mov_b32_e32 v128, v127
	v_mov_b32_e32 v115, v127
	v_mov_b32_e32 v114, v127
	v_mov_b32_e32 v113, v127
	v_mov_b32_e32 v112, v127
	v_mov_b32_e32 v111, v127
	v_mov_b32_e32 v110, v127
	v_mov_b32_e32 v109, v127
	v_mov_b32_e32 v108, v127
	v_mov_b32_e32 v99, v127
	v_mov_b32_e32 v98, v127
	v_mov_b32_e32 v97, v127
	v_mov_b32_e32 v96, v127
	v_mov_b32_e32 v95, v127
	v_mov_b32_e32 v94, v127
	v_mov_b32_e32 v93, v127
	v_mov_b32_e32 v92, v127
	v_mov_b32_e32 v83, v127
	v_mov_b32_e32 v82, v127
	v_mov_b32_e32 v81, v127
	v_mov_b32_e32 v80, v127
	v_mov_b32_e32 v79, v127
	v_mov_b32_e32 v78, v127
	v_mov_b32_e32 v77, v127
	v_mov_b32_e32 v76, v127
	v_mov_b32_e32 v123, v127
	v_mov_b32_e32 v122, v127
	v_mov_b32_e32 v121, v127
	v_mov_b32_e32 v120, v127
	v_mov_b32_e32 v119, v127
	v_mov_b32_e32 v118, v127
	v_mov_b32_e32 v117, v127
	v_mov_b32_e32 v116, v127
	v_mov_b32_e32 v107, v127
	v_mov_b32_e32 v106, v127
	v_mov_b32_e32 v105, v127
	v_mov_b32_e32 v104, v127
	v_mov_b32_e32 v103, v127
	v_mov_b32_e32 v102, v127
	v_mov_b32_e32 v101, v127
	v_mov_b32_e32 v100, v127
	v_mov_b32_e32 v91, v127
	v_mov_b32_e32 v90, v127
	v_mov_b32_e32 v89, v127
	v_mov_b32_e32 v88, v127
	v_mov_b32_e32 v87, v127
	v_mov_b32_e32 v86, v127
	v_mov_b32_e32 v85, v127
	v_mov_b32_e32 v84, v127
	v_mov_b32_e32 v75, v127
	v_mov_b32_e32 v74, v127
	v_mov_b32_e32 v73, v127
	v_mov_b32_e32 v72, v127
	v_mov_b32_e32 v71, v127
	v_mov_b32_e32 v70, v127
	v_mov_b32_e32 v69, v127
	v_mov_b32_e32 v68, v127
	v_mov_b32_e32 v67, v127
	v_mov_b32_e32 v66, v127
	v_mov_b32_e32 v65, v127
	v_mov_b32_e32 v64, v127
	v_mov_b32_e32 v63, v127
	v_mov_b32_e32 v62, v127
	v_mov_b32_e32 v61, v127
	v_mov_b32_e32 v60, v127
	v_mov_b32_e32 v51, v127
	v_mov_b32_e32 v50, v127
	v_mov_b32_e32 v49, v127
	v_mov_b32_e32 v48, v127
	v_mov_b32_e32 v47, v127
	v_mov_b32_e32 v46, v127
	v_mov_b32_e32 v45, v127
	v_mov_b32_e32 v44, v127
	v_mov_b32_e32 v35, v127
	v_mov_b32_e32 v34, v127
	v_mov_b32_e32 v33, v127
	v_mov_b32_e32 v32, v127
	v_mov_b32_e32 v31, v127
	v_mov_b32_e32 v30, v127
	v_mov_b32_e32 v29, v127
	v_mov_b32_e32 v28, v127
	v_mov_b32_e32 v19, v127
	v_mov_b32_e32 v18, v127
	v_mov_b32_e32 v17, v127
	v_mov_b32_e32 v16, v127
	v_mov_b32_e32 v15, v127
	v_mov_b32_e32 v14, v127
	v_mov_b32_e32 v13, v127
	v_mov_b32_e32 v12, v127
	v_mov_b32_e32 v59, v127
	v_mov_b32_e32 v58, v127
	v_mov_b32_e32 v57, v127
	v_mov_b32_e32 v56, v127
	v_mov_b32_e32 v55, v127
	v_mov_b32_e32 v54, v127
	v_mov_b32_e32 v53, v127
	v_mov_b32_e32 v52, v127
	v_mov_b32_e32 v43, v127
	v_mov_b32_e32 v42, v127
	v_mov_b32_e32 v41, v127
	v_mov_b32_e32 v40, v127
	v_mov_b32_e32 v39, v127
	v_mov_b32_e32 v38, v127
	v_mov_b32_e32 v37, v127
	v_mov_b32_e32 v36, v127
	v_mov_b32_e32 v27, v127
	v_mov_b32_e32 v26, v127
	v_mov_b32_e32 v25, v127
	v_mov_b32_e32 v24, v127
	v_mov_b32_e32 v23, v127
	v_mov_b32_e32 v22, v127
	v_mov_b32_e32 v21, v127
	v_mov_b32_e32 v20, v127
	v_mov_b32_e32 v11, v127
	v_mov_b32_e32 v10, v127
	v_mov_b32_e32 v9, v127
	v_mov_b32_e32 v8, v127
	v_mov_b32_e32 v7, v127
	v_mov_b32_e32 v6, v127
	v_mov_b32_e32 v5, v127
	v_mov_b32_e32 v4, v127
	s_cbranch_vccnz .LBB0_3105
	s_and_b64 s[0:1], s[0:1], exec
	s_cselect_b32 s45, s49, s5
	s_cselect_b32 s51, s48, s4
	s_add_u32 s0, s4, 0x10080
	s_addc_u32 s1, s5, 0
	s_add_u32 s4, s2, 0x100
	v_mov_b32_e32 v4, 0
	v_mov_b32_e32 v218, 0x200
	v_mov_b32_e32 v217, 0x100
	v_mov_b32_e32 v219, 0x8000
	v_mov_b32_e32 v203, 1
	v_mov_b32_e32 v200, 0x80
	v_mov_b32_e32 v206, 0xfffffa00
	v_mov_b32_e32 v201, 0xfffff400
	v_mov_b32_e32 v216, 0x3e38aa3b
	v_mov_b32_e32 v202, 0x260
	v_mov_b32_e32 v163, 0x3727c5ac
	s_addc_u32 s5, s3, 0
	s_mov_b32 s2, 0
	v_mov_b32_e32 v5, v4
	v_mov_b32_e32 v6, v4
	v_mov_b32_e32 v7, v4
	v_mov_b32_e32 v8, v4
	v_mov_b32_e32 v9, v4
	v_mov_b32_e32 v10, v4
	v_mov_b32_e32 v11, v4
	v_mov_b32_e32 v20, v4
	v_mov_b32_e32 v21, v4
	v_mov_b32_e32 v22, v4
	v_mov_b32_e32 v23, v4
	v_mov_b32_e32 v24, v4
	v_mov_b32_e32 v25, v4
	v_mov_b32_e32 v26, v4
	v_mov_b32_e32 v27, v4
	v_mov_b32_e32 v36, v4
	v_mov_b32_e32 v37, v4
	v_mov_b32_e32 v38, v4
	v_mov_b32_e32 v39, v4
	v_mov_b32_e32 v40, v4
	v_mov_b32_e32 v41, v4
	v_mov_b32_e32 v42, v4
	v_mov_b32_e32 v43, v4
	v_mov_b32_e32 v52, v4
	v_mov_b32_e32 v53, v4
	v_mov_b32_e32 v54, v4
	v_mov_b32_e32 v55, v4
	v_mov_b32_e32 v56, v4
	v_mov_b32_e32 v57, v4
	v_mov_b32_e32 v58, v4
	v_mov_b32_e32 v59, v4
	v_mov_b32_e32 v12, v4
	v_mov_b32_e32 v13, v4
	v_mov_b32_e32 v14, v4
	v_mov_b32_e32 v15, v4
	v_mov_b32_e32 v16, v4
	v_mov_b32_e32 v17, v4
	v_mov_b32_e32 v18, v4
	v_mov_b32_e32 v19, v4
	v_mov_b32_e32 v28, v4
	v_mov_b32_e32 v29, v4
	v_mov_b32_e32 v30, v4
	v_mov_b32_e32 v31, v4
	v_mov_b32_e32 v32, v4
	v_mov_b32_e32 v33, v4
	v_mov_b32_e32 v34, v4
	v_mov_b32_e32 v35, v4
	v_mov_b32_e32 v44, v4
	v_mov_b32_e32 v45, v4
	v_mov_b32_e32 v46, v4
	v_mov_b32_e32 v47, v4
	v_mov_b32_e32 v48, v4
	v_mov_b32_e32 v49, v4
	v_mov_b32_e32 v50, v4
	v_mov_b32_e32 v51, v4
	v_mov_b32_e32 v60, v4
	v_mov_b32_e32 v61, v4
	v_mov_b32_e32 v62, v4
	v_mov_b32_e32 v63, v4
	v_mov_b32_e32 v64, v4
	v_mov_b32_e32 v65, v4
	v_mov_b32_e32 v66, v4
	v_mov_b32_e32 v67, v4
	v_mov_b32_e32 v68, v4
	v_mov_b32_e32 v69, v4
	v_mov_b32_e32 v70, v4
	v_mov_b32_e32 v71, v4
	v_mov_b32_e32 v72, v4
	v_mov_b32_e32 v73, v4
	v_mov_b32_e32 v74, v4
	v_mov_b32_e32 v75, v4
	v_mov_b32_e32 v84, v4
	v_mov_b32_e32 v85, v4
	v_mov_b32_e32 v86, v4
	v_mov_b32_e32 v87, v4
	v_mov_b32_e32 v88, v4
	v_mov_b32_e32 v89, v4
	v_mov_b32_e32 v90, v4
	v_mov_b32_e32 v91, v4
	v_mov_b32_e32 v100, v4
	v_mov_b32_e32 v101, v4
	v_mov_b32_e32 v102, v4
	v_mov_b32_e32 v103, v4
	v_mov_b32_e32 v104, v4
	v_mov_b32_e32 v105, v4
	v_mov_b32_e32 v106, v4
	v_mov_b32_e32 v107, v4
	v_mov_b32_e32 v116, v4
	v_mov_b32_e32 v117, v4
	v_mov_b32_e32 v118, v4
	v_mov_b32_e32 v119, v4
	v_mov_b32_e32 v120, v4
	v_mov_b32_e32 v121, v4
	v_mov_b32_e32 v122, v4
	v_mov_b32_e32 v123, v4
	v_mov_b32_e32 v76, v4
	v_mov_b32_e32 v77, v4
	v_mov_b32_e32 v78, v4
	v_mov_b32_e32 v79, v4
	v_mov_b32_e32 v80, v4
	v_mov_b32_e32 v81, v4
	v_mov_b32_e32 v82, v4
	v_mov_b32_e32 v83, v4
	v_mov_b32_e32 v92, v4
	v_mov_b32_e32 v93, v4
	v_mov_b32_e32 v94, v4
	v_mov_b32_e32 v95, v4
	v_mov_b32_e32 v96, v4
	v_mov_b32_e32 v97, v4
	v_mov_b32_e32 v98, v4
	v_mov_b32_e32 v99, v4
	v_mov_b32_e32 v108, v4
	v_mov_b32_e32 v109, v4
	v_mov_b32_e32 v110, v4
	v_mov_b32_e32 v111, v4
	v_mov_b32_e32 v112, v4
	v_mov_b32_e32 v113, v4
	v_mov_b32_e32 v114, v4
	v_mov_b32_e32 v115, v4
	v_mov_b32_e32 v128, v4
	v_mov_b32_e32 v129, v4
	v_mov_b32_e32 v130, v4
	v_mov_b32_e32 v131, v4
	v_mov_b32_e32 v124, v4
	v_mov_b32_e32 v125, v4
	v_mov_b32_e32 v126, v4
	v_mov_b32_e32 v127, v4
	.p2align	6
